# GEMM K-loops: DMA first in each load phase, LDS-DMA issue balanced 4-4-4-4 (B half-1 one phase later), per-phase setprio flips removed
# speedup vs baseline: 1.0065x; 1.0065x over previous
; #define GM_STAGE(bufoff, gbase, voff) do { _Pragma("unroll") for (int _i = 0; _i < 2; ++_i) \
;         __builtin_amdgcn_global_load_lds((const unsigned*)((const char*)(gbase) + (voff)[_i]), (LAS unsigned*)(lds + (bufoff) + ldsw + _i * 8192), 16, 0, 0); } while (0)
; #define GM_WAIT_V(n) asm volatile("s_waitcnt vmcnt(" #n ")" ::: "memory")
; #define GM_BAR __builtin_amdgcn_s_barrier()
; #define GM_STA_H0(buf, p, o0) do { if constexpr (GATHER) GM_STAGE(buf, p, o0); else GM_STAGE(buf, p, voffA); } while (0)
; #define GM_STA_H1(buf, p, o1) do { if constexpr (GATHER) GM_STAGE(buf, p, o1); else GM_STAGE(buf, (p) + hstepB, voffA); } while (0)
; template <bool BF, bool GATHER = false, class Epi, class Hook>
; __device__ __forceinline__ void gemm_phase(LAS unsigned char* lds, const Gemm g, const Order& S, const Epi& E, Hook& HK) {
;     ...
;     const size_t hstep = GATHER ? (size_t)0 : (size_t)HALF * K * 2;
;     const size_t hstepB = (size_t)HALF * K * 2;
;     const size_t tstep = 2 * hstepB;
;     const unsigned ldsw = (unsigned)wid * 1024u;
;     const int aoff = lds_byte(wr * 64 + fr, fq * 8), boff = lds_byte(wc * 32 + fr, fq * 8);
;     ...
;     GM_STAGE(GM_SB(0, 0), cB, voffB); GM_STAGE(GM_SB(0, 1), cB + hstepB, voffB); GM_STA_H0(GM_SA(0, 0), cA, gA0); GM_STA_H1(GM_SA(0, 1), cA, gA1);
;     if (wr == 1) GM_BAR;
;     GM_WAIT_V(2); GM_BAR;
;     GM_STAGE(GM_SB(1, 0), cB + kstep, voffB); GM_STA_H0(GM_SA(1, 0), cA + kstep, gA0); GM_STAGE(GM_SB(1, 1), cB + hstepB + kstep, voffB);
;     GM_WAIT_V(6); GM_BAR;
.LBB0_374:
	s_add_u32 s12, s90, 0x1c6000
	s_mov_b64 s[14:15], 0x80
	s_addc_u32 s13, s91, 0
	s_and_b32 s9, s5, 3
	s_add_i32 m0, s27, 0x18000
	v_lshl_add_u64 v[8:9], v[8:9], 0, s[14:15]
	s_lshl_b32 s40, s6, 6
	s_lshl_b32 s5, s6, 13
	s_lshl_b32 s16, s9, 12
	s_ashr_i32 s41, s92, 31
	s_waitcnt vmcnt(2)
	s_barrier
	global_load_lds_dwordx4 v[8:9], off
	v_lshl_add_u64 v[6:7], v[6:7], 0, s[14:15]
	s_add_i32 m0, s27, 0x1a000
	s_add_i32 s42, s27, 0x8000
	s_add_i32 s43, s27, 0xa000
	global_load_lds_dwordx4 v[6:7], off
	v_lshl_add_u64 v[2:3], v[2:3], 0, s[14:15]
	s_mov_b32 m0, s42
	s_add_u32 s6, s28, 0x40080
	global_load_lds_dwordx4 v[2:3], off
	v_lshl_add_u64 v[2:3], v[4:5], 0, s[14:15]
	s_mov_b32 m0, s43
	s_addc_u32 s7, s29, 0
	global_load_lds_dwordx4 v[2:3], off
	v_and_b32_e32 v1, 15, v10
	v_lshrrev_b32_e32 v2, 1, v10
	v_and_b32_e32 v152, 24, v2
	v_lshlrev_b32_e32 v2, 1, v152
	v_lshlrev_b32_e32 v3, 2, v10
	v_lshl_or_b32 v2, v1, 6, v2
	v_and_b32_e32 v3, 32, v3
	v_bitop3_b32 v4, v2, s5, v3 bitop3:0xde
	v_bitop3_b32 v153, v2, s16, v3 bitop3:0xde
	v_lshlrev_b32_e32 v2, 14, v11
	v_and_b32_e32 v2, 0xffff8000, v2
	v_lshl_add_u32 v2, v12, 11, v2
	v_and_b32_e32 v3, 1, v11
	v_lshl_or_b32 v2, v3, 6, v2
	v_lshl_add_u32 v138, v13, 1, v2
	v_lshlrev_b32_e32 v2, 14, v14
	s_cmpk_lt_u32 s4, 0x100
	v_and_b32_e32 v2, 0xffff8000, v2
	s_waitcnt vmcnt(4)
	s_cselect_b64 s[16:17], -1, 0
	s_bitcmp0_b32 s4, 6
	v_lshl_add_u32 v2, v15, 11, v2
	v_and_b32_e32 v3, 1, v14
	s_cselect_b64 s[4:5], -1, 0
	v_lshl_or_b32 v2, v3, 6, v2
	s_add_i32 s45, 0, 0x10000
	s_add_i32 s46, 0, 0x14000
	v_or_b32_e32 v154, 16, v1
	v_or_b32_e32 v155, 32, v1
	v_or_b32_e32 v156, 48, v1
	s_ashr_i32 s44, s96, 31
	v_lshl_or_b32 v157, s9, 5, v152
	v_mov_b32_e32 v139, v133
	v_lshl_add_u32 v140, v16, 1, v2
	v_mov_b32_e32 v141, v133
	v_mov_b64_e32 v[142:143], 0x6c0
	v_mov_b64_e32 v[144:145], 0x6bf
	v_add_u32_e32 v158, s45, v153
	v_add_u32_e32 v159, s46, v153
	v_add_u32_e32 v160, 0, v4
	s_movk_i32 s47, 0x1800
	v_mov_b32_e32 v161, 0x3e38aa3b
	s_barrier
	s_branch .LBB0_377

; #define GM_STAGE(bufoff, gbase, voff) do { _Pragma("unroll") for (int _i = 0; _i < 2; ++_i) \
;         __builtin_amdgcn_global_load_lds((const unsigned*)((const char*)(gbase) + (voff)[_i]), (LAS unsigned*)(lds + (bufoff) + ldsw + _i * 8192), 16, 0, 0); } while (0)
; #define GM_LDA(dst, b, h) do { _Pragma("unroll") for (int m = 0; m < 4; ++m) _Pragma("unroll") for (int k = 0; k < 2; ++k) dst[m][k] = *(const LAS s16x8*)(lds + GM_SA(b, h) + aoff + m * 2048 + k * 1024); } while (0)
; #define GM_LDB(dst, b, h) do { _Pragma("unroll") for (int n = 0; n < 2; ++n) _Pragma("unroll") for (int k = 0; k < 2; ++k) dst[n][k] = *(const LAS s16x8*)(lds + GM_SB(b, h) + boff + n * 2048 + k * 1024); } while (0)
; #define GM_MMA(ai, bj, At, Bt) do { __builtin_amdgcn_s_setprio(1); _Pragma("unroll") for (int m = 0; m < 4; ++m) _Pragma("unroll") for (int n = 0; n < 2; ++n) _Pragma("unroll") for (int k = 0; k < 2; ++k) \
;         acc[ai][bj][m][n] = mma16<BF>(Bt[n][k], At[m][k], acc[ai][bj][m][n]); __builtin_amdgcn_s_setprio(0); } while (0)
; #define GM_WAIT_V(n) asm volatile("s_waitcnt vmcnt(" #n ")" ::: "memory")
; #define GM_WAIT_L(n) asm volatile("s_waitcnt lgkmcnt(" #n ")" ::: "memory")
; #define GM_BAR __builtin_amdgcn_s_barrier()
; #define GM_SCHED __builtin_amdgcn_sched_barrier(0)
; #define GM_STA_H0(buf, p, o0) do { if constexpr (GATHER) GM_STAGE(buf, p, o0); else GM_STAGE(buf, p, voffA); } while (0)
; #define GM_STA_H1(buf, p, o1) do { if constexpr (GATHER) GM_STAGE(buf, p, o1); else GM_STAGE(buf, (p) + hstepB, voffA); } while (0)
; template <bool BF, bool GATHER = false, class Epi, class Hook>
; __device__ __forceinline__ void gemm_phase(LAS unsigned char* lds, const Gemm g, const Order& S, const Epi& E, Hook& HK) {
;     ...
;             GM_LDB(B0, 0, 0); GM_LDB(B1, 0, 1); GM_SCHED; GM_LDA(At, 0, 0); GM_STA_H1(GM_SA(1, 1), a1, gA1);
;             GM_WAIT_V(8); GM_WAIT_L(0); GM_BAR; GM_MMA(0, 0, At, B0); GM_MMA(0, 1, At, B1); GM_BAR; GM_SCHED;
;             GM_LDA(At, 0, 1); GM_STAGE(GM_SB(0, 0), b2, voffB); GM_STAGE(GM_SB(0, 1), b2 + hstepB, voffB); GM_STA_H0(GM_SA(0, 0), a2, s0);
;             GM_WAIT_V(8); GM_WAIT_L(0); GM_BAR; GM_MMA(1, 0, At, B0); GM_MMA(1, 1, At, B1); GM_BAR; GM_SCHED;
.LBB0_380:
	s_add_u32 s28, s2, 0xfffc0080
	s_addc_u32 s29, s3, -1
	s_cmp_eq_u32 s51, 12
	s_cselect_b32 s31, s9, s29
	s_cselect_b32 s30, s19, s28
	s_cselect_b32 s29, s21, s50
	s_cselect_b32 s28, s48, s49
	s_add_u32 s98, s49, 0x3ff80
	s_addc_u32 s99, s50, 0
	v_lshl_add_u64 v[252:253], s[98:99], 0, v[132:133]
	s_add_i32 m0, s35, 0x1c000
	s_nop 0
	global_load_lds_dwordx4 v[252:253], off
	v_lshl_add_u64 v[252:253], s[98:99], 0, v[136:137]
	s_add_i32 m0, s35, 0x1e000
	s_nop 0
	global_load_lds_dwordx4 v[252:253], off
	v_lshl_add_u64 v[150:151], s[2:3], 0, v[138:139]
	s_add_i32 m0, s27, 0xc000
	global_load_lds_dwordx4 v[150:151], off
	v_lshl_add_u64 v[150:151], s[2:3], 0, v[140:141]
	s_add_i32 m0, s27, 0xe000
	s_nop 0
	global_load_lds_dwordx4 v[150:151], off
	ds_read_b128 v[146:149], v158
	ds_read_b128 v[162:165], v158 offset:1024
	ds_read_b128 v[166:169], v158 offset:2048
	ds_read_b128 v[170:173], v158 offset:3072
	ds_read_b128 v[174:177], v159
	ds_read_b128 v[178:181], v159 offset:1024
	ds_read_b128 v[182:185], v159 offset:2048
	ds_read_b128 v[186:189], v159 offset:3072
	ds_read_b128 v[190:193], v160
	ds_read_b128 v[194:197], v160 offset:1024
	ds_read_b128 v[198:201], v160 offset:2048
	ds_read_b128 v[202:205], v160 offset:3072
	ds_read_b128 v[206:209], v160 offset:4096
	ds_read_b128 v[210:213], v160 offset:5120
	ds_read_b128 v[214:217], v160 offset:6144
	ds_read_b128 v[218:221], v160 offset:7168
	s_waitcnt vmcnt(8)
	s_waitcnt lgkmcnt(0)
	s_barrier
	s_waitcnt lgkmcnt(0)
	v_mfma_f32_16x16x32_f16 v[126:129], v[146:149], v[190:193], v[126:129]
	v_mfma_f32_16x16x32_f16 v[122:125], v[166:169], v[190:193], v[122:125]
	v_mfma_f32_16x16x32_f16 v[110:113], v[146:149], v[198:201], v[110:113]
	v_mfma_f32_16x16x32_f16 v[106:109], v[166:169], v[198:201], v[106:109]
	v_mfma_f32_16x16x32_f16 v[94:97], v[146:149], v[206:209], v[94:97]
	v_mfma_f32_16x16x32_f16 v[90:93], v[166:169], v[206:209], v[90:93]
	v_mfma_f32_16x16x32_f16 v[78:81], v[146:149], v[214:217], v[78:81]
	v_mfma_f32_16x16x32_f16 v[74:77], v[166:169], v[214:217], v[74:77]
	v_mfma_f32_16x16x32_f16 v[126:129], v[162:165], v[194:197], v[126:129]
	v_mfma_f32_16x16x32_f16 v[122:125], v[170:173], v[194:197], v[122:125]
	v_mfma_f32_16x16x32_f16 v[110:113], v[162:165], v[202:205], v[110:113]
	v_mfma_f32_16x16x32_f16 v[106:109], v[170:173], v[202:205], v[106:109]
	v_mfma_f32_16x16x32_f16 v[94:97], v[162:165], v[210:213], v[94:97]
	v_mfma_f32_16x16x32_f16 v[90:93], v[170:173], v[210:213], v[90:93]
	v_mfma_f32_16x16x32_f16 v[78:81], v[162:165], v[218:221], v[78:81]
	v_mfma_f32_16x16x32_f16 v[74:77], v[170:173], v[218:221], v[74:77]
	v_mfma_f32_16x16x32_f16 v[118:121], v[174:177], v[190:193], v[118:121]
	v_mfma_f32_16x16x32_f16 v[114:117], v[182:185], v[190:193], v[114:117]
	v_mfma_f32_16x16x32_f16 v[102:105], v[174:177], v[198:201], v[102:105]
	v_mfma_f32_16x16x32_f16 v[98:101], v[182:185], v[198:201], v[98:101]
	v_mfma_f32_16x16x32_f16 v[86:89], v[174:177], v[206:209], v[86:89]
	v_mfma_f32_16x16x32_f16 v[82:85], v[182:185], v[206:209], v[82:85]
	v_mfma_f32_16x16x32_f16 v[70:73], v[174:177], v[214:217], v[70:73]
	v_mfma_f32_16x16x32_f16 v[66:69], v[182:185], v[214:217], v[66:69]
	v_mfma_f32_16x16x32_f16 v[118:121], v[178:181], v[194:197], v[118:121]
	v_mfma_f32_16x16x32_f16 v[114:117], v[186:189], v[194:197], v[114:117]
	v_mfma_f32_16x16x32_f16 v[102:105], v[178:181], v[202:205], v[102:105]
	v_mfma_f32_16x16x32_f16 v[98:101], v[186:189], v[202:205], v[98:101]
	v_mfma_f32_16x16x32_f16 v[86:89], v[178:181], v[210:213], v[86:89]
	v_mfma_f32_16x16x32_f16 v[82:85], v[186:189], v[210:213], v[82:85]
	v_mfma_f32_16x16x32_f16 v[70:73], v[178:181], v[218:221], v[70:73]
	v_mfma_f32_16x16x32_f16 v[66:69], v[186:189], v[218:221], v[66:69]
	s_barrier
	s_add_i32 s52, s45, s35
	v_lshl_add_u64 v[150:151], s[28:29], 0, v[132:133]
	s_mov_b32 m0, s52
	global_load_lds_dwordx4 v[150:151], off
	s_add_i32 m0, s52, 0x2000
	s_add_u32 s52, s28, 0x40000
	v_lshl_add_u64 v[222:223], s[28:29], 0, v[136:137]
	s_addc_u32 s53, s29, 0
	s_add_i32 s54, s46, s35
	global_load_lds_dwordx4 v[222:223], off
	v_lshl_add_u64 v[226:227], s[30:31], 0, v[134:135]
	v_lshl_add_u64 v[224:225], s[30:31], 0, v[130:131]
	s_mov_b32 m0, s27
	s_nop 0
	global_load_lds_dwordx4 v[224:225], off
	s_mov_b32 m0, s36
	s_nop 0
	global_load_lds_dwordx4 v[226:227], off
	ds_read_b128 v[190:193], v160 offset:16384
	ds_read_b128 v[194:197], v160 offset:17408
	ds_read_b128 v[198:201], v160 offset:18432
	ds_read_b128 v[202:205], v160 offset:19456
	ds_read_b128 v[206:209], v160 offset:20480
	ds_read_b128 v[210:213], v160 offset:21504
	ds_read_b128 v[214:217], v160 offset:22528
	ds_read_b128 v[218:221], v160 offset:23552
	s_waitcnt vmcnt(6)
	s_waitcnt lgkmcnt(0)
	s_barrier
; #define GM_STAGE(bufoff, gbase, voff) do { _Pragma("unroll") for (int _i = 0; _i < 2; ++_i) \
;         __builtin_amdgcn_global_load_lds((const unsigned*)((const char*)(gbase) + (voff)[_i]), (LAS unsigned*)(lds + (bufoff) + ldsw + _i * 8192), 16, 0, 0); } while (0)
; #define GM_LDA(dst, b, h) do { _Pragma("unroll") for (int m = 0; m < 4; ++m) _Pragma("unroll") for (int k = 0; k < 2; ++k) dst[m][k] = *(const LAS s16x8*)(lds + GM_SA(b, h) + aoff + m * 2048 + k * 1024); } while (0)
; #define GM_LDB(dst, b, h) do { _Pragma("unroll") for (int n = 0; n < 2; ++n) _Pragma("unroll") for (int k = 0; k < 2; ++k) dst[n][k] = *(const LAS s16x8*)(lds + GM_SB(b, h) + boff + n * 2048 + k * 1024); } while (0)
; #define GM_MMA(ai, bj, At, Bt) do { __builtin_amdgcn_s_setprio(1); _Pragma("unroll") for (int m = 0; m < 4; ++m) _Pragma("unroll") for (int n = 0; n < 2; ++n) _Pragma("unroll") for (int k = 0; k < 2; ++k) \
;         acc[ai][bj][m][n] = mma16<BF>(Bt[n][k], At[m][k], acc[ai][bj][m][n]); __builtin_amdgcn_s_setprio(0); } while (0)
; #define GM_WAIT_V(n) asm volatile("s_waitcnt vmcnt(" #n ")" ::: "memory")
; #define GM_WAIT_L(n) asm volatile("s_waitcnt lgkmcnt(" #n ")" ::: "memory")
; #define GM_BAR __builtin_amdgcn_s_barrier()
; #define GM_SCHED __builtin_amdgcn_sched_barrier(0)
; #define GM_STA_H0(buf, p, o0) do { if constexpr (GATHER) GM_STAGE(buf, p, o0); else GM_STAGE(buf, p, voffA); } while (0)
; #define GM_STA_H1(buf, p, o1) do { if constexpr (GATHER) GM_STAGE(buf, p, o1); else GM_STAGE(buf, (p) + hstepB, voffA); } while (0)
; template <bool BF, bool GATHER = false, class Epi, class Hook>
; __device__ __forceinline__ void gemm_phase(LAS unsigned char* lds, const Gemm g, const Order& S, const Epi& E, Hook& HK) {
;     ...
;             GM_WAIT_V(8); GM_WAIT_L(0); GM_BAR; GM_MMA(1, 0, At, B0); GM_MMA(1, 1, At, B1); GM_BAR; GM_SCHED;
;             GM_LDB(B0, 1, 0); GM_LDB(B1, 1, 1); GM_SCHED; GM_LDA(At, 1, 0); GM_STA_H1(GM_SA(0, 1), a2, s1);
;             GM_WAIT_V(8); GM_WAIT_L(0); GM_BAR; GM_MMA(0, 0, At, B0); GM_MMA(0, 1, At, B1); GM_BAR; GM_SCHED;
;             GM_LDA(At, 1, 1); GM_STAGE(GM_SB(1, 0), b3, voffB); GM_STAGE(GM_SB(1, 1), b3 + hstepB, voffB); GM_STA_H0(GM_SA(1, 0), a3, s0);
	s_waitcnt lgkmcnt(0)
	v_mfma_f32_16x16x32_f16 v[62:65], v[146:149], v[190:193], v[62:65]
	v_mfma_f32_16x16x32_f16 v[58:61], v[166:169], v[190:193], v[58:61]
	v_mfma_f32_16x16x32_f16 v[46:49], v[146:149], v[198:201], v[46:49]
	v_mfma_f32_16x16x32_f16 v[42:45], v[166:169], v[198:201], v[42:45]
	v_mfma_f32_16x16x32_f16 v[30:33], v[146:149], v[206:209], v[30:33]
	v_mfma_f32_16x16x32_f16 v[26:29], v[166:169], v[206:209], v[26:29]
	v_mfma_f32_16x16x32_f16 v[14:17], v[146:149], v[214:217], v[14:17]
	v_mfma_f32_16x16x32_f16 v[10:13], v[166:169], v[214:217], v[10:13]
	v_mfma_f32_16x16x32_f16 v[62:65], v[162:165], v[194:197], v[62:65]
	v_mfma_f32_16x16x32_f16 v[58:61], v[170:173], v[194:197], v[58:61]
	v_mfma_f32_16x16x32_f16 v[46:49], v[162:165], v[202:205], v[46:49]
	v_mfma_f32_16x16x32_f16 v[42:45], v[170:173], v[202:205], v[42:45]
	v_mfma_f32_16x16x32_f16 v[30:33], v[162:165], v[210:213], v[30:33]
	v_mfma_f32_16x16x32_f16 v[26:29], v[170:173], v[210:213], v[26:29]
	v_mfma_f32_16x16x32_f16 v[14:17], v[162:165], v[218:221], v[14:17]
	v_mfma_f32_16x16x32_f16 v[10:13], v[170:173], v[218:221], v[10:13]
	v_mfma_f32_16x16x32_f16 v[54:57], v[174:177], v[190:193], v[54:57]
	v_mfma_f32_16x16x32_f16 v[50:53], v[182:185], v[190:193], v[50:53]
	v_mfma_f32_16x16x32_f16 v[38:41], v[174:177], v[198:201], v[38:41]
	v_mfma_f32_16x16x32_f16 v[34:37], v[182:185], v[198:201], v[34:37]
	v_mfma_f32_16x16x32_f16 v[22:25], v[174:177], v[206:209], v[22:25]
	v_mfma_f32_16x16x32_f16 v[18:21], v[182:185], v[206:209], v[18:21]
	v_mfma_f32_16x16x32_f16 v[6:9], v[174:177], v[214:217], v[6:9]
	v_mfma_f32_16x16x32_f16 v[2:5], v[182:185], v[214:217], v[2:5]
	v_mfma_f32_16x16x32_f16 v[54:57], v[178:181], v[194:197], v[54:57]
	v_mfma_f32_16x16x32_f16 v[50:53], v[186:189], v[194:197], v[50:53]
	v_mfma_f32_16x16x32_f16 v[38:41], v[178:181], v[202:205], v[38:41]
	v_mfma_f32_16x16x32_f16 v[34:37], v[186:189], v[202:205], v[34:37]
	v_mfma_f32_16x16x32_f16 v[22:25], v[178:181], v[210:213], v[22:25]
	v_mfma_f32_16x16x32_f16 v[18:21], v[186:189], v[210:213], v[18:21]
	v_mfma_f32_16x16x32_f16 v[6:9], v[178:181], v[218:221], v[6:9]
	v_mfma_f32_16x16x32_f16 v[2:5], v[186:189], v[218:221], v[2:5]
	s_barrier
	s_add_u32 s30, s30, 0x40000
	s_addc_u32 s31, s31, 0
	s_add_u32 s98, s28, 0x40000
	s_addc_u32 s99, s29, 0
	v_lshl_add_u64 v[252:253], s[98:99], 0, v[132:133]
	s_add_i32 m0, s35, 0x14000
	s_nop 0
	global_load_lds_dwordx4 v[252:253], off
	v_lshl_add_u64 v[252:253], s[98:99], 0, v[136:137]
	s_add_i32 m0, s35, 0x16000
	s_nop 0
	global_load_lds_dwordx4 v[252:253], off
	s_mov_b32 m0, s37
	v_lshl_add_u64 v[228:229], s[30:31], 0, v[130:131]
	global_load_lds_dwordx4 v[228:229], off
	v_lshl_add_u64 v[228:229], s[30:31], 0, v[134:135]
	s_mov_b32 m0, s38
	s_nop 0
	global_load_lds_dwordx4 v[228:229], off
	s_mov_b32 s53, 0x1c000
	s_mov_b32 s52, 0x18000
	v_add_u32_e32 v244, s52, v153
	v_add_u32_e32 v245, s53, v153
	ds_read_b128 v[146:149], v244
	ds_read_b128 v[162:165], v244 offset:1024
	ds_read_b128 v[166:169], v244 offset:2048
	ds_read_b128 v[170:173], v244 offset:3072
	ds_read_b128 v[174:177], v245
	ds_read_b128 v[178:181], v245 offset:1024
	ds_read_b128 v[182:185], v245 offset:2048
	ds_read_b128 v[186:189], v245 offset:3072
	ds_read_b128 v[190:193], v160 offset:32768
	ds_read_b128 v[194:197], v160 offset:33792
	ds_read_b128 v[198:201], v160 offset:34816
	ds_read_b128 v[202:205], v160 offset:35840
	ds_read_b128 v[206:209], v160 offset:36864
	ds_read_b128 v[210:213], v160 offset:37888
	ds_read_b128 v[214:217], v160 offset:38912
	ds_read_b128 v[218:221], v160 offset:39936
	s_waitcnt vmcnt(8)
	s_waitcnt lgkmcnt(0)
	s_barrier
; #define GM_STAGE(bufoff, gbase, voff) do { _Pragma("unroll") for (int _i = 0; _i < 2; ++_i) \
;         __builtin_amdgcn_global_load_lds((const unsigned*)((const char*)(gbase) + (voff)[_i]), (LAS unsigned*)(lds + (bufoff) + ldsw + _i * 8192), 16, 0, 0); } while (0)
; #define GM_LDA(dst, b, h) do { _Pragma("unroll") for (int m = 0; m < 4; ++m) _Pragma("unroll") for (int k = 0; k < 2; ++k) dst[m][k] = *(const LAS s16x8*)(lds + GM_SA(b, h) + aoff + m * 2048 + k * 1024); } while (0)
; #define GM_MMA(ai, bj, At, Bt) do { __builtin_amdgcn_s_setprio(1); _Pragma("unroll") for (int m = 0; m < 4; ++m) _Pragma("unroll") for (int n = 0; n < 2; ++n) _Pragma("unroll") for (int k = 0; k < 2; ++k) \
;         acc[ai][bj][m][n] = mma16<BF>(Bt[n][k], At[m][k], acc[ai][bj][m][n]); __builtin_amdgcn_s_setprio(0); } while (0)
; #define GM_WAIT_V(n) asm volatile("s_waitcnt vmcnt(" #n ")" ::: "memory")
; #define GM_WAIT_L(n) asm volatile("s_waitcnt lgkmcnt(" #n ")" ::: "memory")
; #define GM_BAR __builtin_amdgcn_s_barrier()
; #define GM_SCHED __builtin_amdgcn_sched_barrier(0)
; #define GM_STA_H0(buf, p, o0) do { if constexpr (GATHER) GM_STAGE(buf, p, o0); else GM_STAGE(buf, p, voffA); } while (0)
; template <bool BF, bool GATHER = false, class Epi, class Hook>
; __device__ __forceinline__ void gemm_phase(LAS unsigned char* lds, const Gemm g, const Order& S, const Epi& E, Hook& HK) {
;     ...
;             GM_WAIT_V(8); GM_WAIT_L(0); GM_BAR; GM_MMA(0, 0, At, B0); GM_MMA(0, 1, At, B1); GM_BAR; GM_SCHED;
;             GM_LDA(At, 1, 1); GM_STAGE(GM_SB(1, 0), b3, voffB); GM_STAGE(GM_SB(1, 1), b3 + hstepB, voffB); GM_STA_H0(GM_SA(1, 0), a3, s0);
;             GM_WAIT_V(8); GM_WAIT_L(0); GM_BAR; GM_MMA(1, 0, At, B0); GM_MMA(1, 1, At, B1); GM_BAR; GM_SCHED;
;         }
	s_waitcnt lgkmcnt(0)
	v_mfma_f32_16x16x32_f16 v[126:129], v[146:149], v[190:193], v[126:129]
	v_mfma_f32_16x16x32_f16 v[122:125], v[166:169], v[190:193], v[122:125]
	v_mfma_f32_16x16x32_f16 v[110:113], v[146:149], v[198:201], v[110:113]
	v_mfma_f32_16x16x32_f16 v[106:109], v[166:169], v[198:201], v[106:109]
	v_mfma_f32_16x16x32_f16 v[94:97], v[146:149], v[206:209], v[94:97]
	v_mfma_f32_16x16x32_f16 v[90:93], v[166:169], v[206:209], v[90:93]
	v_mfma_f32_16x16x32_f16 v[78:81], v[146:149], v[214:217], v[78:81]
	v_mfma_f32_16x16x32_f16 v[74:77], v[166:169], v[214:217], v[74:77]
	v_mfma_f32_16x16x32_f16 v[126:129], v[162:165], v[194:197], v[126:129]
	v_mfma_f32_16x16x32_f16 v[122:125], v[170:173], v[194:197], v[122:125]
	v_mfma_f32_16x16x32_f16 v[110:113], v[162:165], v[202:205], v[110:113]
	v_mfma_f32_16x16x32_f16 v[106:109], v[170:173], v[202:205], v[106:109]
	v_mfma_f32_16x16x32_f16 v[94:97], v[162:165], v[210:213], v[94:97]
	v_mfma_f32_16x16x32_f16 v[90:93], v[170:173], v[210:213], v[90:93]
	v_mfma_f32_16x16x32_f16 v[78:81], v[162:165], v[218:221], v[78:81]
	v_mfma_f32_16x16x32_f16 v[74:77], v[170:173], v[218:221], v[74:77]
	v_mfma_f32_16x16x32_f16 v[118:121], v[174:177], v[190:193], v[118:121]
	v_mfma_f32_16x16x32_f16 v[114:117], v[182:185], v[190:193], v[114:117]
	v_mfma_f32_16x16x32_f16 v[102:105], v[174:177], v[198:201], v[102:105]
	v_mfma_f32_16x16x32_f16 v[98:101], v[182:185], v[198:201], v[98:101]
	v_mfma_f32_16x16x32_f16 v[86:89], v[174:177], v[206:209], v[86:89]
	v_mfma_f32_16x16x32_f16 v[82:85], v[182:185], v[206:209], v[82:85]
	v_mfma_f32_16x16x32_f16 v[70:73], v[174:177], v[214:217], v[70:73]
	v_mfma_f32_16x16x32_f16 v[66:69], v[182:185], v[214:217], v[66:69]
	v_mfma_f32_16x16x32_f16 v[118:121], v[178:181], v[194:197], v[118:121]
	v_mfma_f32_16x16x32_f16 v[114:117], v[186:189], v[194:197], v[114:117]
	v_mfma_f32_16x16x32_f16 v[102:105], v[178:181], v[202:205], v[102:105]
	v_mfma_f32_16x16x32_f16 v[98:101], v[186:189], v[202:205], v[98:101]
	v_mfma_f32_16x16x32_f16 v[86:89], v[178:181], v[210:213], v[86:89]
	v_mfma_f32_16x16x32_f16 v[82:85], v[186:189], v[210:213], v[82:85]
	v_mfma_f32_16x16x32_f16 v[70:73], v[178:181], v[218:221], v[70:73]
	v_mfma_f32_16x16x32_f16 v[66:69], v[186:189], v[218:221], v[66:69]
	s_barrier
	s_add_i32 s30, s52, s35
	v_lshl_add_u64 v[150:151], v[150:151], 0, s[14:15]
	s_mov_b32 m0, s30
	global_load_lds_dwordx4 v[150:151], off
	s_add_i32 m0, s30, 0x2000
	s_add_u32 s28, s28, 0x40080
	v_lshl_add_u64 v[150:151], v[222:223], 0, s[14:15]
	s_addc_u32 s29, s29, 0
	s_add_i32 s30, s53, s35
	global_load_lds_dwordx4 v[150:151], off
	v_lshl_add_u64 v[150:151], v[224:225], 0, s[14:15]
	s_mov_b32 m0, s42
	s_nop 0
	global_load_lds_dwordx4 v[150:151], off
	v_lshl_add_u64 v[150:151], v[226:227], 0, s[14:15]
	s_mov_b32 m0, s43
	s_nop 0
	global_load_lds_dwordx4 v[150:151], off
	ds_read_b128 v[190:193], v160 offset:49152
	ds_read_b128 v[194:197], v160 offset:50176
	ds_read_b128 v[198:201], v160 offset:51200
	ds_read_b128 v[202:205], v160 offset:52224
	ds_read_b128 v[206:209], v160 offset:53248
	ds_read_b128 v[210:213], v160 offset:54272
	ds_read_b128 v[214:217], v160 offset:55296
	ds_read_b128 v[218:221], v160 offset:56320
	s_waitcnt vmcnt(6)
	s_waitcnt lgkmcnt(0)
	s_barrier
	s_waitcnt lgkmcnt(0)
	v_mfma_f32_16x16x32_f16 v[62:65], v[146:149], v[190:193], v[62:65]
	v_mfma_f32_16x16x32_f16 v[58:61], v[166:169], v[190:193], v[58:61]
	v_mfma_f32_16x16x32_f16 v[46:49], v[146:149], v[198:201], v[46:49]
	v_mfma_f32_16x16x32_f16 v[42:45], v[166:169], v[198:201], v[42:45]
	v_mfma_f32_16x16x32_f16 v[30:33], v[146:149], v[206:209], v[30:33]
	v_mfma_f32_16x16x32_f16 v[26:29], v[166:169], v[206:209], v[26:29]
	v_mfma_f32_16x16x32_f16 v[14:17], v[146:149], v[214:217], v[14:17]
	v_mfma_f32_16x16x32_f16 v[10:13], v[166:169], v[214:217], v[10:13]
	v_mfma_f32_16x16x32_f16 v[62:65], v[162:165], v[194:197], v[62:65]
	v_mfma_f32_16x16x32_f16 v[58:61], v[170:173], v[194:197], v[58:61]
	v_mfma_f32_16x16x32_f16 v[46:49], v[162:165], v[202:205], v[46:49]
	v_mfma_f32_16x16x32_f16 v[42:45], v[170:173], v[202:205], v[42:45]
	v_mfma_f32_16x16x32_f16 v[30:33], v[162:165], v[210:213], v[30:33]
	v_mfma_f32_16x16x32_f16 v[26:29], v[170:173], v[210:213], v[26:29]
	v_mfma_f32_16x16x32_f16 v[14:17], v[162:165], v[218:221], v[14:17]
	v_mfma_f32_16x16x32_f16 v[10:13], v[170:173], v[218:221], v[10:13]
	v_mfma_f32_16x16x32_f16 v[54:57], v[174:177], v[190:193], v[54:57]
	v_mfma_f32_16x16x32_f16 v[50:53], v[182:185], v[190:193], v[50:53]
	v_mfma_f32_16x16x32_f16 v[38:41], v[174:177], v[198:201], v[38:41]
	v_mfma_f32_16x16x32_f16 v[34:37], v[182:185], v[198:201], v[34:37]
	v_mfma_f32_16x16x32_f16 v[22:25], v[174:177], v[206:209], v[22:25]
	v_mfma_f32_16x16x32_f16 v[18:21], v[182:185], v[206:209], v[18:21]
	v_mfma_f32_16x16x32_f16 v[6:9], v[174:177], v[214:217], v[6:9]
	v_mfma_f32_16x16x32_f16 v[2:5], v[182:185], v[214:217], v[2:5]
	v_mfma_f32_16x16x32_f16 v[54:57], v[178:181], v[194:197], v[54:57]
	v_mfma_f32_16x16x32_f16 v[50:53], v[186:189], v[194:197], v[50:53]
	v_mfma_f32_16x16x32_f16 v[38:41], v[178:181], v[202:205], v[38:41]
	v_mfma_f32_16x16x32_f16 v[34:37], v[186:189], v[202:205], v[34:37]
	v_mfma_f32_16x16x32_f16 v[22:25], v[178:181], v[210:213], v[22:25]
	v_mfma_f32_16x16x32_f16 v[18:21], v[186:189], v[210:213], v[18:21]
	v_mfma_f32_16x16x32_f16 v[6:9], v[178:181], v[218:221], v[6:9]
	v_mfma_f32_16x16x32_f16 v[2:5], v[186:189], v[218:221], v[2:5]
	s_barrier
	s_add_i32 s51, s51, 2
	s_add_u32 s2, s2, 0x100
	s_addc_u32 s3, s3, 0
	s_add_u32 s49, s49, 0x100
	s_addc_u32 s50, s50, 0
	s_cmp_gt_u32 s51, 13
	s_cbranch_scc0 .LBB0_380
	s_and_b64 vcc, exec, s[16:17]
	s_cbranch_vccz .LBB0_383
	s_barrier

; #define GM_STAGE(bufoff, gbase, voff) do { _Pragma("unroll") for (int _i = 0; _i < 2; ++_i) \
;         __builtin_amdgcn_global_load_lds((const unsigned*)((const char*)(gbase) + (voff)[_i]), (LAS unsigned*)(lds + (bufoff) + ldsw + _i * 8192), 16, 0, 0); } while (0)
; #define GM_WAIT_V(n) asm volatile("s_waitcnt vmcnt(" #n ")" ::: "memory")
; #define GM_BAR __builtin_amdgcn_s_barrier()
; #define GM_STA_H0(buf, p, o0) do { if constexpr (GATHER) GM_STAGE(buf, p, o0); else GM_STAGE(buf, p, voffA); } while (0)
; #define GM_STA_H1(buf, p, o1) do { if constexpr (GATHER) GM_STAGE(buf, p, o1); else GM_STAGE(buf, (p) + hstepB, voffA); } while (0)
; template <bool BF, bool GATHER = false, class Epi, class Hook>
; __device__ __forceinline__ void gemm_phase(LAS unsigned char* lds, const Gemm g, const Order& S, const Epi& E, Hook& HK) {
;     ...
;     const size_t hstep = GATHER ? (size_t)0 : (size_t)HALF * K * 2;
;     const size_t hstepB = (size_t)HALF * K * 2;
;     const size_t tstep = 2 * hstepB;
;     const unsigned ldsw = (unsigned)wid * 1024u;
;     const int aoff = lds_byte(wr * 64 + fr, fq * 8), boff = lds_byte(wc * 32 + fr, fq * 8);
;     ...
;     GM_STAGE(GM_SB(0, 0), cB, voffB); GM_STAGE(GM_SB(0, 1), cB + hstepB, voffB); GM_STA_H0(GM_SA(0, 0), cA, gA0); GM_STA_H1(GM_SA(0, 1), cA, gA1);
;     if (wr == 1) GM_BAR;
;     GM_WAIT_V(2); GM_BAR;
;     GM_STAGE(GM_SB(1, 0), cB + kstep, voffB); GM_STA_H0(GM_SA(1, 0), cA + kstep, gA0); GM_STAGE(GM_SB(1, 1), cB + hstepB + kstep, voffB);
;     GM_WAIT_V(6); GM_BAR;
.LBB0_705:
	s_add_u32 s36, s90, 0x102000
	s_addc_u32 s37, s91, 0
	s_lshl_b32 s3, s8, 5
	s_mov_b64 s[8:9], 0x80
	s_and_b32 s14, s3, 0x60
	s_add_i32 m0, s30, 0x18000
	v_lshl_add_u64 v[8:9], v[8:9], 0, s[8:9]
	s_lshl_b32 s11, s10, 13
	s_lshl_b32 s15, s14, 7
	s_waitcnt vmcnt(2)
	s_barrier
	global_load_lds_dwordx4 v[8:9], off
	v_lshl_add_u64 v[6:7], v[6:7], 0, s[8:9]
	s_add_i32 m0, s30, 0x1a000
	s_add_i32 s38, s30, 0x8000
	s_add_i32 s39, s30, 0xa000
	global_load_lds_dwordx4 v[6:7], off
	v_lshl_add_u64 v[2:3], v[2:3], 0, s[8:9]
	s_mov_b32 m0, s38
	s_add_u32 s12, s22, 0x40080
	global_load_lds_dwordx4 v[2:3], off
	v_lshl_add_u64 v[2:3], v[4:5], 0, s[8:9]
	s_mov_b32 m0, s39
	s_addc_u32 s13, s23, 0
	global_load_lds_dwordx4 v[2:3], off
	s_cmpk_lt_u32 s5, 0x100
	v_lshrrev_b32_e32 v3, 1, v10
	v_and_b32_e32 v3, 24, v3
	v_and_b32_e32 v2, 15, v10
	v_lshlrev_b32_e32 v4, 1, v3
	v_lshl_or_b32 v1, s10, 6, v2
	v_lshl_or_b32 v2, v2, 6, v4
	v_lshlrev_b32_e32 v4, 2, v10
	v_and_b32_e32 v4, 32, v4
	v_bitop3_b32 v5, v2, s11, v4 bitop3:0xde
	v_bitop3_b32 v166, v2, s15, v4 bitop3:0xde
	v_lshlrev_b32_e32 v2, 14, v11
	v_and_b32_e32 v2, 0xffff8000, v2
	v_or_b32_e32 v167, s14, v3
	v_lshl_add_u32 v2, v12, 11, v2
	v_and_b32_e32 v3, 1, v11
	v_lshl_or_b32 v2, v3, 6, v2
	v_lshl_add_u32 v154, v13, 1, v2
	v_lshlrev_b32_e32 v2, 14, v14
	v_and_b32_e32 v2, 0xffff8000, v2
	s_waitcnt vmcnt(4)
	v_lshl_add_u32 v2, v15, 11, v2
	v_and_b32_e32 v3, 1, v14
	s_cselect_b64 s[10:11], -1, 0
	v_lshl_or_b32 v2, v3, 6, v2
	s_add_i32 s41, 0, 0x10000
	s_add_i32 s42, 0, 0x14000
	s_sext_i32_i8 s3, s4
	s_ashr_i32 s40, s96, 31
	v_mov_b32_e32 v155, v149
	v_lshl_add_u32 v156, v16, 1, v2
	v_mov_b32_e32 v157, v149
	v_mov_b64_e32 v[158:159], 0x200
	v_mov_b64_e32 v[160:161], 0x1ff
	v_add_u32_e32 v168, s41, v166
	v_add_u32_e32 v169, s42, v166
	v_add_u32_e32 v170, 0, v5
	s_barrier
	s_branch .LBB0_708

; #define GM_STAGE(bufoff, gbase, voff) do { _Pragma("unroll") for (int _i = 0; _i < 2; ++_i) \
;         __builtin_amdgcn_global_load_lds((const unsigned*)((const char*)(gbase) + (voff)[_i]), (LAS unsigned*)(lds + (bufoff) + ldsw + _i * 8192), 16, 0, 0); } while (0)
; #define GM_LDA(dst, b, h) do { _Pragma("unroll") for (int m = 0; m < 4; ++m) _Pragma("unroll") for (int k = 0; k < 2; ++k) dst[m][k] = *(const LAS s16x8*)(lds + GM_SA(b, h) + aoff + m * 2048 + k * 1024); } while (0)
; #define GM_LDB(dst, b, h) do { _Pragma("unroll") for (int n = 0; n < 2; ++n) _Pragma("unroll") for (int k = 0; k < 2; ++k) dst[n][k] = *(const LAS s16x8*)(lds + GM_SB(b, h) + boff + n * 2048 + k * 1024); } while (0)
; #define GM_MMA(ai, bj, At, Bt) do { __builtin_amdgcn_s_setprio(1); _Pragma("unroll") for (int m = 0; m < 4; ++m) _Pragma("unroll") for (int n = 0; n < 2; ++n) _Pragma("unroll") for (int k = 0; k < 2; ++k) \
;         acc[ai][bj][m][n] = mma16<BF>(Bt[n][k], At[m][k], acc[ai][bj][m][n]); __builtin_amdgcn_s_setprio(0); } while (0)
; #define GM_WAIT_V(n) asm volatile("s_waitcnt vmcnt(" #n ")" ::: "memory")
; #define GM_WAIT_L(n) asm volatile("s_waitcnt lgkmcnt(" #n ")" ::: "memory")
; #define GM_BAR __builtin_amdgcn_s_barrier()
; #define GM_SCHED __builtin_amdgcn_sched_barrier(0)
; #define GM_STA_H0(buf, p, o0) do { if constexpr (GATHER) GM_STAGE(buf, p, o0); else GM_STAGE(buf, p, voffA); } while (0)
; #define GM_STA_H1(buf, p, o1) do { if constexpr (GATHER) GM_STAGE(buf, p, o1); else GM_STAGE(buf, (p) + hstepB, voffA); } while (0)
; template <bool BF, bool GATHER = false, class Epi, class Hook>
; __device__ __forceinline__ void gemm_phase(LAS unsigned char* lds, const Gemm g, const Order& S, const Epi& E, Hook& HK) {
;     ...
;             GM_LDB(B0, 0, 0); GM_LDB(B1, 0, 1); GM_SCHED; GM_LDA(At, 0, 0); GM_STA_H1(GM_SA(1, 1), a1, gA1);
;             GM_WAIT_V(8); GM_WAIT_L(0); GM_BAR; GM_MMA(0, 0, At, B0); GM_MMA(0, 1, At, B1); GM_BAR; GM_SCHED;
;             GM_LDA(At, 0, 1); GM_STAGE(GM_SB(0, 0), b2, voffB); GM_STAGE(GM_SB(0, 1), b2 + hstepB, voffB); GM_STA_H0(GM_SA(0, 0), a2, s0);
;             GM_WAIT_V(8); GM_WAIT_L(0); GM_BAR; GM_MMA(1, 0, At, B0); GM_MMA(1, 1, At, B1); GM_BAR; GM_SCHED;
.LBB0_715:
	s_add_u32 s22, s20, 0xfffc0080
	s_addc_u32 s23, s21, -1
	s_cmp_eq_u32 s47, 12
	s_cselect_b32 s25, s13, s23
	s_cselect_b32 s24, s43, s22
	s_cselect_b32 s23, s15, s46
	s_cselect_b32 s22, s44, s45
	s_add_u32 s98, s45, 0x3ff80
	s_addc_u32 s99, s46, 0
	v_lshl_add_u64 v[252:253], s[98:99], 0, v[148:149]
	s_add_i32 m0, s29, 0x1c000
	s_nop 0
	global_load_lds_dwordx4 v[252:253], off
	v_lshl_add_u64 v[252:253], s[98:99], 0, v[152:153]
	s_add_i32 m0, s29, 0x1e000
	s_nop 0
	global_load_lds_dwordx4 v[252:253], off
	v_lshl_add_u64 v[216:217], s[20:21], 0, v[154:155]
	s_add_i32 m0, s30, 0xc000
	global_load_lds_dwordx4 v[216:217], off
	v_lshl_add_u64 v[216:217], s[20:21], 0, v[156:157]
	s_add_i32 m0, s30, 0xe000
	s_nop 0
	global_load_lds_dwordx4 v[216:217], off
	ds_read_b128 v[130:133], v168
	ds_read_b128 v[134:137], v168 offset:1024
	ds_read_b128 v[138:141], v168 offset:2048
	ds_read_b128 v[142:145], v168 offset:3072
	ds_read_b128 v[162:165], v169
	ds_read_b128 v[172:175], v169 offset:1024
	ds_read_b128 v[176:179], v169 offset:2048
	ds_read_b128 v[180:183], v169 offset:3072
	ds_read_b128 v[184:187], v170
	ds_read_b128 v[188:191], v170 offset:1024
	ds_read_b128 v[192:195], v170 offset:2048
	ds_read_b128 v[196:199], v170 offset:3072
	ds_read_b128 v[200:203], v170 offset:4096
	ds_read_b128 v[204:207], v170 offset:5120
	ds_read_b128 v[208:211], v170 offset:6144
	ds_read_b128 v[212:215], v170 offset:7168
	s_waitcnt vmcnt(8)
	s_waitcnt lgkmcnt(0)
	s_barrier
	s_waitcnt lgkmcnt(0)
	v_mfma_f32_16x16x32_f16 v[126:129], v[130:133], v[184:187], v[126:129]
	v_mfma_f32_16x16x32_f16 v[122:125], v[138:141], v[184:187], v[122:125]
	v_mfma_f32_16x16x32_f16 v[110:113], v[130:133], v[192:195], v[110:113]
	v_mfma_f32_16x16x32_f16 v[106:109], v[138:141], v[192:195], v[106:109]
	v_mfma_f32_16x16x32_f16 v[94:97], v[130:133], v[200:203], v[94:97]
	v_mfma_f32_16x16x32_f16 v[90:93], v[138:141], v[200:203], v[90:93]
	v_mfma_f32_16x16x32_f16 v[78:81], v[130:133], v[208:211], v[78:81]
	v_mfma_f32_16x16x32_f16 v[74:77], v[138:141], v[208:211], v[74:77]
	v_mfma_f32_16x16x32_f16 v[126:129], v[134:137], v[188:191], v[126:129]
	v_mfma_f32_16x16x32_f16 v[122:125], v[142:145], v[188:191], v[122:125]
	v_mfma_f32_16x16x32_f16 v[110:113], v[134:137], v[196:199], v[110:113]
	v_mfma_f32_16x16x32_f16 v[106:109], v[142:145], v[196:199], v[106:109]
	v_mfma_f32_16x16x32_f16 v[94:97], v[134:137], v[204:207], v[94:97]
	v_mfma_f32_16x16x32_f16 v[90:93], v[142:145], v[204:207], v[90:93]
	v_mfma_f32_16x16x32_f16 v[78:81], v[134:137], v[212:215], v[78:81]
	v_mfma_f32_16x16x32_f16 v[74:77], v[142:145], v[212:215], v[74:77]
	v_mfma_f32_16x16x32_f16 v[118:121], v[162:165], v[184:187], v[118:121]
	v_mfma_f32_16x16x32_f16 v[114:117], v[176:179], v[184:187], v[114:117]
	v_mfma_f32_16x16x32_f16 v[102:105], v[162:165], v[192:195], v[102:105]
	v_mfma_f32_16x16x32_f16 v[98:101], v[176:179], v[192:195], v[98:101]
	v_mfma_f32_16x16x32_f16 v[86:89], v[162:165], v[200:203], v[86:89]
	v_mfma_f32_16x16x32_f16 v[82:85], v[176:179], v[200:203], v[82:85]
	v_mfma_f32_16x16x32_f16 v[70:73], v[162:165], v[208:211], v[70:73]
	v_mfma_f32_16x16x32_f16 v[66:69], v[176:179], v[208:211], v[66:69]
	v_mfma_f32_16x16x32_f16 v[118:121], v[172:175], v[188:191], v[118:121]
	v_mfma_f32_16x16x32_f16 v[114:117], v[180:183], v[188:191], v[114:117]
	v_mfma_f32_16x16x32_f16 v[102:105], v[172:175], v[196:199], v[102:105]
	v_mfma_f32_16x16x32_f16 v[98:101], v[180:183], v[196:199], v[98:101]
	v_mfma_f32_16x16x32_f16 v[86:89], v[172:175], v[204:207], v[86:89]
	v_mfma_f32_16x16x32_f16 v[82:85], v[180:183], v[204:207], v[82:85]
	v_mfma_f32_16x16x32_f16 v[70:73], v[172:175], v[212:215], v[70:73]
	v_mfma_f32_16x16x32_f16 v[66:69], v[180:183], v[212:215], v[66:69]
	s_barrier
	s_add_i32 s48, s41, s29
	v_lshl_add_u64 v[216:217], s[22:23], 0, v[148:149]
	s_mov_b32 m0, s48
	global_load_lds_dwordx4 v[216:217], off
	s_add_i32 m0, s48, 0x2000
	s_add_u32 s48, s22, 0x40000
	v_lshl_add_u64 v[218:219], s[22:23], 0, v[152:153]
	s_addc_u32 s49, s23, 0
	s_add_i32 s50, s42, s29
	global_load_lds_dwordx4 v[218:219], off
	v_lshl_add_u64 v[222:223], s[24:25], 0, v[150:151]
	v_lshl_add_u64 v[220:221], s[24:25], 0, v[146:147]
	s_mov_b32 m0, s30
	s_nop 0
	global_load_lds_dwordx4 v[220:221], off
	s_mov_b32 m0, s31
	s_nop 0
	global_load_lds_dwordx4 v[222:223], off
	ds_read_b128 v[184:187], v170 offset:16384
	ds_read_b128 v[188:191], v170 offset:17408
	ds_read_b128 v[192:195], v170 offset:18432
	ds_read_b128 v[196:199], v170 offset:19456
	ds_read_b128 v[200:203], v170 offset:20480
	ds_read_b128 v[204:207], v170 offset:21504
	ds_read_b128 v[208:211], v170 offset:22528
	ds_read_b128 v[212:215], v170 offset:23552
	s_waitcnt vmcnt(6)
	s_waitcnt lgkmcnt(0)
	s_barrier
; #define GM_STAGE(bufoff, gbase, voff) do { _Pragma("unroll") for (int _i = 0; _i < 2; ++_i) \
;         __builtin_amdgcn_global_load_lds((const unsigned*)((const char*)(gbase) + (voff)[_i]), (LAS unsigned*)(lds + (bufoff) + ldsw + _i * 8192), 16, 0, 0); } while (0)
; #define GM_LDA(dst, b, h) do { _Pragma("unroll") for (int m = 0; m < 4; ++m) _Pragma("unroll") for (int k = 0; k < 2; ++k) dst[m][k] = *(const LAS s16x8*)(lds + GM_SA(b, h) + aoff + m * 2048 + k * 1024); } while (0)
; #define GM_LDB(dst, b, h) do { _Pragma("unroll") for (int n = 0; n < 2; ++n) _Pragma("unroll") for (int k = 0; k < 2; ++k) dst[n][k] = *(const LAS s16x8*)(lds + GM_SB(b, h) + boff + n * 2048 + k * 1024); } while (0)
; #define GM_MMA(ai, bj, At, Bt) do { __builtin_amdgcn_s_setprio(1); _Pragma("unroll") for (int m = 0; m < 4; ++m) _Pragma("unroll") for (int n = 0; n < 2; ++n) _Pragma("unroll") for (int k = 0; k < 2; ++k) \
;         acc[ai][bj][m][n] = mma16<BF>(Bt[n][k], At[m][k], acc[ai][bj][m][n]); __builtin_amdgcn_s_setprio(0); } while (0)
; #define GM_WAIT_V(n) asm volatile("s_waitcnt vmcnt(" #n ")" ::: "memory")
; #define GM_WAIT_L(n) asm volatile("s_waitcnt lgkmcnt(" #n ")" ::: "memory")
; #define GM_BAR __builtin_amdgcn_s_barrier()
; #define GM_SCHED __builtin_amdgcn_sched_barrier(0)
; #define GM_STA_H0(buf, p, o0) do { if constexpr (GATHER) GM_STAGE(buf, p, o0); else GM_STAGE(buf, p, voffA); } while (0)
; #define GM_STA_H1(buf, p, o1) do { if constexpr (GATHER) GM_STAGE(buf, p, o1); else GM_STAGE(buf, (p) + hstepB, voffA); } while (0)
; template <bool BF, bool GATHER = false, class Epi, class Hook>
; __device__ __forceinline__ void gemm_phase(LAS unsigned char* lds, const Gemm g, const Order& S, const Epi& E, Hook& HK) {
;     ...
;             GM_WAIT_V(8); GM_WAIT_L(0); GM_BAR; GM_MMA(1, 0, At, B0); GM_MMA(1, 1, At, B1); GM_BAR; GM_SCHED;
;             GM_LDB(B0, 1, 0); GM_LDB(B1, 1, 1); GM_SCHED; GM_LDA(At, 1, 0); GM_STA_H1(GM_SA(0, 1), a2, s1);
;             GM_WAIT_V(8); GM_WAIT_L(0); GM_BAR; GM_MMA(0, 0, At, B0); GM_MMA(0, 1, At, B1); GM_BAR; GM_SCHED;
;             GM_LDA(At, 1, 1); GM_STAGE(GM_SB(1, 0), b3, voffB); GM_STAGE(GM_SB(1, 1), b3 + hstepB, voffB); GM_STA_H0(GM_SA(1, 0), a3, s0);
	s_waitcnt lgkmcnt(0)
	v_mfma_f32_16x16x32_f16 v[62:65], v[130:133], v[184:187], v[62:65]
	v_mfma_f32_16x16x32_f16 v[58:61], v[138:141], v[184:187], v[58:61]
	v_mfma_f32_16x16x32_f16 v[46:49], v[130:133], v[192:195], v[46:49]
	v_mfma_f32_16x16x32_f16 v[42:45], v[138:141], v[192:195], v[42:45]
	v_mfma_f32_16x16x32_f16 v[30:33], v[130:133], v[200:203], v[30:33]
	v_mfma_f32_16x16x32_f16 v[26:29], v[138:141], v[200:203], v[26:29]
	v_mfma_f32_16x16x32_f16 v[14:17], v[130:133], v[208:211], v[14:17]
	v_mfma_f32_16x16x32_f16 v[10:13], v[138:141], v[208:211], v[10:13]
	v_mfma_f32_16x16x32_f16 v[62:65], v[134:137], v[188:191], v[62:65]
	v_mfma_f32_16x16x32_f16 v[58:61], v[142:145], v[188:191], v[58:61]
	v_mfma_f32_16x16x32_f16 v[46:49], v[134:137], v[196:199], v[46:49]
	v_mfma_f32_16x16x32_f16 v[42:45], v[142:145], v[196:199], v[42:45]
	v_mfma_f32_16x16x32_f16 v[30:33], v[134:137], v[204:207], v[30:33]
	v_mfma_f32_16x16x32_f16 v[26:29], v[142:145], v[204:207], v[26:29]
	v_mfma_f32_16x16x32_f16 v[14:17], v[134:137], v[212:215], v[14:17]
	v_mfma_f32_16x16x32_f16 v[10:13], v[142:145], v[212:215], v[10:13]
	v_mfma_f32_16x16x32_f16 v[54:57], v[162:165], v[184:187], v[54:57]
	v_mfma_f32_16x16x32_f16 v[50:53], v[176:179], v[184:187], v[50:53]
	v_mfma_f32_16x16x32_f16 v[38:41], v[162:165], v[192:195], v[38:41]
	v_mfma_f32_16x16x32_f16 v[34:37], v[176:179], v[192:195], v[34:37]
	v_mfma_f32_16x16x32_f16 v[22:25], v[162:165], v[200:203], v[22:25]
	v_mfma_f32_16x16x32_f16 v[18:21], v[176:179], v[200:203], v[18:21]
	v_mfma_f32_16x16x32_f16 v[6:9], v[162:165], v[208:211], v[6:9]
	v_mfma_f32_16x16x32_f16 v[2:5], v[176:179], v[208:211], v[2:5]
	v_mfma_f32_16x16x32_f16 v[54:57], v[172:175], v[188:191], v[54:57]
	v_mfma_f32_16x16x32_f16 v[50:53], v[180:183], v[188:191], v[50:53]
	v_mfma_f32_16x16x32_f16 v[38:41], v[172:175], v[196:199], v[38:41]
	v_mfma_f32_16x16x32_f16 v[34:37], v[180:183], v[196:199], v[34:37]
	v_mfma_f32_16x16x32_f16 v[22:25], v[172:175], v[204:207], v[22:25]
	v_mfma_f32_16x16x32_f16 v[18:21], v[180:183], v[204:207], v[18:21]
	v_mfma_f32_16x16x32_f16 v[6:9], v[172:175], v[212:215], v[6:9]
	v_mfma_f32_16x16x32_f16 v[2:5], v[180:183], v[212:215], v[2:5]
	s_barrier
	s_add_u32 s24, s24, 0x40000
	s_addc_u32 s25, s25, 0
	s_add_u32 s98, s22, 0x40000
	s_addc_u32 s99, s23, 0
	v_lshl_add_u64 v[252:253], s[98:99], 0, v[148:149]
	s_add_i32 m0, s29, 0x14000
	s_nop 0
	global_load_lds_dwordx4 v[252:253], off
	v_lshl_add_u64 v[252:253], s[98:99], 0, v[152:153]
	s_add_i32 m0, s29, 0x16000
	s_nop 0
	global_load_lds_dwordx4 v[252:253], off
	s_mov_b32 m0, s33
	v_lshl_add_u64 v[224:225], s[24:25], 0, v[146:147]
	global_load_lds_dwordx4 v[224:225], off
	v_lshl_add_u64 v[224:225], s[24:25], 0, v[150:151]
	s_mov_b32 m0, s34
	s_nop 0
	global_load_lds_dwordx4 v[224:225], off
	s_mov_b32 s49, 0x1c000
	s_mov_b32 s48, 0x18000
	v_add_u32_e32 v244, s48, v166
	v_add_u32_e32 v245, s49, v166
	ds_read_b128 v[130:133], v244
	ds_read_b128 v[134:137], v244 offset:1024
	ds_read_b128 v[138:141], v244 offset:2048
	ds_read_b128 v[142:145], v244 offset:3072
	ds_read_b128 v[162:165], v245
	ds_read_b128 v[172:175], v245 offset:1024
	ds_read_b128 v[176:179], v245 offset:2048
	ds_read_b128 v[180:183], v245 offset:3072
	ds_read_b128 v[184:187], v170 offset:32768
	ds_read_b128 v[188:191], v170 offset:33792
	ds_read_b128 v[192:195], v170 offset:34816
	ds_read_b128 v[196:199], v170 offset:35840
	ds_read_b128 v[200:203], v170 offset:36864
	ds_read_b128 v[204:207], v170 offset:37888
	ds_read_b128 v[208:211], v170 offset:38912
	ds_read_b128 v[212:215], v170 offset:39936
	s_waitcnt vmcnt(8)
	s_waitcnt lgkmcnt(0)
	s_barrier
; #define GM_STAGE(bufoff, gbase, voff) do { _Pragma("unroll") for (int _i = 0; _i < 2; ++_i) \
;         __builtin_amdgcn_global_load_lds((const unsigned*)((const char*)(gbase) + (voff)[_i]), (LAS unsigned*)(lds + (bufoff) + ldsw + _i * 8192), 16, 0, 0); } while (0)
; #define GM_LDA(dst, b, h) do { _Pragma("unroll") for (int m = 0; m < 4; ++m) _Pragma("unroll") for (int k = 0; k < 2; ++k) dst[m][k] = *(const LAS s16x8*)(lds + GM_SA(b, h) + aoff + m * 2048 + k * 1024); } while (0)
; #define GM_MMA(ai, bj, At, Bt) do { __builtin_amdgcn_s_setprio(1); _Pragma("unroll") for (int m = 0; m < 4; ++m) _Pragma("unroll") for (int n = 0; n < 2; ++n) _Pragma("unroll") for (int k = 0; k < 2; ++k) \
;         acc[ai][bj][m][n] = mma16<BF>(Bt[n][k], At[m][k], acc[ai][bj][m][n]); __builtin_amdgcn_s_setprio(0); } while (0)
; #define GM_WAIT_V(n) asm volatile("s_waitcnt vmcnt(" #n ")" ::: "memory")
; #define GM_WAIT_L(n) asm volatile("s_waitcnt lgkmcnt(" #n ")" ::: "memory")
; #define GM_BAR __builtin_amdgcn_s_barrier()
; #define GM_SCHED __builtin_amdgcn_sched_barrier(0)
; #define GM_STA_H0(buf, p, o0) do { if constexpr (GATHER) GM_STAGE(buf, p, o0); else GM_STAGE(buf, p, voffA); } while (0)
; template <bool BF, bool GATHER = false, class Epi, class Hook>
; __device__ __forceinline__ void gemm_phase(LAS unsigned char* lds, const Gemm g, const Order& S, const Epi& E, Hook& HK) {
;     ...
;             GM_WAIT_V(8); GM_WAIT_L(0); GM_BAR; GM_MMA(0, 0, At, B0); GM_MMA(0, 1, At, B1); GM_BAR; GM_SCHED;
;             GM_LDA(At, 1, 1); GM_STAGE(GM_SB(1, 0), b3, voffB); GM_STAGE(GM_SB(1, 1), b3 + hstepB, voffB); GM_STA_H0(GM_SA(1, 0), a3, s0);
;             GM_WAIT_V(8); GM_WAIT_L(0); GM_BAR; GM_MMA(1, 0, At, B0); GM_MMA(1, 1, At, B1); GM_BAR; GM_SCHED;
;         }
	s_waitcnt lgkmcnt(0)
	v_mfma_f32_16x16x32_f16 v[126:129], v[130:133], v[184:187], v[126:129]
	v_mfma_f32_16x16x32_f16 v[122:125], v[138:141], v[184:187], v[122:125]
	v_mfma_f32_16x16x32_f16 v[110:113], v[130:133], v[192:195], v[110:113]
	v_mfma_f32_16x16x32_f16 v[106:109], v[138:141], v[192:195], v[106:109]
	v_mfma_f32_16x16x32_f16 v[94:97], v[130:133], v[200:203], v[94:97]
	v_mfma_f32_16x16x32_f16 v[90:93], v[138:141], v[200:203], v[90:93]
	v_mfma_f32_16x16x32_f16 v[78:81], v[130:133], v[208:211], v[78:81]
	v_mfma_f32_16x16x32_f16 v[74:77], v[138:141], v[208:211], v[74:77]
	v_mfma_f32_16x16x32_f16 v[126:129], v[134:137], v[188:191], v[126:129]
	v_mfma_f32_16x16x32_f16 v[122:125], v[142:145], v[188:191], v[122:125]
	v_mfma_f32_16x16x32_f16 v[110:113], v[134:137], v[196:199], v[110:113]
	v_mfma_f32_16x16x32_f16 v[106:109], v[142:145], v[196:199], v[106:109]
	v_mfma_f32_16x16x32_f16 v[94:97], v[134:137], v[204:207], v[94:97]
	v_mfma_f32_16x16x32_f16 v[90:93], v[142:145], v[204:207], v[90:93]
	v_mfma_f32_16x16x32_f16 v[78:81], v[134:137], v[212:215], v[78:81]
	v_mfma_f32_16x16x32_f16 v[74:77], v[142:145], v[212:215], v[74:77]
	v_mfma_f32_16x16x32_f16 v[118:121], v[162:165], v[184:187], v[118:121]
	v_mfma_f32_16x16x32_f16 v[114:117], v[176:179], v[184:187], v[114:117]
	v_mfma_f32_16x16x32_f16 v[102:105], v[162:165], v[192:195], v[102:105]
	v_mfma_f32_16x16x32_f16 v[98:101], v[176:179], v[192:195], v[98:101]
	v_mfma_f32_16x16x32_f16 v[86:89], v[162:165], v[200:203], v[86:89]
	v_mfma_f32_16x16x32_f16 v[82:85], v[176:179], v[200:203], v[82:85]
	v_mfma_f32_16x16x32_f16 v[70:73], v[162:165], v[208:211], v[70:73]
	v_mfma_f32_16x16x32_f16 v[66:69], v[176:179], v[208:211], v[66:69]
	v_mfma_f32_16x16x32_f16 v[118:121], v[172:175], v[188:191], v[118:121]
	v_mfma_f32_16x16x32_f16 v[114:117], v[180:183], v[188:191], v[114:117]
	v_mfma_f32_16x16x32_f16 v[102:105], v[172:175], v[196:199], v[102:105]
	v_mfma_f32_16x16x32_f16 v[98:101], v[180:183], v[196:199], v[98:101]
	v_mfma_f32_16x16x32_f16 v[86:89], v[172:175], v[204:207], v[86:89]
	v_mfma_f32_16x16x32_f16 v[82:85], v[180:183], v[204:207], v[82:85]
	v_mfma_f32_16x16x32_f16 v[70:73], v[172:175], v[212:215], v[70:73]
	v_mfma_f32_16x16x32_f16 v[66:69], v[180:183], v[212:215], v[66:69]
	s_barrier
	s_add_i32 s24, s48, s29
	v_lshl_add_u64 v[216:217], v[216:217], 0, s[8:9]
	s_mov_b32 m0, s24
	global_load_lds_dwordx4 v[216:217], off
	s_add_i32 m0, s24, 0x2000
	s_add_u32 s22, s22, 0x40080
	v_lshl_add_u64 v[216:217], v[218:219], 0, s[8:9]
	s_addc_u32 s23, s23, 0
	s_add_i32 s24, s49, s29
	global_load_lds_dwordx4 v[216:217], off
	v_lshl_add_u64 v[216:217], v[220:221], 0, s[8:9]
	s_mov_b32 m0, s38
	s_nop 0
	global_load_lds_dwordx4 v[216:217], off
	v_lshl_add_u64 v[216:217], v[222:223], 0, s[8:9]
	s_mov_b32 m0, s39
	s_nop 0
	global_load_lds_dwordx4 v[216:217], off
	ds_read_b128 v[184:187], v170 offset:49152
	ds_read_b128 v[188:191], v170 offset:50176
	ds_read_b128 v[192:195], v170 offset:51200
	ds_read_b128 v[196:199], v170 offset:52224
	ds_read_b128 v[200:203], v170 offset:53248
	ds_read_b128 v[204:207], v170 offset:54272
	ds_read_b128 v[208:211], v170 offset:55296
	ds_read_b128 v[212:215], v170 offset:56320
	s_waitcnt vmcnt(6)
	s_waitcnt lgkmcnt(0)
	s_barrier
	s_waitcnt lgkmcnt(0)
	v_mfma_f32_16x16x32_f16 v[62:65], v[130:133], v[184:187], v[62:65]
	v_mfma_f32_16x16x32_f16 v[58:61], v[138:141], v[184:187], v[58:61]
	v_mfma_f32_16x16x32_f16 v[46:49], v[130:133], v[192:195], v[46:49]
	v_mfma_f32_16x16x32_f16 v[42:45], v[138:141], v[192:195], v[42:45]
	v_mfma_f32_16x16x32_f16 v[30:33], v[130:133], v[200:203], v[30:33]
	v_mfma_f32_16x16x32_f16 v[26:29], v[138:141], v[200:203], v[26:29]
	v_mfma_f32_16x16x32_f16 v[14:17], v[130:133], v[208:211], v[14:17]
	v_mfma_f32_16x16x32_f16 v[10:13], v[138:141], v[208:211], v[10:13]
	v_mfma_f32_16x16x32_f16 v[62:65], v[134:137], v[188:191], v[62:65]
	v_mfma_f32_16x16x32_f16 v[58:61], v[142:145], v[188:191], v[58:61]
	v_mfma_f32_16x16x32_f16 v[46:49], v[134:137], v[196:199], v[46:49]
	v_mfma_f32_16x16x32_f16 v[42:45], v[142:145], v[196:199], v[42:45]
	v_mfma_f32_16x16x32_f16 v[30:33], v[134:137], v[204:207], v[30:33]
	v_mfma_f32_16x16x32_f16 v[26:29], v[142:145], v[204:207], v[26:29]
	v_mfma_f32_16x16x32_f16 v[14:17], v[134:137], v[212:215], v[14:17]
	v_mfma_f32_16x16x32_f16 v[10:13], v[142:145], v[212:215], v[10:13]
	v_mfma_f32_16x16x32_f16 v[54:57], v[162:165], v[184:187], v[54:57]
	v_mfma_f32_16x16x32_f16 v[50:53], v[176:179], v[184:187], v[50:53]
	v_mfma_f32_16x16x32_f16 v[38:41], v[162:165], v[192:195], v[38:41]
	v_mfma_f32_16x16x32_f16 v[34:37], v[176:179], v[192:195], v[34:37]
	v_mfma_f32_16x16x32_f16 v[22:25], v[162:165], v[200:203], v[22:25]
	v_mfma_f32_16x16x32_f16 v[18:21], v[176:179], v[200:203], v[18:21]
	v_mfma_f32_16x16x32_f16 v[6:9], v[162:165], v[208:211], v[6:9]
	v_mfma_f32_16x16x32_f16 v[2:5], v[176:179], v[208:211], v[2:5]
	v_mfma_f32_16x16x32_f16 v[54:57], v[172:175], v[188:191], v[54:57]
	v_mfma_f32_16x16x32_f16 v[50:53], v[180:183], v[188:191], v[50:53]
	v_mfma_f32_16x16x32_f16 v[38:41], v[172:175], v[196:199], v[38:41]
	v_mfma_f32_16x16x32_f16 v[34:37], v[180:183], v[196:199], v[34:37]
	v_mfma_f32_16x16x32_f16 v[22:25], v[172:175], v[204:207], v[22:25]
	v_mfma_f32_16x16x32_f16 v[18:21], v[180:183], v[204:207], v[18:21]
	v_mfma_f32_16x16x32_f16 v[6:9], v[172:175], v[212:215], v[6:9]
	v_mfma_f32_16x16x32_f16 v[2:5], v[180:183], v[212:215], v[2:5]
	s_barrier
	s_add_i32 s47, s47, 2
	s_add_u32 s20, s20, 0x100
	s_addc_u32 s21, s21, 0
	s_add_u32 s45, s45, 0x100
	s_addc_u32 s46, s46, 0
	s_cmp_gt_u32 s47, 13
	s_cbranch_scc0 .LBB0_715
	s_and_b64 vcc, exec, s[10:11]
	s_cbranch_vccz .LBB0_718
	s_barrier

; #define GM_STAGE(bufoff, gbase, voff) do { _Pragma("unroll") for (int _i = 0; _i < 2; ++_i) \
;         __builtin_amdgcn_global_load_lds((const unsigned*)((const char*)(gbase) + (voff)[_i]), (LAS unsigned*)(lds + (bufoff) + ldsw + _i * 8192), 16, 0, 0); } while (0)
; #define GM_WAIT_V(n) asm volatile("s_waitcnt vmcnt(" #n ")" ::: "memory")
; #define GM_BAR __builtin_amdgcn_s_barrier()
; #define GM_STA_H0(buf, p, o0) do { if constexpr (GATHER) GM_STAGE(buf, p, o0); else GM_STAGE(buf, p, voffA); } while (0)
; #define GM_STA_H1(buf, p, o1) do { if constexpr (GATHER) GM_STAGE(buf, p, o1); else GM_STAGE(buf, (p) + hstepB, voffA); } while (0)
; template <bool BF, bool GATHER = false, class Epi, class Hook>
; __device__ __forceinline__ void gemm_phase(LAS unsigned char* lds, const Gemm g, const Order& S, const Epi& E, Hook& HK) {
;     ...
;     Unit cur, nxt; int ui = 0;
;     if (!S.next(0, cur)) return;
;     Acc acc;
; #pragma unroll
;     for (int a = 0; a < 2; ++a)
; #pragma unroll
;         for (int b = 0; b < 2; ++b)
; #pragma unroll
;             for (int m = 0; m < 4; ++m)
; #pragma unroll
;                 for (int n = 0; n < 2; ++n) acc[a][b][m][n] = (f32x4){0.f, 0.f, 0.f, 0.f};
;     ...
;     GM_STAGE(GM_SB(0, 0), cB, voffB); GM_STAGE(GM_SB(0, 1), cB + hstepB, voffB); GM_STA_H0(GM_SA(0, 0), cA, gA0); GM_STA_H1(GM_SA(0, 1), cA, gA1);
;     if (wr == 1) GM_BAR;
;     GM_WAIT_V(2); GM_BAR;
;     GM_STAGE(GM_SB(1, 0), cB + kstep, voffB); GM_STA_H0(GM_SA(1, 0), cA + kstep, gA0); GM_STAGE(GM_SB(1, 1), cB + hstepB + kstep, voffB);
;     GM_WAIT_V(6); GM_BAR;
.LBB0_1002:
	v_lshrrev_b32_e32 v8, 1, v6
	v_and_b32_e32 v8, 24, v8
	v_and_b32_e32 v7, 15, v6
	v_lshlrev_b32_e32 v9, 1, v8
	v_lshlrev_b32_e32 v6, 2, v6
	v_lshl_or_b32 v155, s5, 6, v7
	v_lshl_or_b32 v7, v7, 6, v9
	s_lshl_b32 s0, s5, 13
	v_and_b32_e32 v6, 32, v6
	v_bitop3_b32 v9, v7, s0, v6 bitop3:0xde
	s_lshl_b32 s0, s6, 5
	s_mov_b64 s[14:15], 0x80
	s_and_b32 s5, s0, 0x60
	s_add_i32 m0, s28, 0x18000
	v_lshl_add_u64 v[4:5], v[4:5], 0, s[14:15]
	s_lshl_b32 s0, s5, 7
	s_waitcnt vmcnt(2)
	s_barrier
	global_load_lds_dwordx4 v[4:5], off
	s_add_i32 m0, s28, 0x1a000
	s_add_u32 s16, s90, 0x11e00080
	v_lshl_add_u64 v[2:3], v[2:3], 0, s[14:15]
	s_addc_u32 s17, s91, 0
	s_add_i32 s33, s28, 0x8000
	s_add_i32 s34, s28, 0xa000
	v_bitop3_b32 v156, v7, s0, v6 bitop3:0xde
	global_load_lds_dwordx4 v[2:3], off
	v_lshl_add_u64 v[2:3], s[16:17], 0, v[142:143]
	s_mov_b32 m0, s33
	s_add_u32 s0, s2, 0x40080
	global_load_lds_dwordx4 v[2:3], off
	v_lshl_add_u64 v[2:3], s[16:17], 0, v[146:147]
	s_mov_b32 m0, s34
	s_addc_u32 s1, s3, 0
	global_load_lds_dwordx4 v[2:3], off
	s_cmpk_lt_u32 s4, 0x100
	s_waitcnt vmcnt(4)
	v_mov_b32_e32 v135, 0
	s_cselect_b64 s[18:19], -1, 0
	v_or_b32_e32 v143, s5, v8
	v_mov_b64_e32 v[136:137], 0x1600
	v_mov_b64_e32 v[138:139], 0x15ff
	s_add_i32 s35, 0, 0x10000
	s_add_i32 s36, 0, 0x14000
	v_add_u32_e32 v147, 0, v9
	s_movk_i32 s37, 0x1600
	v_mov_b32_e32 v157, v144
	v_mov_b32_e32 v158, v140
	v_mov_b32_e32 v2, v135
	v_mov_b32_e32 v3, v135
	v_mov_b32_e32 v4, v135
	v_mov_b32_e32 v5, v135
	v_mov_b32_e32 v6, v135
	v_mov_b32_e32 v7, v135
	v_mov_b32_e32 v8, v135
	v_mov_b32_e32 v9, v135
	v_mov_b32_e32 v10, v135
	v_mov_b32_e32 v11, v135
	v_mov_b32_e32 v12, v135
	v_mov_b32_e32 v13, v135
	v_mov_b32_e32 v14, v135
	v_mov_b32_e32 v15, v135
	v_mov_b32_e32 v16, v135
	v_mov_b32_e32 v17, v135
	v_mov_b32_e32 v18, v135
	v_mov_b32_e32 v19, v135
	v_mov_b32_e32 v20, v135
	v_mov_b32_e32 v21, v135
	v_mov_b32_e32 v22, v135
	v_mov_b32_e32 v23, v135
	v_mov_b32_e32 v24, v135
	v_mov_b32_e32 v25, v135
	v_mov_b32_e32 v26, v135
	v_mov_b32_e32 v27, v135
	v_mov_b32_e32 v28, v135
	v_mov_b32_e32 v29, v135
	v_mov_b32_e32 v30, v135
	v_mov_b32_e32 v31, v135
	v_mov_b32_e32 v32, v135
	v_mov_b32_e32 v33, v135
	v_mov_b32_e32 v34, v135
	v_mov_b32_e32 v35, v135
	v_mov_b32_e32 v36, v135
	v_mov_b32_e32 v37, v135
	v_mov_b32_e32 v38, v135
	v_mov_b32_e32 v39, v135
	v_mov_b32_e32 v40, v135
	v_mov_b32_e32 v41, v135
	v_mov_b32_e32 v42, v135
	v_mov_b32_e32 v43, v135
	v_mov_b32_e32 v44, v135
	v_mov_b32_e32 v45, v135
	v_mov_b32_e32 v46, v135
	v_mov_b32_e32 v47, v135
	v_mov_b32_e32 v48, v135
	v_mov_b32_e32 v49, v135
	v_mov_b32_e32 v50, v135
	v_mov_b32_e32 v51, v135
	v_mov_b32_e32 v52, v135
	v_mov_b32_e32 v53, v135
	v_mov_b32_e32 v54, v135
	v_mov_b32_e32 v55, v135
	v_mov_b32_e32 v56, v135
	v_mov_b32_e32 v57, v135
	v_mov_b32_e32 v58, v135
	v_mov_b32_e32 v59, v135
	v_mov_b32_e32 v60, v135
	v_mov_b32_e32 v61, v135
	v_mov_b32_e32 v62, v135
	v_mov_b32_e32 v63, v135
	v_mov_b32_e32 v64, v135
	v_mov_b32_e32 v65, v135
	v_mov_b32_e32 v66, v135
	v_mov_b32_e32 v67, v135
	v_mov_b32_e32 v68, v135
	v_mov_b32_e32 v69, v135
	v_mov_b32_e32 v70, v135
	v_mov_b32_e32 v71, v135
	v_mov_b32_e32 v72, v135
	v_mov_b32_e32 v73, v135
	v_mov_b32_e32 v74, v135
	v_mov_b32_e32 v75, v135
	v_mov_b32_e32 v76, v135
	v_mov_b32_e32 v77, v135
	v_mov_b32_e32 v78, v135
	v_mov_b32_e32 v79, v135
	v_mov_b32_e32 v80, v135
	v_mov_b32_e32 v81, v135
	v_mov_b32_e32 v82, v135
	v_mov_b32_e32 v83, v135
	v_mov_b32_e32 v84, v135
	v_mov_b32_e32 v85, v135
	v_mov_b32_e32 v86, v135
	v_mov_b32_e32 v87, v135
	v_mov_b32_e32 v88, v135
	v_mov_b32_e32 v89, v135
	v_mov_b32_e32 v90, v135
	v_mov_b32_e32 v91, v135
	v_mov_b32_e32 v92, v135
	v_mov_b32_e32 v93, v135
	v_mov_b32_e32 v94, v135
	v_mov_b32_e32 v95, v135
	v_mov_b32_e32 v96, v135
	v_mov_b32_e32 v97, v135
	v_mov_b32_e32 v98, v135
	v_mov_b32_e32 v99, v135
	v_mov_b32_e32 v100, v135
	v_mov_b32_e32 v101, v135
	v_mov_b32_e32 v102, v135
	v_mov_b32_e32 v103, v135
	v_mov_b32_e32 v104, v135
	v_mov_b32_e32 v105, v135
	v_mov_b32_e32 v106, v135
	v_mov_b32_e32 v107, v135
	v_mov_b32_e32 v108, v135
	v_mov_b32_e32 v109, v135
	v_mov_b32_e32 v110, v135
	v_mov_b32_e32 v111, v135
	v_mov_b32_e32 v112, v135
	v_mov_b32_e32 v113, v135
	v_mov_b32_e32 v114, v135
	v_mov_b32_e32 v115, v135
	v_mov_b32_e32 v116, v135
	v_mov_b32_e32 v117, v135
	v_mov_b32_e32 v118, v135
	v_mov_b32_e32 v119, v135
	v_mov_b32_e32 v120, v135
	v_mov_b32_e32 v121, v135
	v_mov_b32_e32 v122, v135
	v_mov_b32_e32 v123, v135
	v_mov_b32_e32 v124, v135
	v_mov_b32_e32 v125, v135
	v_mov_b32_e32 v126, v135
	v_mov_b32_e32 v127, v135
	v_mov_b32_e32 v128, v135
	v_mov_b32_e32 v129, v135
	s_barrier
	s_branch .LBB0_1004

; #define GM_STAGE(bufoff, gbase, voff) do { _Pragma("unroll") for (int _i = 0; _i < 2; ++_i) \
;         __builtin_amdgcn_global_load_lds((const unsigned*)((const char*)(gbase) + (voff)[_i]), (LAS unsigned*)(lds + (bufoff) + ldsw + _i * 8192), 16, 0, 0); } while (0)
; #define GM_LDA(dst, b, h) do { _Pragma("unroll") for (int m = 0; m < 4; ++m) _Pragma("unroll") for (int k = 0; k < 2; ++k) dst[m][k] = *(const LAS s16x8*)(lds + GM_SA(b, h) + aoff + m * 2048 + k * 1024); } while (0)
; #define GM_LDB(dst, b, h) do { _Pragma("unroll") for (int n = 0; n < 2; ++n) _Pragma("unroll") for (int k = 0; k < 2; ++k) dst[n][k] = *(const LAS s16x8*)(lds + GM_SB(b, h) + boff + n * 2048 + k * 1024); } while (0)
; #define GM_MMA(ai, bj, At, Bt) do { __builtin_amdgcn_s_setprio(1); _Pragma("unroll") for (int m = 0; m < 4; ++m) _Pragma("unroll") for (int n = 0; n < 2; ++n) _Pragma("unroll") for (int k = 0; k < 2; ++k) \
;         acc[ai][bj][m][n] = mma16<BF>(Bt[n][k], At[m][k], acc[ai][bj][m][n]); __builtin_amdgcn_s_setprio(0); } while (0)
; #define GM_WAIT_V(n) asm volatile("s_waitcnt vmcnt(" #n ")" ::: "memory")
; #define GM_WAIT_L(n) asm volatile("s_waitcnt lgkmcnt(" #n ")" ::: "memory")
; #define GM_BAR __builtin_amdgcn_s_barrier()
; #define GM_SCHED __builtin_amdgcn_sched_barrier(0)
; #define GM_STA_H0(buf, p, o0) do { if constexpr (GATHER) GM_STAGE(buf, p, o0); else GM_STAGE(buf, p, voffA); } while (0)
; #define GM_STA_H1(buf, p, o1) do { if constexpr (GATHER) GM_STAGE(buf, p, o1); else GM_STAGE(buf, (p) + hstepB, voffA); } while (0)
; template <bool BF, bool GATHER = false, class Epi, class Hook>
; __device__ __forceinline__ void gemm_phase(LAS unsigned char* lds, const Gemm g, const Order& S, const Epi& E, Hook& HK) {
;     ...
;             if constexpr (GATHER) { s0[0] = last ? nA0[0] : gA0[0]; s0[1] = last ? nA0[1] : gA0[1]; s1[0] = last ? nA1[0] : gA1[0]; s1[1] = last ? nA1[1] : gA1[1]; }
;             GM_LDB(B0, 0, 0); GM_LDB(B1, 0, 1); GM_SCHED; GM_LDA(At, 0, 0); GM_STA_H1(GM_SA(1, 1), a1, gA1);
;             GM_WAIT_V(8); GM_WAIT_L(0); GM_BAR; GM_MMA(0, 0, At, B0); GM_MMA(0, 1, At, B1); GM_BAR; GM_SCHED;
;             GM_LDA(At, 0, 1); GM_STAGE(GM_SB(0, 0), b2, voffB); GM_STAGE(GM_SB(0, 1), b2 + hstepB, voffB); GM_STA_H0(GM_SA(0, 0), a2, s0);
;             GM_WAIT_V(8); GM_WAIT_L(0); GM_BAR; GM_MMA(1, 0, At, B0); GM_MMA(1, 1, At, B1); GM_BAR; GM_SCHED;
.LBB0_1011:
	s_add_u32 s22, s90, s2
	s_addc_u32 s23, s91, s3
	s_add_u32 s24, s22, 0x11e00100
	s_addc_u32 s25, s23, 0
	s_add_u32 s44, s21, s2
	s_addc_u32 s45, s42, s3
	s_cmpk_eq_i32 s2, 0x700
	s_cselect_b64 vcc, -1, 0
	s_and_b64 s[22:23], vcc, exec
	v_cndmask_b32_e32 v134, v142, v159, vcc
	s_cselect_b32 s25, s69, s25
	s_cselect_b32 s24, s68, s24
	v_cndmask_b32_e32 v228, v146, v162, vcc
	v_cndmask_b32_e32 v141, v158, v160, vcc
	v_cndmask_b32_e32 v145, v157, v161, vcc
	s_cselect_b32 s23, s1, s45
	s_cselect_b32 s22, s0, s44
	s_add_u32 s98, s44, 0x3ff80
	s_addc_u32 s99, s45, 0
	v_lshl_add_u64 v[252:253], s[98:99], 0, v[130:131]
	s_add_i32 m0, s11, 0x1c000
	s_nop 0
	global_load_lds_dwordx4 v[252:253], off
	v_lshl_add_u64 v[252:253], s[98:99], 0, v[132:133]
	s_add_i32 m0, s11, 0x1e000
	s_nop 0
	global_load_lds_dwordx4 v[252:253], off
	v_lshl_add_u64 v[230:231], v[150:151], 0, s[2:3]
	s_add_i32 m0, s28, 0xc000
	global_load_lds_dwordx4 v[230:231], off
	v_lshl_add_u64 v[230:231], v[148:149], 0, s[2:3]
	s_add_i32 m0, s28, 0xe000
	s_nop 0
	global_load_lds_dwordx4 v[230:231], off
	v_add_u32_e32 v244, s35, v156
	ds_read_b128 v[164:167], v244
	ds_read_b128 v[168:171], v244 offset:1024
	ds_read_b128 v[172:175], v244 offset:2048
	ds_read_b128 v[176:179], v244 offset:3072
	v_add_u32_e32 v244, s36, v156
	ds_read_b128 v[180:183], v244
	ds_read_b128 v[184:187], v244 offset:1024
	ds_read_b128 v[188:191], v244 offset:2048
	ds_read_b128 v[192:195], v244 offset:3072
	ds_read_b128 v[196:199], v147
	ds_read_b128 v[200:203], v147 offset:1024
	ds_read_b128 v[204:207], v147 offset:2048
	ds_read_b128 v[208:211], v147 offset:3072
	ds_read_b128 v[212:215], v147 offset:4096
	ds_read_b128 v[216:219], v147 offset:5120
	ds_read_b128 v[220:223], v147 offset:6144
	ds_read_b128 v[224:227], v147 offset:7168
	s_waitcnt vmcnt(8)
	s_waitcnt lgkmcnt(0)
	s_barrier
	s_waitcnt lgkmcnt(0)
	v_mfma_f32_16x16x32_bf16 v[98:101], v[164:167], v[196:199], v[98:101]
	v_mfma_f32_16x16x32_bf16 v[94:97], v[172:175], v[196:199], v[94:97]
	v_mfma_f32_16x16x32_bf16 v[90:93], v[164:167], v[204:207], v[90:93]
	v_mfma_f32_16x16x32_bf16 v[86:89], v[172:175], v[204:207], v[86:89]
	v_mfma_f32_16x16x32_bf16 v[82:85], v[164:167], v[212:215], v[82:85]
	v_mfma_f32_16x16x32_bf16 v[78:81], v[172:175], v[212:215], v[78:81]
	v_mfma_f32_16x16x32_bf16 v[74:77], v[164:167], v[220:223], v[74:77]
	v_mfma_f32_16x16x32_bf16 v[70:73], v[172:175], v[220:223], v[70:73]
	v_mfma_f32_16x16x32_bf16 v[98:101], v[168:171], v[200:203], v[98:101]
	v_mfma_f32_16x16x32_bf16 v[94:97], v[176:179], v[200:203], v[94:97]
	v_mfma_f32_16x16x32_bf16 v[90:93], v[168:171], v[208:211], v[90:93]
	v_mfma_f32_16x16x32_bf16 v[86:89], v[176:179], v[208:211], v[86:89]
	v_mfma_f32_16x16x32_bf16 v[82:85], v[168:171], v[216:219], v[82:85]
	v_mfma_f32_16x16x32_bf16 v[78:81], v[176:179], v[216:219], v[78:81]
	v_mfma_f32_16x16x32_bf16 v[74:77], v[168:171], v[224:227], v[74:77]
	v_mfma_f32_16x16x32_bf16 v[70:73], v[176:179], v[224:227], v[70:73]
	v_mfma_f32_16x16x32_bf16 v[66:69], v[180:183], v[196:199], v[66:69]
	v_mfma_f32_16x16x32_bf16 v[62:65], v[188:191], v[196:199], v[62:65]
	v_mfma_f32_16x16x32_bf16 v[58:61], v[180:183], v[204:207], v[58:61]
	v_mfma_f32_16x16x32_bf16 v[54:57], v[188:191], v[204:207], v[54:57]
	v_mfma_f32_16x16x32_bf16 v[50:53], v[180:183], v[212:215], v[50:53]
	v_mfma_f32_16x16x32_bf16 v[46:49], v[188:191], v[212:215], v[46:49]
	v_mfma_f32_16x16x32_bf16 v[42:45], v[180:183], v[220:223], v[42:45]
	v_mfma_f32_16x16x32_bf16 v[38:41], v[188:191], v[220:223], v[38:41]
	v_mfma_f32_16x16x32_bf16 v[66:69], v[184:187], v[200:203], v[66:69]
	v_mfma_f32_16x16x32_bf16 v[62:65], v[192:195], v[200:203], v[62:65]
	v_mfma_f32_16x16x32_bf16 v[58:61], v[184:187], v[208:211], v[58:61]
	v_mfma_f32_16x16x32_bf16 v[54:57], v[192:195], v[208:211], v[54:57]
	v_mfma_f32_16x16x32_bf16 v[50:53], v[184:187], v[216:219], v[50:53]
	v_mfma_f32_16x16x32_bf16 v[46:49], v[192:195], v[216:219], v[46:49]
	v_mfma_f32_16x16x32_bf16 v[42:45], v[184:187], v[224:227], v[42:45]
	v_mfma_f32_16x16x32_bf16 v[38:41], v[192:195], v[224:227], v[38:41]
	s_barrier
	s_add_i32 s44, s35, s11
	v_lshl_add_u64 v[230:231], s[22:23], 0, v[130:131]
	s_mov_b32 m0, s44
	global_load_lds_dwordx4 v[230:231], off
	s_add_i32 m0, s44, 0x2000
	s_add_u32 s44, s22, 0x40000
	v_lshl_add_u64 v[232:233], s[22:23], 0, v[132:133]
	s_addc_u32 s45, s23, 0
	s_add_i32 s46, s36, s11
	global_load_lds_dwordx4 v[232:233], off
	v_mov_b32_e32 v229, v135
	s_mov_b32 m0, s28
	v_lshl_add_u64 v[234:235], s[24:25], 0, v[134:135]
	global_load_lds_dwordx4 v134, s[24:25]
	s_mov_b32 m0, s29
	s_nop 0
	global_load_lds_dwordx4 v228, s[24:25]
	v_lshl_add_u64 v[228:229], s[24:25], 0, v[228:229]
	ds_read_b128 v[196:199], v147 offset:16384
	ds_read_b128 v[200:203], v147 offset:17408
	ds_read_b128 v[204:207], v147 offset:18432
	ds_read_b128 v[208:211], v147 offset:19456
	ds_read_b128 v[212:215], v147 offset:20480
	ds_read_b128 v[216:219], v147 offset:21504
	ds_read_b128 v[220:223], v147 offset:22528
	ds_read_b128 v[224:227], v147 offset:23552
	s_waitcnt vmcnt(6)
	s_waitcnt lgkmcnt(0)
	s_barrier
; #define GM_STAGE(bufoff, gbase, voff) do { _Pragma("unroll") for (int _i = 0; _i < 2; ++_i) \
;         __builtin_amdgcn_global_load_lds((const unsigned*)((const char*)(gbase) + (voff)[_i]), (LAS unsigned*)(lds + (bufoff) + ldsw + _i * 8192), 16, 0, 0); } while (0)
; #define GM_LDA(dst, b, h) do { _Pragma("unroll") for (int m = 0; m < 4; ++m) _Pragma("unroll") for (int k = 0; k < 2; ++k) dst[m][k] = *(const LAS s16x8*)(lds + GM_SA(b, h) + aoff + m * 2048 + k * 1024); } while (0)
; #define GM_LDB(dst, b, h) do { _Pragma("unroll") for (int n = 0; n < 2; ++n) _Pragma("unroll") for (int k = 0; k < 2; ++k) dst[n][k] = *(const LAS s16x8*)(lds + GM_SB(b, h) + boff + n * 2048 + k * 1024); } while (0)
; #define GM_MMA(ai, bj, At, Bt) do { __builtin_amdgcn_s_setprio(1); _Pragma("unroll") for (int m = 0; m < 4; ++m) _Pragma("unroll") for (int n = 0; n < 2; ++n) _Pragma("unroll") for (int k = 0; k < 2; ++k) \
;         acc[ai][bj][m][n] = mma16<BF>(Bt[n][k], At[m][k], acc[ai][bj][m][n]); __builtin_amdgcn_s_setprio(0); } while (0)
; #define GM_WAIT_V(n) asm volatile("s_waitcnt vmcnt(" #n ")" ::: "memory")
; #define GM_WAIT_L(n) asm volatile("s_waitcnt lgkmcnt(" #n ")" ::: "memory")
; #define GM_BAR __builtin_amdgcn_s_barrier()
; #define GM_SCHED __builtin_amdgcn_sched_barrier(0)
; #define GM_STA_H0(buf, p, o0) do { if constexpr (GATHER) GM_STAGE(buf, p, o0); else GM_STAGE(buf, p, voffA); } while (0)
; #define GM_STA_H1(buf, p, o1) do { if constexpr (GATHER) GM_STAGE(buf, p, o1); else GM_STAGE(buf, (p) + hstepB, voffA); } while (0)
; template <bool BF, bool GATHER = false, class Epi, class Hook>
; __device__ __forceinline__ void gemm_phase(LAS unsigned char* lds, const Gemm g, const Order& S, const Epi& E, Hook& HK) {
;     ...
;             GM_WAIT_V(8); GM_WAIT_L(0); GM_BAR; GM_MMA(1, 0, At, B0); GM_MMA(1, 1, At, B1); GM_BAR; GM_SCHED;
;             GM_LDB(B0, 1, 0); GM_LDB(B1, 1, 1); GM_SCHED; GM_LDA(At, 1, 0); GM_STA_H1(GM_SA(0, 1), a2, s1);
;             GM_WAIT_V(8); GM_WAIT_L(0); GM_BAR; GM_MMA(0, 0, At, B0); GM_MMA(0, 1, At, B1); GM_BAR; GM_SCHED;
;             GM_LDA(At, 1, 1); GM_STAGE(GM_SB(1, 0), b3, voffB); GM_STAGE(GM_SB(1, 1), b3 + hstepB, voffB); GM_STA_H0(GM_SA(1, 0), a3, s0);
	s_waitcnt lgkmcnt(0)
	v_mfma_f32_16x16x32_bf16 v[34:37], v[164:167], v[196:199], v[34:37]
	v_mfma_f32_16x16x32_bf16 v[30:33], v[172:175], v[196:199], v[30:33]
	v_mfma_f32_16x16x32_bf16 v[26:29], v[164:167], v[204:207], v[26:29]
	v_mfma_f32_16x16x32_bf16 v[22:25], v[172:175], v[204:207], v[22:25]
	v_mfma_f32_16x16x32_bf16 v[18:21], v[164:167], v[212:215], v[18:21]
	v_mfma_f32_16x16x32_bf16 v[14:17], v[172:175], v[212:215], v[14:17]
	v_mfma_f32_16x16x32_bf16 v[10:13], v[164:167], v[220:223], v[10:13]
	v_mfma_f32_16x16x32_bf16 v[6:9], v[172:175], v[220:223], v[6:9]
	v_mfma_f32_16x16x32_bf16 v[34:37], v[168:171], v[200:203], v[34:37]
	v_mfma_f32_16x16x32_bf16 v[30:33], v[176:179], v[200:203], v[30:33]
	v_mfma_f32_16x16x32_bf16 v[26:29], v[168:171], v[208:211], v[26:29]
	v_mfma_f32_16x16x32_bf16 v[22:25], v[176:179], v[208:211], v[22:25]
	v_mfma_f32_16x16x32_bf16 v[18:21], v[168:171], v[216:219], v[18:21]
	v_mfma_f32_16x16x32_bf16 v[14:17], v[176:179], v[216:219], v[14:17]
	v_mfma_f32_16x16x32_bf16 v[10:13], v[168:171], v[224:227], v[10:13]
	v_mfma_f32_16x16x32_bf16 v[6:9], v[176:179], v[224:227], v[6:9]
	v_mfma_f32_16x16x32_bf16 v[2:5], v[180:183], v[196:199], v[2:5]
	v_mfma_f32_16x16x32_bf16 v[102:105], v[188:191], v[196:199], v[102:105]
	v_mfma_f32_16x16x32_bf16 v[106:109], v[180:183], v[204:207], v[106:109]
	v_mfma_f32_16x16x32_bf16 v[110:113], v[188:191], v[204:207], v[110:113]
	v_mfma_f32_16x16x32_bf16 v[114:117], v[180:183], v[212:215], v[114:117]
	v_mfma_f32_16x16x32_bf16 v[118:121], v[188:191], v[212:215], v[118:121]
	v_mfma_f32_16x16x32_bf16 v[122:125], v[180:183], v[220:223], v[122:125]
	v_mfma_f32_16x16x32_bf16 v[126:129], v[188:191], v[220:223], v[126:129]
	v_mfma_f32_16x16x32_bf16 v[2:5], v[184:187], v[200:203], v[2:5]
	v_mfma_f32_16x16x32_bf16 v[102:105], v[192:195], v[200:203], v[102:105]
	v_mfma_f32_16x16x32_bf16 v[106:109], v[184:187], v[208:211], v[106:109]
	v_mfma_f32_16x16x32_bf16 v[110:113], v[192:195], v[208:211], v[110:113]
	v_mfma_f32_16x16x32_bf16 v[114:117], v[184:187], v[216:219], v[114:117]
	v_mfma_f32_16x16x32_bf16 v[118:121], v[192:195], v[216:219], v[118:121]
	v_mfma_f32_16x16x32_bf16 v[122:125], v[184:187], v[224:227], v[122:125]
	v_mfma_f32_16x16x32_bf16 v[126:129], v[192:195], v[224:227], v[126:129]
	s_barrier
	s_add_u32 s98, s22, 0x40000
	s_addc_u32 s99, s23, 0
	v_lshl_add_u64 v[252:253], s[98:99], 0, v[130:131]
	s_add_i32 m0, s11, 0x14000
	s_nop 0
	global_load_lds_dwordx4 v[252:253], off
	v_lshl_add_u64 v[252:253], s[98:99], 0, v[132:133]
	s_add_i32 m0, s11, 0x16000
	s_nop 0
	global_load_lds_dwordx4 v[252:253], off
	s_mov_b32 m0, s30
	global_load_lds_dwordx4 v141, s[24:25]
	s_mov_b32 m0, s31
	s_nop 0
	global_load_lds_dwordx4 v145, s[24:25]
	s_mov_b32 s45, 0x1c000
	s_mov_b32 s44, 0x18000
	v_add_u32_e32 v245, s44, v156
	ds_read_b128 v[164:167], v245
	ds_read_b128 v[168:171], v245 offset:1024
	ds_read_b128 v[172:175], v245 offset:2048
	ds_read_b128 v[176:179], v245 offset:3072
	v_add_u32_e32 v245, s45, v156
	ds_read_b128 v[180:183], v245
	ds_read_b128 v[184:187], v245 offset:1024
	ds_read_b128 v[188:191], v245 offset:2048
	ds_read_b128 v[192:195], v245 offset:3072
	ds_read_b128 v[196:199], v147 offset:32768
	ds_read_b128 v[200:203], v147 offset:33792
	ds_read_b128 v[204:207], v147 offset:34816
	ds_read_b128 v[208:211], v147 offset:35840
	ds_read_b128 v[212:215], v147 offset:36864
	ds_read_b128 v[216:219], v147 offset:37888
	ds_read_b128 v[220:223], v147 offset:38912
	ds_read_b128 v[224:227], v147 offset:39936
	s_waitcnt vmcnt(8)
	s_waitcnt lgkmcnt(0)
	s_barrier
; #define GM_STAGE(bufoff, gbase, voff) do { _Pragma("unroll") for (int _i = 0; _i < 2; ++_i) \
;         __builtin_amdgcn_global_load_lds((const unsigned*)((const char*)(gbase) + (voff)[_i]), (LAS unsigned*)(lds + (bufoff) + ldsw + _i * 8192), 16, 0, 0); } while (0)
; #define GM_LDA(dst, b, h) do { _Pragma("unroll") for (int m = 0; m < 4; ++m) _Pragma("unroll") for (int k = 0; k < 2; ++k) dst[m][k] = *(const LAS s16x8*)(lds + GM_SA(b, h) + aoff + m * 2048 + k * 1024); } while (0)
; #define GM_MMA(ai, bj, At, Bt) do { __builtin_amdgcn_s_setprio(1); _Pragma("unroll") for (int m = 0; m < 4; ++m) _Pragma("unroll") for (int n = 0; n < 2; ++n) _Pragma("unroll") for (int k = 0; k < 2; ++k) \
;         acc[ai][bj][m][n] = mma16<BF>(Bt[n][k], At[m][k], acc[ai][bj][m][n]); __builtin_amdgcn_s_setprio(0); } while (0)
; #define GM_WAIT_V(n) asm volatile("s_waitcnt vmcnt(" #n ")" ::: "memory")
; #define GM_WAIT_L(n) asm volatile("s_waitcnt lgkmcnt(" #n ")" ::: "memory")
; #define GM_BAR __builtin_amdgcn_s_barrier()
; #define GM_SCHED __builtin_amdgcn_sched_barrier(0)
; #define GM_STA_H0(buf, p, o0) do { if constexpr (GATHER) GM_STAGE(buf, p, o0); else GM_STAGE(buf, p, voffA); } while (0)
; template <bool BF, bool GATHER = false, class Epi, class Hook>
; __device__ __forceinline__ void gemm_phase(LAS unsigned char* lds, const Gemm g, const Order& S, const Epi& E, Hook& HK) {
;     ...
;             GM_WAIT_V(8); GM_WAIT_L(0); GM_BAR; GM_MMA(0, 0, At, B0); GM_MMA(0, 1, At, B1); GM_BAR; GM_SCHED;
;             GM_LDA(At, 1, 1); GM_STAGE(GM_SB(1, 0), b3, voffB); GM_STAGE(GM_SB(1, 1), b3 + hstepB, voffB); GM_STA_H0(GM_SA(1, 0), a3, s0);
;             GM_WAIT_V(8); GM_WAIT_L(0); GM_BAR; GM_MMA(1, 0, At, B0); GM_MMA(1, 1, At, B1); GM_BAR; GM_SCHED;
;         }
	s_waitcnt lgkmcnt(0)
	v_mfma_f32_16x16x32_bf16 v[98:101], v[164:167], v[196:199], v[98:101]
	v_mfma_f32_16x16x32_bf16 v[94:97], v[172:175], v[196:199], v[94:97]
	v_mfma_f32_16x16x32_bf16 v[90:93], v[164:167], v[204:207], v[90:93]
	v_mfma_f32_16x16x32_bf16 v[86:89], v[172:175], v[204:207], v[86:89]
	v_mfma_f32_16x16x32_bf16 v[82:85], v[164:167], v[212:215], v[82:85]
	v_mfma_f32_16x16x32_bf16 v[78:81], v[172:175], v[212:215], v[78:81]
	v_mfma_f32_16x16x32_bf16 v[74:77], v[164:167], v[220:223], v[74:77]
	v_mfma_f32_16x16x32_bf16 v[70:73], v[172:175], v[220:223], v[70:73]
	v_mfma_f32_16x16x32_bf16 v[98:101], v[168:171], v[200:203], v[98:101]
	v_mfma_f32_16x16x32_bf16 v[94:97], v[176:179], v[200:203], v[94:97]
	v_mfma_f32_16x16x32_bf16 v[90:93], v[168:171], v[208:211], v[90:93]
	v_mfma_f32_16x16x32_bf16 v[86:89], v[176:179], v[208:211], v[86:89]
	v_mfma_f32_16x16x32_bf16 v[82:85], v[168:171], v[216:219], v[82:85]
	v_mfma_f32_16x16x32_bf16 v[78:81], v[176:179], v[216:219], v[78:81]
	v_mfma_f32_16x16x32_bf16 v[74:77], v[168:171], v[224:227], v[74:77]
	v_mfma_f32_16x16x32_bf16 v[70:73], v[176:179], v[224:227], v[70:73]
	v_mfma_f32_16x16x32_bf16 v[66:69], v[180:183], v[196:199], v[66:69]
	v_mfma_f32_16x16x32_bf16 v[62:65], v[188:191], v[196:199], v[62:65]
	v_mfma_f32_16x16x32_bf16 v[58:61], v[180:183], v[204:207], v[58:61]
	v_mfma_f32_16x16x32_bf16 v[54:57], v[188:191], v[204:207], v[54:57]
	v_mfma_f32_16x16x32_bf16 v[50:53], v[180:183], v[212:215], v[50:53]
	v_mfma_f32_16x16x32_bf16 v[46:49], v[188:191], v[212:215], v[46:49]
	v_mfma_f32_16x16x32_bf16 v[42:45], v[180:183], v[220:223], v[42:45]
	v_mfma_f32_16x16x32_bf16 v[38:41], v[188:191], v[220:223], v[38:41]
	v_mfma_f32_16x16x32_bf16 v[66:69], v[184:187], v[200:203], v[66:69]
	v_mfma_f32_16x16x32_bf16 v[62:65], v[192:195], v[200:203], v[62:65]
	v_mfma_f32_16x16x32_bf16 v[58:61], v[184:187], v[208:211], v[58:61]
	v_mfma_f32_16x16x32_bf16 v[54:57], v[192:195], v[208:211], v[54:57]
	v_mfma_f32_16x16x32_bf16 v[50:53], v[184:187], v[216:219], v[50:53]
	v_mfma_f32_16x16x32_bf16 v[46:49], v[192:195], v[216:219], v[46:49]
	v_mfma_f32_16x16x32_bf16 v[42:45], v[184:187], v[224:227], v[42:45]
	v_mfma_f32_16x16x32_bf16 v[38:41], v[192:195], v[224:227], v[38:41]
	s_barrier
	s_add_i32 s24, s44, s11
	v_lshl_add_u64 v[230:231], v[230:231], 0, s[14:15]
	s_mov_b32 m0, s24
	global_load_lds_dwordx4 v[230:231], off
	s_add_i32 m0, s24, 0x2000
	s_add_u32 s22, s22, 0x40080
	v_lshl_add_u64 v[230:231], v[232:233], 0, s[14:15]
	s_addc_u32 s23, s23, 0
	s_add_i32 s24, s45, s11
	global_load_lds_dwordx4 v[230:231], off
	v_lshl_add_u64 v[228:229], v[228:229], 0, s[14:15]
	v_lshl_add_u64 v[230:231], v[234:235], 0, s[14:15]
	s_mov_b32 m0, s33
	s_nop 0
	global_load_lds_dwordx4 v[230:231], off
	s_mov_b32 m0, s34
	s_nop 0
	global_load_lds_dwordx4 v[228:229], off
	ds_read_b128 v[196:199], v147 offset:49152
	ds_read_b128 v[200:203], v147 offset:50176
	ds_read_b128 v[204:207], v147 offset:51200
	ds_read_b128 v[208:211], v147 offset:52224
	ds_read_b128 v[212:215], v147 offset:53248
	ds_read_b128 v[216:219], v147 offset:54272
	ds_read_b128 v[220:223], v147 offset:55296
	ds_read_b128 v[224:227], v147 offset:56320
	s_waitcnt vmcnt(6)
	s_waitcnt lgkmcnt(0)
	s_barrier
	s_waitcnt lgkmcnt(0)
	v_mfma_f32_16x16x32_bf16 v[34:37], v[164:167], v[196:199], v[34:37]
	v_mfma_f32_16x16x32_bf16 v[30:33], v[172:175], v[196:199], v[30:33]
	v_mfma_f32_16x16x32_bf16 v[26:29], v[164:167], v[204:207], v[26:29]
	v_mfma_f32_16x16x32_bf16 v[22:25], v[172:175], v[204:207], v[22:25]
	v_mfma_f32_16x16x32_bf16 v[18:21], v[164:167], v[212:215], v[18:21]
	v_mfma_f32_16x16x32_bf16 v[14:17], v[172:175], v[212:215], v[14:17]
	v_mfma_f32_16x16x32_bf16 v[10:13], v[164:167], v[220:223], v[10:13]
	v_mfma_f32_16x16x32_bf16 v[6:9], v[172:175], v[220:223], v[6:9]
	v_mfma_f32_16x16x32_bf16 v[34:37], v[168:171], v[200:203], v[34:37]
	v_mfma_f32_16x16x32_bf16 v[30:33], v[176:179], v[200:203], v[30:33]
	v_mfma_f32_16x16x32_bf16 v[26:29], v[168:171], v[208:211], v[26:29]
	v_mfma_f32_16x16x32_bf16 v[22:25], v[176:179], v[208:211], v[22:25]
	v_mfma_f32_16x16x32_bf16 v[18:21], v[168:171], v[216:219], v[18:21]
	v_mfma_f32_16x16x32_bf16 v[14:17], v[176:179], v[216:219], v[14:17]
	v_mfma_f32_16x16x32_bf16 v[10:13], v[168:171], v[224:227], v[10:13]
	v_mfma_f32_16x16x32_bf16 v[6:9], v[176:179], v[224:227], v[6:9]
	v_mfma_f32_16x16x32_bf16 v[2:5], v[180:183], v[196:199], v[2:5]
	v_mfma_f32_16x16x32_bf16 v[102:105], v[188:191], v[196:199], v[102:105]
	v_mfma_f32_16x16x32_bf16 v[106:109], v[180:183], v[204:207], v[106:109]
	v_mfma_f32_16x16x32_bf16 v[110:113], v[188:191], v[204:207], v[110:113]
	v_mfma_f32_16x16x32_bf16 v[114:117], v[180:183], v[212:215], v[114:117]
	v_mfma_f32_16x16x32_bf16 v[118:121], v[188:191], v[212:215], v[118:121]
	v_mfma_f32_16x16x32_bf16 v[122:125], v[180:183], v[220:223], v[122:125]
	v_mfma_f32_16x16x32_bf16 v[126:129], v[188:191], v[220:223], v[126:129]
	v_mfma_f32_16x16x32_bf16 v[2:5], v[184:187], v[200:203], v[2:5]
	v_mfma_f32_16x16x32_bf16 v[102:105], v[192:195], v[200:203], v[102:105]
	v_mfma_f32_16x16x32_bf16 v[106:109], v[184:187], v[208:211], v[106:109]
	v_mfma_f32_16x16x32_bf16 v[110:113], v[192:195], v[208:211], v[110:113]
	v_mfma_f32_16x16x32_bf16 v[114:117], v[184:187], v[216:219], v[114:117]
	v_mfma_f32_16x16x32_bf16 v[118:121], v[192:195], v[216:219], v[118:121]
	v_mfma_f32_16x16x32_bf16 v[122:125], v[184:187], v[224:227], v[122:125]
	v_mfma_f32_16x16x32_bf16 v[126:129], v[192:195], v[224:227], v[126:129]
	s_barrier
	s_add_i32 s43, s43, 2
	s_add_u32 s2, s2, 0x100
	s_addc_u32 s3, s3, 0
	s_cmp_gt_u32 s43, 13
	s_cbranch_scc0 .LBB0_1011
	s_and_b64 vcc, exec, s[18:19]
	s_cbranch_vccz .LBB0_1014
	s_barrier

; #define GM_STAGE(bufoff, gbase, voff) do { _Pragma("unroll") for (int _i = 0; _i < 2; ++_i) \
;         __builtin_amdgcn_global_load_lds((const unsigned*)((const char*)(gbase) + (voff)[_i]), (LAS unsigned*)(lds + (bufoff) + ldsw + _i * 8192), 16, 0, 0); } while (0)
; #define GM_WAIT_V(n) asm volatile("s_waitcnt vmcnt(" #n ")" ::: "memory")
; #define GM_BAR __builtin_amdgcn_s_barrier()
; #define GM_STA_H0(buf, p, o0) do { if constexpr (GATHER) GM_STAGE(buf, p, o0); else GM_STAGE(buf, p, voffA); } while (0)
; #define GM_STA_H1(buf, p, o1) do { if constexpr (GATHER) GM_STAGE(buf, p, o1); else GM_STAGE(buf, (p) + hstepB, voffA); } while (0)
; template <bool BF, bool GATHER = false, class Epi, class Hook>
; __device__ __forceinline__ void gemm_phase(LAS unsigned char* lds, const Gemm g, const Order& S, const Epi& E, Hook& HK) {
;     ...
;     const size_t kstep = (size_t)(BK * 2);
;     const size_t hstep = GATHER ? (size_t)0 : (size_t)HALF * K * 2;
;     const size_t hstepB = (size_t)HALF * K * 2;
;     const size_t tstep = 2 * hstepB;
;     const unsigned ldsw = (unsigned)wid * 1024u;
;     const int aoff = lds_byte(wr * 64 + fr, fq * 8), boff = lds_byte(wc * 32 + fr, fq * 8);
;     ...
;     GM_STAGE(GM_SB(0, 0), cB, voffB); GM_STAGE(GM_SB(0, 1), cB + hstepB, voffB); GM_STA_H0(GM_SA(0, 0), cA, gA0); GM_STA_H1(GM_SA(0, 1), cA, gA1);
;     if (wr == 1) GM_BAR;
;     GM_WAIT_V(2); GM_BAR;
;     GM_STAGE(GM_SB(1, 0), cB + kstep, voffB); GM_STA_H0(GM_SA(1, 0), cA + kstep, gA0); GM_STAGE(GM_SB(1, 1), cB + hstepB + kstep, voffB);
;     GM_WAIT_V(6); GM_BAR;
.LBB0_1085:
	s_lshl_b32 s16, s6, 6
	s_lshl_b32 s14, s6, 13
	s_lshl_b32 s6, s7, 5
	s_mov_b64 s[12:13], 0x80
	s_and_b32 s17, s6, 0x60
	s_add_i32 m0, s29, 0x18000
	v_lshl_add_u64 v[8:9], v[8:9], 0, s[12:13]
	s_lshl_b32 s15, s17, 7
	s_ashr_i32 s35, s92, 31
	s_waitcnt vmcnt(2)
	s_barrier
	global_load_lds_dwordx4 v[8:9], off
	v_lshl_add_u64 v[6:7], v[6:7], 0, s[12:13]
	s_add_i32 m0, s29, 0x1a000
	s_add_i32 s36, s29, 0x8000
	s_add_i32 s37, s29, 0xa000
	global_load_lds_dwordx4 v[6:7], off
	v_lshl_add_u64 v[2:3], v[2:3], 0, s[12:13]
	s_mov_b32 m0, s36
	s_add_u32 s6, s22, 0xb0080
	global_load_lds_dwordx4 v[2:3], off
	v_lshl_add_u64 v[2:3], v[4:5], 0, s[12:13]
	s_mov_b32 m0, s37
	s_addc_u32 s7, s23, 0
	global_load_lds_dwordx4 v[2:3], off
	v_lshlrev_b32_e32 v5, 2, v10
	v_lshrrev_b32_e32 v3, 1, v10
	v_and_b32_e32 v3, 24, v3
	v_and_b32_e32 v2, 15, v10
	v_lshlrev_b32_e32 v4, 1, v3
	v_lshl_or_b32 v4, v2, 6, v4
	v_and_b32_e32 v5, 32, v5
	s_cmpk_lt_u32 s4, 0x100
	v_bitop3_b32 v6, v4, s14, v5 bitop3:0xde
	v_bitop3_b32 v150, v4, s15, v5 bitop3:0xde
	s_cselect_b64 s[14:15], -1, 0
	s_lshl_b32 s4, s92, 3
	v_mov_b32_e32 v4, 0xcf
	s_and_b32 s40, s4, 8
	s_ashr_i32 s4, s92, 5
	v_or_b32_e32 v1, s16, v2
	v_bitop3_b32 v151, s16, v4, v2 bitop3:0xc8
	s_add_i32 s40, s40, s4
	v_or_b32_e32 v152, s17, v3
	v_lshrrev_b32_e32 v3, 1, v11
	v_mul_lo_u32 v2, v13, s5
	s_mov_b32 s4, 0xb000
	v_mad_u64_u32 v[2:3], s[16:17], v3, s4, v[2:3]
	v_or_b32_e32 v2, v2, v12
	s_mov_b64 s[6:7], 0xb0080
	v_add_lshl_u32 v2, v2, v14, 1
	v_mov_b32_e32 v3, v133
	v_lshl_add_u64 v[138:139], v[2:3], 0, s[6:7]
	v_lshrrev_b32_e32 v3, 1, v15
	v_mul_lo_u32 v2, v16, s5
	v_mad_u64_u32 v[2:3], s[4:5], v3, s4, v[2:3]
	s_waitcnt vmcnt(4)
	v_or_b32_e32 v2, v2, v17
	v_add_lshl_u32 v2, v2, v18, 1
	v_mov_b32_e32 v3, v133
	s_add_i32 s42, 0, 0x10000
	s_add_i32 s43, 0, 0x14000
	s_ashr_i32 s38, s96, 31
	s_bfe_u32 s39, s92, 0x20001
	s_bfe_u32 s41, s92, 0x20003
	v_lshl_add_u64 v[140:141], v[2:3], 0, s[6:7]
	v_mov_b64_e32 v[142:143], 0x400
	v_mov_b64_e32 v[144:145], 0x3ff
	v_add_u32_e32 v153, s42, v150
	v_add_u32_e32 v154, s43, v150
	v_add_u32_e32 v155, 0, v6
	s_movk_i32 s44, 0xdf
	s_movk_i32 s45, 0xef
	s_movk_i32 s46, 0xff
	s_barrier
	s_branch .LBB0_1088

; #define GM_STAGE(bufoff, gbase, voff) do { _Pragma("unroll") for (int _i = 0; _i < 2; ++_i) \
;         __builtin_amdgcn_global_load_lds((const unsigned*)((const char*)(gbase) + (voff)[_i]), (LAS unsigned*)(lds + (bufoff) + ldsw + _i * 8192), 16, 0, 0); } while (0)
; #define GM_LDA(dst, b, h) do { _Pragma("unroll") for (int m = 0; m < 4; ++m) _Pragma("unroll") for (int k = 0; k < 2; ++k) dst[m][k] = *(const LAS s16x8*)(lds + GM_SA(b, h) + aoff + m * 2048 + k * 1024); } while (0)
; #define GM_LDB(dst, b, h) do { _Pragma("unroll") for (int n = 0; n < 2; ++n) _Pragma("unroll") for (int k = 0; k < 2; ++k) dst[n][k] = *(const LAS s16x8*)(lds + GM_SB(b, h) + boff + n * 2048 + k * 1024); } while (0)
; #define GM_MMA(ai, bj, At, Bt) do { __builtin_amdgcn_s_setprio(1); _Pragma("unroll") for (int m = 0; m < 4; ++m) _Pragma("unroll") for (int n = 0; n < 2; ++n) _Pragma("unroll") for (int k = 0; k < 2; ++k) \
;         acc[ai][bj][m][n] = mma16<BF>(Bt[n][k], At[m][k], acc[ai][bj][m][n]); __builtin_amdgcn_s_setprio(0); } while (0)
; #define GM_WAIT_V(n) asm volatile("s_waitcnt vmcnt(" #n ")" ::: "memory")
; #define GM_WAIT_L(n) asm volatile("s_waitcnt lgkmcnt(" #n ")" ::: "memory")
; #define GM_BAR __builtin_amdgcn_s_barrier()
; #define GM_SCHED __builtin_amdgcn_sched_barrier(0)
; #define GM_STA_H0(buf, p, o0) do { if constexpr (GATHER) GM_STAGE(buf, p, o0); else GM_STAGE(buf, p, voffA); } while (0)
; #define GM_STA_H1(buf, p, o1) do { if constexpr (GATHER) GM_STAGE(buf, p, o1); else GM_STAGE(buf, (p) + hstepB, voffA); } while (0)
; template <bool BF, bool GATHER = false, class Epi, class Hook>
; __device__ __forceinline__ void gemm_phase(LAS unsigned char* lds, const Gemm g, const Order& S, const Epi& E, Hook& HK) {
;     ...
;             GM_LDB(B0, 0, 0); GM_LDB(B1, 0, 1); GM_SCHED; GM_LDA(At, 0, 0); GM_STA_H1(GM_SA(1, 1), a1, gA1);
;             GM_WAIT_V(8); GM_WAIT_L(0); GM_BAR; GM_MMA(0, 0, At, B0); GM_MMA(0, 1, At, B1); GM_BAR; GM_SCHED;
;             GM_LDA(At, 0, 1); GM_STAGE(GM_SB(0, 0), b2, voffB); GM_STAGE(GM_SB(0, 1), b2 + hstepB, voffB); GM_STA_H0(GM_SA(0, 0), a2, s0);
;             GM_WAIT_V(8); GM_WAIT_L(0); GM_BAR; GM_MMA(1, 0, At, B0); GM_MMA(1, 1, At, B1); GM_BAR; GM_SCHED;
.LBB0_1102:
	s_add_u32 s22, s2, 0x100
	s_addc_u32 s23, s3, 0
	s_cmp_eq_u32 s51, 40
	s_cselect_b32 s27, s7, s23
	s_cselect_b32 s26, s6, s22
	s_cselect_b32 s25, s21, s50
	s_cselect_b32 s24, s20, s49
	s_add_u32 s98, s49, 0xaff80
	s_addc_u32 s99, s50, 0
	v_lshl_add_u64 v[252:253], s[98:99], 0, v[132:133]
	s_add_i32 m0, s28, 0x1c000
	s_nop 0
	global_load_lds_dwordx4 v[252:253], off
	v_lshl_add_u64 v[252:253], s[98:99], 0, v[136:137]
	s_add_i32 m0, s28, 0x1e000
	s_nop 0
	global_load_lds_dwordx4 v[252:253], off
	v_lshl_add_u64 v[216:217], s[2:3], 0, v[138:139]
	s_add_i32 m0, s29, 0xc000
	global_load_lds_dwordx4 v[216:217], off
	v_lshl_add_u64 v[216:217], s[2:3], 0, v[140:141]
	s_add_i32 m0, s29, 0xe000
	s_nop 0
	global_load_lds_dwordx4 v[216:217], off
	ds_read_b128 v[146:149], v153
	ds_read_b128 v[156:159], v153 offset:1024
	ds_read_b128 v[160:163], v153 offset:2048
	ds_read_b128 v[164:167], v153 offset:3072
	ds_read_b128 v[168:171], v154
	ds_read_b128 v[172:175], v154 offset:1024
	ds_read_b128 v[176:179], v154 offset:2048
	ds_read_b128 v[180:183], v154 offset:3072
	ds_read_b128 v[184:187], v155
	ds_read_b128 v[188:191], v155 offset:1024
	ds_read_b128 v[192:195], v155 offset:2048
	ds_read_b128 v[196:199], v155 offset:3072
	ds_read_b128 v[200:203], v155 offset:4096
	ds_read_b128 v[204:207], v155 offset:5120
	ds_read_b128 v[208:211], v155 offset:6144
	ds_read_b128 v[212:215], v155 offset:7168
	s_waitcnt vmcnt(8)
	s_waitcnt lgkmcnt(0)
	s_barrier
	s_waitcnt lgkmcnt(0)
	v_mfma_f32_16x16x32_bf16 v[126:129], v[146:149], v[184:187], v[126:129]
	v_mfma_f32_16x16x32_bf16 v[122:125], v[160:163], v[184:187], v[122:125]
	v_mfma_f32_16x16x32_bf16 v[110:113], v[146:149], v[192:195], v[110:113]
	v_mfma_f32_16x16x32_bf16 v[106:109], v[160:163], v[192:195], v[106:109]
	v_mfma_f32_16x16x32_bf16 v[94:97], v[146:149], v[200:203], v[94:97]
	v_mfma_f32_16x16x32_bf16 v[90:93], v[160:163], v[200:203], v[90:93]
	v_mfma_f32_16x16x32_bf16 v[78:81], v[146:149], v[208:211], v[78:81]
	v_mfma_f32_16x16x32_bf16 v[74:77], v[160:163], v[208:211], v[74:77]
	v_mfma_f32_16x16x32_bf16 v[126:129], v[156:159], v[188:191], v[126:129]
	v_mfma_f32_16x16x32_bf16 v[122:125], v[164:167], v[188:191], v[122:125]
	v_mfma_f32_16x16x32_bf16 v[110:113], v[156:159], v[196:199], v[110:113]
	v_mfma_f32_16x16x32_bf16 v[106:109], v[164:167], v[196:199], v[106:109]
	v_mfma_f32_16x16x32_bf16 v[94:97], v[156:159], v[204:207], v[94:97]
	v_mfma_f32_16x16x32_bf16 v[90:93], v[164:167], v[204:207], v[90:93]
	v_mfma_f32_16x16x32_bf16 v[78:81], v[156:159], v[212:215], v[78:81]
	v_mfma_f32_16x16x32_bf16 v[74:77], v[164:167], v[212:215], v[74:77]
	v_mfma_f32_16x16x32_bf16 v[118:121], v[168:171], v[184:187], v[118:121]
	v_mfma_f32_16x16x32_bf16 v[114:117], v[176:179], v[184:187], v[114:117]
	v_mfma_f32_16x16x32_bf16 v[102:105], v[168:171], v[192:195], v[102:105]
	v_mfma_f32_16x16x32_bf16 v[98:101], v[176:179], v[192:195], v[98:101]
	v_mfma_f32_16x16x32_bf16 v[86:89], v[168:171], v[200:203], v[86:89]
	v_mfma_f32_16x16x32_bf16 v[82:85], v[176:179], v[200:203], v[82:85]
	v_mfma_f32_16x16x32_bf16 v[70:73], v[168:171], v[208:211], v[70:73]
	v_mfma_f32_16x16x32_bf16 v[66:69], v[176:179], v[208:211], v[66:69]
	v_mfma_f32_16x16x32_bf16 v[118:121], v[172:175], v[188:191], v[118:121]
	v_mfma_f32_16x16x32_bf16 v[114:117], v[180:183], v[188:191], v[114:117]
	v_mfma_f32_16x16x32_bf16 v[102:105], v[172:175], v[196:199], v[102:105]
	v_mfma_f32_16x16x32_bf16 v[98:101], v[180:183], v[196:199], v[98:101]
	v_mfma_f32_16x16x32_bf16 v[86:89], v[172:175], v[204:207], v[86:89]
	v_mfma_f32_16x16x32_bf16 v[82:85], v[180:183], v[204:207], v[82:85]
	v_mfma_f32_16x16x32_bf16 v[70:73], v[172:175], v[212:215], v[70:73]
	v_mfma_f32_16x16x32_bf16 v[66:69], v[180:183], v[212:215], v[66:69]
	s_barrier
	s_add_i32 s2, s42, s28
	v_lshl_add_u64 v[216:217], s[24:25], 0, v[132:133]
	s_mov_b32 m0, s2
	global_load_lds_dwordx4 v[216:217], off
	s_add_i32 m0, s2, 0x2000
	s_add_u32 s2, s24, 0xb0000
	v_lshl_add_u64 v[218:219], s[24:25], 0, v[136:137]
	s_addc_u32 s3, s25, 0
	s_add_i32 s52, s43, s28
	global_load_lds_dwordx4 v[218:219], off
	v_lshl_add_u64 v[222:223], s[26:27], 0, v[134:135]
	v_lshl_add_u64 v[220:221], s[26:27], 0, v[130:131]
	s_mov_b32 m0, s29
	s_nop 0
	global_load_lds_dwordx4 v[220:221], off
	s_mov_b32 m0, s30
	s_nop 0
	global_load_lds_dwordx4 v[222:223], off
	ds_read_b128 v[184:187], v155 offset:16384
	ds_read_b128 v[188:191], v155 offset:17408
	ds_read_b128 v[192:195], v155 offset:18432
	ds_read_b128 v[196:199], v155 offset:19456
	ds_read_b128 v[200:203], v155 offset:20480
	ds_read_b128 v[204:207], v155 offset:21504
	ds_read_b128 v[208:211], v155 offset:22528
	ds_read_b128 v[212:215], v155 offset:23552
	s_waitcnt vmcnt(6)
	s_waitcnt lgkmcnt(0)
	s_barrier
; #define GM_STAGE(bufoff, gbase, voff) do { _Pragma("unroll") for (int _i = 0; _i < 2; ++_i) \
;         __builtin_amdgcn_global_load_lds((const unsigned*)((const char*)(gbase) + (voff)[_i]), (LAS unsigned*)(lds + (bufoff) + ldsw + _i * 8192), 16, 0, 0); } while (0)
; #define GM_LDA(dst, b, h) do { _Pragma("unroll") for (int m = 0; m < 4; ++m) _Pragma("unroll") for (int k = 0; k < 2; ++k) dst[m][k] = *(const LAS s16x8*)(lds + GM_SA(b, h) + aoff + m * 2048 + k * 1024); } while (0)
; #define GM_LDB(dst, b, h) do { _Pragma("unroll") for (int n = 0; n < 2; ++n) _Pragma("unroll") for (int k = 0; k < 2; ++k) dst[n][k] = *(const LAS s16x8*)(lds + GM_SB(b, h) + boff + n * 2048 + k * 1024); } while (0)
; #define GM_MMA(ai, bj, At, Bt) do { __builtin_amdgcn_s_setprio(1); _Pragma("unroll") for (int m = 0; m < 4; ++m) _Pragma("unroll") for (int n = 0; n < 2; ++n) _Pragma("unroll") for (int k = 0; k < 2; ++k) \
;         acc[ai][bj][m][n] = mma16<BF>(Bt[n][k], At[m][k], acc[ai][bj][m][n]); __builtin_amdgcn_s_setprio(0); } while (0)
; #define GM_WAIT_V(n) asm volatile("s_waitcnt vmcnt(" #n ")" ::: "memory")
; #define GM_WAIT_L(n) asm volatile("s_waitcnt lgkmcnt(" #n ")" ::: "memory")
; #define GM_BAR __builtin_amdgcn_s_barrier()
; #define GM_SCHED __builtin_amdgcn_sched_barrier(0)
; #define GM_STA_H0(buf, p, o0) do { if constexpr (GATHER) GM_STAGE(buf, p, o0); else GM_STAGE(buf, p, voffA); } while (0)
; #define GM_STA_H1(buf, p, o1) do { if constexpr (GATHER) GM_STAGE(buf, p, o1); else GM_STAGE(buf, (p) + hstepB, voffA); } while (0)
; template <bool BF, bool GATHER = false, class Epi, class Hook>
; __device__ __forceinline__ void gemm_phase(LAS unsigned char* lds, const Gemm g, const Order& S, const Epi& E, Hook& HK) {
;     ...
;             GM_WAIT_V(8); GM_WAIT_L(0); GM_BAR; GM_MMA(1, 0, At, B0); GM_MMA(1, 1, At, B1); GM_BAR; GM_SCHED;
;             GM_LDB(B0, 1, 0); GM_LDB(B1, 1, 1); GM_SCHED; GM_LDA(At, 1, 0); GM_STA_H1(GM_SA(0, 1), a2, s1);
;             GM_WAIT_V(8); GM_WAIT_L(0); GM_BAR; GM_MMA(0, 0, At, B0); GM_MMA(0, 1, At, B1); GM_BAR; GM_SCHED;
;             GM_LDA(At, 1, 1); GM_STAGE(GM_SB(1, 0), b3, voffB); GM_STAGE(GM_SB(1, 1), b3 + hstepB, voffB); GM_STA_H0(GM_SA(1, 0), a3, s0);
	s_waitcnt lgkmcnt(0)
	v_mfma_f32_16x16x32_bf16 v[62:65], v[146:149], v[184:187], v[62:65]
	v_mfma_f32_16x16x32_bf16 v[58:61], v[160:163], v[184:187], v[58:61]
	v_mfma_f32_16x16x32_bf16 v[46:49], v[146:149], v[192:195], v[46:49]
	v_mfma_f32_16x16x32_bf16 v[42:45], v[160:163], v[192:195], v[42:45]
	v_mfma_f32_16x16x32_bf16 v[30:33], v[146:149], v[200:203], v[30:33]
	v_mfma_f32_16x16x32_bf16 v[26:29], v[160:163], v[200:203], v[26:29]
	v_mfma_f32_16x16x32_bf16 v[14:17], v[146:149], v[208:211], v[14:17]
	v_mfma_f32_16x16x32_bf16 v[10:13], v[160:163], v[208:211], v[10:13]
	v_mfma_f32_16x16x32_bf16 v[62:65], v[156:159], v[188:191], v[62:65]
	v_mfma_f32_16x16x32_bf16 v[58:61], v[164:167], v[188:191], v[58:61]
	v_mfma_f32_16x16x32_bf16 v[46:49], v[156:159], v[196:199], v[46:49]
	v_mfma_f32_16x16x32_bf16 v[42:45], v[164:167], v[196:199], v[42:45]
	v_mfma_f32_16x16x32_bf16 v[30:33], v[156:159], v[204:207], v[30:33]
	v_mfma_f32_16x16x32_bf16 v[26:29], v[164:167], v[204:207], v[26:29]
	v_mfma_f32_16x16x32_bf16 v[14:17], v[156:159], v[212:215], v[14:17]
	v_mfma_f32_16x16x32_bf16 v[10:13], v[164:167], v[212:215], v[10:13]
	v_mfma_f32_16x16x32_bf16 v[54:57], v[168:171], v[184:187], v[54:57]
	v_mfma_f32_16x16x32_bf16 v[50:53], v[176:179], v[184:187], v[50:53]
	v_mfma_f32_16x16x32_bf16 v[38:41], v[168:171], v[192:195], v[38:41]
	v_mfma_f32_16x16x32_bf16 v[34:37], v[176:179], v[192:195], v[34:37]
	v_mfma_f32_16x16x32_bf16 v[22:25], v[168:171], v[200:203], v[22:25]
	v_mfma_f32_16x16x32_bf16 v[18:21], v[176:179], v[200:203], v[18:21]
	v_mfma_f32_16x16x32_bf16 v[6:9], v[168:171], v[208:211], v[6:9]
	v_mfma_f32_16x16x32_bf16 v[2:5], v[176:179], v[208:211], v[2:5]
	v_mfma_f32_16x16x32_bf16 v[54:57], v[172:175], v[188:191], v[54:57]
	v_mfma_f32_16x16x32_bf16 v[50:53], v[180:183], v[188:191], v[50:53]
	v_mfma_f32_16x16x32_bf16 v[38:41], v[172:175], v[196:199], v[38:41]
	v_mfma_f32_16x16x32_bf16 v[34:37], v[180:183], v[196:199], v[34:37]
	v_mfma_f32_16x16x32_bf16 v[22:25], v[172:175], v[204:207], v[22:25]
	v_mfma_f32_16x16x32_bf16 v[18:21], v[180:183], v[204:207], v[18:21]
	v_mfma_f32_16x16x32_bf16 v[6:9], v[172:175], v[212:215], v[6:9]
	v_mfma_f32_16x16x32_bf16 v[2:5], v[180:183], v[212:215], v[2:5]
	s_barrier
	s_add_u32 s2, s26, 0xb0000
	s_addc_u32 s3, s27, 0
	s_add_u32 s98, s24, 0xb0000
	s_addc_u32 s99, s25, 0
	v_lshl_add_u64 v[252:253], s[98:99], 0, v[132:133]
	s_add_i32 m0, s28, 0x14000
	s_nop 0
	global_load_lds_dwordx4 v[252:253], off
	v_lshl_add_u64 v[252:253], s[98:99], 0, v[136:137]
	s_add_i32 m0, s28, 0x16000
	s_nop 0
	global_load_lds_dwordx4 v[252:253], off
	s_mov_b32 m0, s31
	v_lshl_add_u64 v[224:225], s[2:3], 0, v[130:131]
	global_load_lds_dwordx4 v[224:225], off
	v_lshl_add_u64 v[224:225], s[2:3], 0, v[134:135]
	s_mov_b32 m0, s33
	s_nop 0
	global_load_lds_dwordx4 v[224:225], off
	s_mov_b32 s53, 0x1c000
	s_mov_b32 s52, 0x18000
	v_add_u32_e32 v244, s52, v150
	v_add_u32_e32 v245, s53, v150
	ds_read_b128 v[146:149], v244
	ds_read_b128 v[156:159], v244 offset:1024
	ds_read_b128 v[160:163], v244 offset:2048
	ds_read_b128 v[164:167], v244 offset:3072
	ds_read_b128 v[168:171], v245
	ds_read_b128 v[172:175], v245 offset:1024
	ds_read_b128 v[176:179], v245 offset:2048
	ds_read_b128 v[180:183], v245 offset:3072
	ds_read_b128 v[184:187], v155 offset:32768
	ds_read_b128 v[188:191], v155 offset:33792
	ds_read_b128 v[192:195], v155 offset:34816
	ds_read_b128 v[196:199], v155 offset:35840
	ds_read_b128 v[200:203], v155 offset:36864
	ds_read_b128 v[204:207], v155 offset:37888
	ds_read_b128 v[208:211], v155 offset:38912
	ds_read_b128 v[212:215], v155 offset:39936
	s_waitcnt vmcnt(8)
	s_waitcnt lgkmcnt(0)
	s_barrier
; #define GM_STAGE(bufoff, gbase, voff) do { _Pragma("unroll") for (int _i = 0; _i < 2; ++_i) \
;         __builtin_amdgcn_global_load_lds((const unsigned*)((const char*)(gbase) + (voff)[_i]), (LAS unsigned*)(lds + (bufoff) + ldsw + _i * 8192), 16, 0, 0); } while (0)
; #define GM_LDA(dst, b, h) do { _Pragma("unroll") for (int m = 0; m < 4; ++m) _Pragma("unroll") for (int k = 0; k < 2; ++k) dst[m][k] = *(const LAS s16x8*)(lds + GM_SA(b, h) + aoff + m * 2048 + k * 1024); } while (0)
; #define GM_MMA(ai, bj, At, Bt) do { __builtin_amdgcn_s_setprio(1); _Pragma("unroll") for (int m = 0; m < 4; ++m) _Pragma("unroll") for (int n = 0; n < 2; ++n) _Pragma("unroll") for (int k = 0; k < 2; ++k) \
;         acc[ai][bj][m][n] = mma16<BF>(Bt[n][k], At[m][k], acc[ai][bj][m][n]); __builtin_amdgcn_s_setprio(0); } while (0)
; #define GM_WAIT_V(n) asm volatile("s_waitcnt vmcnt(" #n ")" ::: "memory")
; #define GM_WAIT_L(n) asm volatile("s_waitcnt lgkmcnt(" #n ")" ::: "memory")
; #define GM_BAR __builtin_amdgcn_s_barrier()
; #define GM_SCHED __builtin_amdgcn_sched_barrier(0)
; #define GM_STA_H0(buf, p, o0) do { if constexpr (GATHER) GM_STAGE(buf, p, o0); else GM_STAGE(buf, p, voffA); } while (0)
; template <bool BF, bool GATHER = false, class Epi, class Hook>
; __device__ __forceinline__ void gemm_phase(LAS unsigned char* lds, const Gemm g, const Order& S, const Epi& E, Hook& HK) {
;     ...
;             GM_WAIT_V(8); GM_WAIT_L(0); GM_BAR; GM_MMA(0, 0, At, B0); GM_MMA(0, 1, At, B1); GM_BAR; GM_SCHED;
;             GM_LDA(At, 1, 1); GM_STAGE(GM_SB(1, 0), b3, voffB); GM_STAGE(GM_SB(1, 1), b3 + hstepB, voffB); GM_STA_H0(GM_SA(1, 0), a3, s0);
;             GM_WAIT_V(8); GM_WAIT_L(0); GM_BAR; GM_MMA(1, 0, At, B0); GM_MMA(1, 1, At, B1); GM_BAR; GM_SCHED;
;         }
	s_waitcnt lgkmcnt(0)
	v_mfma_f32_16x16x32_bf16 v[126:129], v[146:149], v[184:187], v[126:129]
	v_mfma_f32_16x16x32_bf16 v[122:125], v[160:163], v[184:187], v[122:125]
	v_mfma_f32_16x16x32_bf16 v[110:113], v[146:149], v[192:195], v[110:113]
	v_mfma_f32_16x16x32_bf16 v[106:109], v[160:163], v[192:195], v[106:109]
	v_mfma_f32_16x16x32_bf16 v[94:97], v[146:149], v[200:203], v[94:97]
	v_mfma_f32_16x16x32_bf16 v[90:93], v[160:163], v[200:203], v[90:93]
	v_mfma_f32_16x16x32_bf16 v[78:81], v[146:149], v[208:211], v[78:81]
	v_mfma_f32_16x16x32_bf16 v[74:77], v[160:163], v[208:211], v[74:77]
	v_mfma_f32_16x16x32_bf16 v[126:129], v[156:159], v[188:191], v[126:129]
	v_mfma_f32_16x16x32_bf16 v[122:125], v[164:167], v[188:191], v[122:125]
	v_mfma_f32_16x16x32_bf16 v[110:113], v[156:159], v[196:199], v[110:113]
	v_mfma_f32_16x16x32_bf16 v[106:109], v[164:167], v[196:199], v[106:109]
	v_mfma_f32_16x16x32_bf16 v[94:97], v[156:159], v[204:207], v[94:97]
	v_mfma_f32_16x16x32_bf16 v[90:93], v[164:167], v[204:207], v[90:93]
	v_mfma_f32_16x16x32_bf16 v[78:81], v[156:159], v[212:215], v[78:81]
	v_mfma_f32_16x16x32_bf16 v[74:77], v[164:167], v[212:215], v[74:77]
	v_mfma_f32_16x16x32_bf16 v[118:121], v[168:171], v[184:187], v[118:121]
	v_mfma_f32_16x16x32_bf16 v[114:117], v[176:179], v[184:187], v[114:117]
	v_mfma_f32_16x16x32_bf16 v[102:105], v[168:171], v[192:195], v[102:105]
	v_mfma_f32_16x16x32_bf16 v[98:101], v[176:179], v[192:195], v[98:101]
	v_mfma_f32_16x16x32_bf16 v[86:89], v[168:171], v[200:203], v[86:89]
	v_mfma_f32_16x16x32_bf16 v[82:85], v[176:179], v[200:203], v[82:85]
	v_mfma_f32_16x16x32_bf16 v[70:73], v[168:171], v[208:211], v[70:73]
	v_mfma_f32_16x16x32_bf16 v[66:69], v[176:179], v[208:211], v[66:69]
	v_mfma_f32_16x16x32_bf16 v[118:121], v[172:175], v[188:191], v[118:121]
	v_mfma_f32_16x16x32_bf16 v[114:117], v[180:183], v[188:191], v[114:117]
	v_mfma_f32_16x16x32_bf16 v[102:105], v[172:175], v[196:199], v[102:105]
	v_mfma_f32_16x16x32_bf16 v[98:101], v[180:183], v[196:199], v[98:101]
	v_mfma_f32_16x16x32_bf16 v[86:89], v[172:175], v[204:207], v[86:89]
	v_mfma_f32_16x16x32_bf16 v[82:85], v[180:183], v[204:207], v[82:85]
	v_mfma_f32_16x16x32_bf16 v[70:73], v[172:175], v[212:215], v[70:73]
	v_mfma_f32_16x16x32_bf16 v[66:69], v[180:183], v[212:215], v[66:69]
	s_barrier
	s_add_i32 s2, s52, s28
	v_lshl_add_u64 v[216:217], v[216:217], 0, s[12:13]
	s_mov_b32 m0, s2
	global_load_lds_dwordx4 v[216:217], off
	s_add_i32 m0, s2, 0x2000
	s_add_u32 s2, s24, 0xb0080
	v_lshl_add_u64 v[216:217], v[218:219], 0, s[12:13]
	s_addc_u32 s3, s25, 0
	s_add_i32 s24, s53, s28
	global_load_lds_dwordx4 v[216:217], off
	v_lshl_add_u64 v[216:217], v[220:221], 0, s[12:13]
	s_mov_b32 m0, s36
	s_nop 0
	global_load_lds_dwordx4 v[216:217], off
	v_lshl_add_u64 v[216:217], v[222:223], 0, s[12:13]
	s_mov_b32 m0, s37
	s_nop 0
	global_load_lds_dwordx4 v[216:217], off
	ds_read_b128 v[184:187], v155 offset:49152
	ds_read_b128 v[188:191], v155 offset:50176
	ds_read_b128 v[192:195], v155 offset:51200
	ds_read_b128 v[196:199], v155 offset:52224
	ds_read_b128 v[200:203], v155 offset:53248
	ds_read_b128 v[204:207], v155 offset:54272
	ds_read_b128 v[208:211], v155 offset:55296
	ds_read_b128 v[212:215], v155 offset:56320
	s_waitcnt vmcnt(6)
	s_waitcnt lgkmcnt(0)
	s_barrier
	s_waitcnt lgkmcnt(0)
	v_mfma_f32_16x16x32_bf16 v[62:65], v[146:149], v[184:187], v[62:65]
	v_mfma_f32_16x16x32_bf16 v[58:61], v[160:163], v[184:187], v[58:61]
	v_mfma_f32_16x16x32_bf16 v[46:49], v[146:149], v[192:195], v[46:49]
	v_mfma_f32_16x16x32_bf16 v[42:45], v[160:163], v[192:195], v[42:45]
	v_mfma_f32_16x16x32_bf16 v[30:33], v[146:149], v[200:203], v[30:33]
	v_mfma_f32_16x16x32_bf16 v[26:29], v[160:163], v[200:203], v[26:29]
	v_mfma_f32_16x16x32_bf16 v[14:17], v[146:149], v[208:211], v[14:17]
	v_mfma_f32_16x16x32_bf16 v[10:13], v[160:163], v[208:211], v[10:13]
	v_mfma_f32_16x16x32_bf16 v[62:65], v[156:159], v[188:191], v[62:65]
	v_mfma_f32_16x16x32_bf16 v[58:61], v[164:167], v[188:191], v[58:61]
	v_mfma_f32_16x16x32_bf16 v[46:49], v[156:159], v[196:199], v[46:49]
	v_mfma_f32_16x16x32_bf16 v[42:45], v[164:167], v[196:199], v[42:45]
	v_mfma_f32_16x16x32_bf16 v[30:33], v[156:159], v[204:207], v[30:33]
	v_mfma_f32_16x16x32_bf16 v[26:29], v[164:167], v[204:207], v[26:29]
	v_mfma_f32_16x16x32_bf16 v[14:17], v[156:159], v[212:215], v[14:17]
	v_mfma_f32_16x16x32_bf16 v[10:13], v[164:167], v[212:215], v[10:13]
	v_mfma_f32_16x16x32_bf16 v[54:57], v[168:171], v[184:187], v[54:57]
	v_mfma_f32_16x16x32_bf16 v[50:53], v[176:179], v[184:187], v[50:53]
	v_mfma_f32_16x16x32_bf16 v[38:41], v[168:171], v[192:195], v[38:41]
	v_mfma_f32_16x16x32_bf16 v[34:37], v[176:179], v[192:195], v[34:37]
	v_mfma_f32_16x16x32_bf16 v[22:25], v[168:171], v[200:203], v[22:25]
	v_mfma_f32_16x16x32_bf16 v[18:21], v[176:179], v[200:203], v[18:21]
	v_mfma_f32_16x16x32_bf16 v[6:9], v[168:171], v[208:211], v[6:9]
	v_mfma_f32_16x16x32_bf16 v[2:5], v[176:179], v[208:211], v[2:5]
	v_mfma_f32_16x16x32_bf16 v[54:57], v[172:175], v[188:191], v[54:57]
	v_mfma_f32_16x16x32_bf16 v[50:53], v[180:183], v[188:191], v[50:53]
	v_mfma_f32_16x16x32_bf16 v[38:41], v[172:175], v[196:199], v[38:41]
	v_mfma_f32_16x16x32_bf16 v[34:37], v[180:183], v[196:199], v[34:37]
	v_mfma_f32_16x16x32_bf16 v[22:25], v[172:175], v[204:207], v[22:25]
	v_mfma_f32_16x16x32_bf16 v[18:21], v[180:183], v[204:207], v[18:21]
	v_mfma_f32_16x16x32_bf16 v[6:9], v[172:175], v[212:215], v[6:9]
	v_mfma_f32_16x16x32_bf16 v[2:5], v[180:183], v[212:215], v[2:5]
	s_barrier
	s_add_i32 s51, s51, 2
	s_add_u32 s49, s49, 0x100
	s_addc_u32 s50, s50, 0
	s_cmp_gt_u32 s51, 41
	s_mov_b64 s[2:3], s[22:23]
	s_cbranch_scc0 .LBB0_1102
	s_and_b64 vcc, exec, s[14:15]
	s_cbranch_vccz .LBB0_1105
	s_barrier

; #define GM_STAGE(bufoff, gbase, voff) do { _Pragma("unroll") for (int _i = 0; _i < 2; ++_i) \
;         __builtin_amdgcn_global_load_lds((const unsigned*)((const char*)(gbase) + (voff)[_i]), (LAS unsigned*)(lds + (bufoff) + ldsw + _i * 8192), 16, 0, 0); } while (0)
; #define GM_WAIT_V(n) asm volatile("s_waitcnt vmcnt(" #n ")" ::: "memory")
; #define GM_BAR __builtin_amdgcn_s_barrier()
; #define GM_STA_H0(buf, p, o0) do { if constexpr (GATHER) GM_STAGE(buf, p, o0); else GM_STAGE(buf, p, voffA); } while (0)
; #define GM_STA_H1(buf, p, o1) do { if constexpr (GATHER) GM_STAGE(buf, p, o1); else GM_STAGE(buf, (p) + hstepB, voffA); } while (0)
; template <bool BF, bool GATHER = false, class Epi, class Hook>
; __device__ __forceinline__ void gemm_phase(LAS unsigned char* lds, const Gemm g, const Order& S, const Epi& E, Hook& HK) {
;     ...
;     const size_t kstep = (size_t)(BK * 2);
;     const size_t hstep = GATHER ? (size_t)0 : (size_t)HALF * K * 2;
;     const size_t hstepB = (size_t)HALF * K * 2;
;     const size_t tstep = 2 * hstepB;
;     const unsigned ldsw = (unsigned)wid * 1024u;
;     const int aoff = lds_byte(wr * 64 + fr, fq * 8), boff = lds_byte(wc * 32 + fr, fq * 8);
;     ...
;     GM_STAGE(GM_SB(0, 0), cB, voffB); GM_STAGE(GM_SB(0, 1), cB + hstepB, voffB); GM_STA_H0(GM_SA(0, 0), cA, gA0); GM_STA_H1(GM_SA(0, 1), cA, gA1);
;     if (wr == 1) GM_BAR;
;     GM_WAIT_V(2); GM_BAR;
;     GM_STAGE(GM_SB(1, 0), cB + kstep, voffB); GM_STA_H0(GM_SA(1, 0), cA + kstep, gA0); GM_STAGE(GM_SB(1, 1), cB + hstepB + kstep, voffB);
;     GM_WAIT_V(6); GM_BAR;
.LBB0_1275:
	s_lshl_b32 s8, s8, 5
	s_and_b32 s11, s8, 0x60
	s_mov_b64 s[8:9], 0x80
	s_add_i32 m0, s30, 0x18000
	v_lshl_add_u64 v[8:9], v[8:9], 0, s[8:9]
	s_lshl_b32 s3, s10, 13
	s_lshl_b32 s14, s11, 7
	s_ashr_i32 s36, s92, 31
	s_waitcnt vmcnt(2)
	s_barrier
	global_load_lds_dwordx4 v[8:9], off
	v_lshl_add_u64 v[6:7], v[6:7], 0, s[8:9]
	s_add_i32 m0, s30, 0x1a000
	s_add_i32 s37, s30, 0x8000
	s_add_i32 s38, s30, 0xa000
	global_load_lds_dwordx4 v[6:7], off
	v_lshl_add_u64 v[2:3], v[2:3], 0, s[8:9]
	s_mov_b32 m0, s37
	s_add_u32 s12, s22, 0x40080
	global_load_lds_dwordx4 v[2:3], off
	v_lshl_add_u64 v[2:3], v[4:5], 0, s[8:9]
	s_mov_b32 m0, s38
	s_addc_u32 s13, s23, 0
	global_load_lds_dwordx4 v[2:3], off
	s_cmpk_lt_u32 s5, 0x100
	v_lshrrev_b32_e32 v3, 1, v11
	v_and_b32_e32 v3, 24, v3
	v_and_b32_e32 v2, 15, v11
	v_lshlrev_b32_e32 v4, 1, v3
	v_lshl_or_b32 v1, s10, 6, v2
	v_lshl_or_b32 v2, v2, 6, v4
	v_lshlrev_b32_e32 v4, 2, v11
	v_and_b32_e32 v4, 32, v4
	v_bitop3_b32 v5, v2, s3, v4 bitop3:0xde
	v_bitop3_b32 v148, v2, s14, v4 bitop3:0xde
	v_lshlrev_b32_e32 v2, 14, v15
	v_and_b32_e32 v2, 0xffff8000, v2
	v_or_b32_e32 v149, s11, v3
	v_lshl_add_u32 v2, v14, 11, v2
	v_and_b32_e32 v3, 1, v15
	v_lshl_or_b32 v2, v3, 6, v2
	v_lshl_add_u32 v140, v16, 1, v2
	v_lshlrev_b32_e32 v2, 14, v10
	v_and_b32_e32 v2, 0xffff8000, v2
	s_waitcnt vmcnt(4)
	v_lshl_add_u32 v2, v12, 11, v2
	v_and_b32_e32 v3, 1, v10
	s_cselect_b64 s[10:11], -1, 0
	v_lshl_or_b32 v2, v3, 6, v2
	s_add_i32 s40, 0, 0x10000
	s_add_i32 s41, 0, 0x14000
	s_sext_i32_i8 s43, s4
	v_or_b32_e32 v150, 0xfffffc00, v149
	s_ashr_i32 s39, s96, 31
	v_mov_b32_e32 v141, v139
	v_lshl_add_u32 v142, v13, 1, v2
	v_mov_b32_e32 v143, v139
	v_mov_b64_e32 v[144:145], 0x500
	v_mov_b64_e32 v[146:147], 0x4ff
	v_add_u32_e32 v151, s40, v148
	v_add_u32_e32 v152, s41, v148
	v_add_u32_e32 v153, 0, v5
	s_movk_i32 s42, 0xc00
	s_barrier
	s_branch .LBB0_1278

; #define GM_STAGE(bufoff, gbase, voff) do { _Pragma("unroll") for (int _i = 0; _i < 2; ++_i) \
;         __builtin_amdgcn_global_load_lds((const unsigned*)((const char*)(gbase) + (voff)[_i]), (LAS unsigned*)(lds + (bufoff) + ldsw + _i * 8192), 16, 0, 0); } while (0)
; #define GM_LDA(dst, b, h) do { _Pragma("unroll") for (int m = 0; m < 4; ++m) _Pragma("unroll") for (int k = 0; k < 2; ++k) dst[m][k] = *(const LAS s16x8*)(lds + GM_SA(b, h) + aoff + m * 2048 + k * 1024); } while (0)
; #define GM_LDB(dst, b, h) do { _Pragma("unroll") for (int n = 0; n < 2; ++n) _Pragma("unroll") for (int k = 0; k < 2; ++k) dst[n][k] = *(const LAS s16x8*)(lds + GM_SB(b, h) + boff + n * 2048 + k * 1024); } while (0)
; #define GM_MMA(ai, bj, At, Bt) do { __builtin_amdgcn_s_setprio(1); _Pragma("unroll") for (int m = 0; m < 4; ++m) _Pragma("unroll") for (int n = 0; n < 2; ++n) _Pragma("unroll") for (int k = 0; k < 2; ++k) \
;         acc[ai][bj][m][n] = mma16<BF>(Bt[n][k], At[m][k], acc[ai][bj][m][n]); __builtin_amdgcn_s_setprio(0); } while (0)
; #define GM_WAIT_V(n) asm volatile("s_waitcnt vmcnt(" #n ")" ::: "memory")
; #define GM_WAIT_L(n) asm volatile("s_waitcnt lgkmcnt(" #n ")" ::: "memory")
; #define GM_BAR __builtin_amdgcn_s_barrier()
; #define GM_SCHED __builtin_amdgcn_sched_barrier(0)
; #define GM_STA_H0(buf, p, o0) do { if constexpr (GATHER) GM_STAGE(buf, p, o0); else GM_STAGE(buf, p, voffA); } while (0)
; #define GM_STA_H1(buf, p, o1) do { if constexpr (GATHER) GM_STAGE(buf, p, o1); else GM_STAGE(buf, (p) + hstepB, voffA); } while (0)
; template <bool BF, bool GATHER = false, class Epi, class Hook>
; __device__ __forceinline__ void gemm_phase(LAS unsigned char* lds, const Gemm g, const Order& S, const Epi& E, Hook& HK) {
;     ...
;             GM_LDB(B0, 0, 0); GM_LDB(B1, 0, 1); GM_SCHED; GM_LDA(At, 0, 0); GM_STA_H1(GM_SA(1, 1), a1, gA1);
;             GM_WAIT_V(8); GM_WAIT_L(0); GM_BAR; GM_MMA(0, 0, At, B0); GM_MMA(0, 1, At, B1); GM_BAR; GM_SCHED;
;             GM_LDA(At, 0, 1); GM_STAGE(GM_SB(0, 0), b2, voffB); GM_STAGE(GM_SB(0, 1), b2 + hstepB, voffB); GM_STA_H0(GM_SA(0, 0), a2, s0);
;             GM_WAIT_V(8); GM_WAIT_L(0); GM_BAR; GM_MMA(1, 0, At, B0); GM_MMA(1, 1, At, B1); GM_BAR; GM_SCHED;
.LBB0_1281:
	s_add_u32 s22, s20, 0xfffc0080
	s_addc_u32 s23, s21, -1
	s_cmp_eq_u32 s47, 12
	s_cselect_b32 s25, s3, s23
	s_cselect_b32 s24, s13, s22
	s_cselect_b32 s23, s15, s46
	s_cselect_b32 s22, s44, s45
	s_add_u32 s98, s45, 0x3ff80
	s_addc_u32 s99, s46, 0
	v_lshl_add_u64 v[252:253], s[98:99], 0, v[134:135]
	s_add_i32 m0, s28, 0x1c000
	s_nop 0
	global_load_lds_dwordx4 v[252:253], off
	v_lshl_add_u64 v[252:253], s[98:99], 0, v[130:131]
	s_add_i32 m0, s28, 0x1e000
	s_nop 0
	global_load_lds_dwordx4 v[252:253], off
	v_lshl_add_u64 v[218:219], s[20:21], 0, v[140:141]
	s_add_i32 m0, s30, 0xc000
	global_load_lds_dwordx4 v[218:219], off
	v_lshl_add_u64 v[218:219], s[20:21], 0, v[142:143]
	s_add_i32 m0, s30, 0xe000
	s_nop 0
	global_load_lds_dwordx4 v[218:219], off
	ds_read_b128 v[154:157], v151
	ds_read_b128 v[158:161], v151 offset:1024
	ds_read_b128 v[162:165], v151 offset:2048
	ds_read_b128 v[166:169], v151 offset:3072
	ds_read_b128 v[170:173], v152
	ds_read_b128 v[174:177], v152 offset:1024
	ds_read_b128 v[178:181], v152 offset:2048
	ds_read_b128 v[182:185], v152 offset:3072
	ds_read_b128 v[186:189], v153
	ds_read_b128 v[190:193], v153 offset:1024
	ds_read_b128 v[194:197], v153 offset:2048
	ds_read_b128 v[198:201], v153 offset:3072
	ds_read_b128 v[202:205], v153 offset:4096
	ds_read_b128 v[206:209], v153 offset:5120
	ds_read_b128 v[210:213], v153 offset:6144
	ds_read_b128 v[214:217], v153 offset:7168
	s_waitcnt vmcnt(8)
	s_waitcnt lgkmcnt(0)
	s_barrier
	s_waitcnt lgkmcnt(0)
	v_mfma_f32_16x16x32_f16 v[126:129], v[154:157], v[186:189], v[126:129]
	v_mfma_f32_16x16x32_f16 v[118:121], v[162:165], v[186:189], v[118:121]
	v_mfma_f32_16x16x32_f16 v[110:113], v[154:157], v[194:197], v[110:113]
	v_mfma_f32_16x16x32_f16 v[102:105], v[162:165], v[194:197], v[102:105]
	v_mfma_f32_16x16x32_f16 v[94:97], v[154:157], v[202:205], v[94:97]
	v_mfma_f32_16x16x32_f16 v[86:89], v[162:165], v[202:205], v[86:89]
	v_mfma_f32_16x16x32_f16 v[78:81], v[154:157], v[210:213], v[78:81]
	v_mfma_f32_16x16x32_f16 v[70:73], v[162:165], v[210:213], v[70:73]
	v_mfma_f32_16x16x32_f16 v[126:129], v[158:161], v[190:193], v[126:129]
	v_mfma_f32_16x16x32_f16 v[118:121], v[166:169], v[190:193], v[118:121]
	v_mfma_f32_16x16x32_f16 v[110:113], v[158:161], v[198:201], v[110:113]
	v_mfma_f32_16x16x32_f16 v[102:105], v[166:169], v[198:201], v[102:105]
	v_mfma_f32_16x16x32_f16 v[94:97], v[158:161], v[206:209], v[94:97]
	v_mfma_f32_16x16x32_f16 v[86:89], v[166:169], v[206:209], v[86:89]
	v_mfma_f32_16x16x32_f16 v[78:81], v[158:161], v[214:217], v[78:81]
	v_mfma_f32_16x16x32_f16 v[70:73], v[166:169], v[214:217], v[70:73]
	v_mfma_f32_16x16x32_f16 v[122:125], v[170:173], v[186:189], v[122:125]
	v_mfma_f32_16x16x32_f16 v[114:117], v[178:181], v[186:189], v[114:117]
	v_mfma_f32_16x16x32_f16 v[106:109], v[170:173], v[194:197], v[106:109]
	v_mfma_f32_16x16x32_f16 v[98:101], v[178:181], v[194:197], v[98:101]
	v_mfma_f32_16x16x32_f16 v[90:93], v[170:173], v[202:205], v[90:93]
	v_mfma_f32_16x16x32_f16 v[82:85], v[178:181], v[202:205], v[82:85]
	v_mfma_f32_16x16x32_f16 v[74:77], v[170:173], v[210:213], v[74:77]
	v_mfma_f32_16x16x32_f16 v[66:69], v[178:181], v[210:213], v[66:69]
	v_mfma_f32_16x16x32_f16 v[122:125], v[174:177], v[190:193], v[122:125]
	v_mfma_f32_16x16x32_f16 v[114:117], v[182:185], v[190:193], v[114:117]
	v_mfma_f32_16x16x32_f16 v[106:109], v[174:177], v[198:201], v[106:109]
	v_mfma_f32_16x16x32_f16 v[98:101], v[182:185], v[198:201], v[98:101]
	v_mfma_f32_16x16x32_f16 v[90:93], v[174:177], v[206:209], v[90:93]
	v_mfma_f32_16x16x32_f16 v[82:85], v[182:185], v[206:209], v[82:85]
	v_mfma_f32_16x16x32_f16 v[74:77], v[174:177], v[214:217], v[74:77]
	v_mfma_f32_16x16x32_f16 v[66:69], v[182:185], v[214:217], v[66:69]
	s_barrier
	s_add_i32 s48, s40, s28
	v_lshl_add_u64 v[218:219], s[22:23], 0, v[134:135]
	s_mov_b32 m0, s48
	global_load_lds_dwordx4 v[218:219], off
	s_add_i32 m0, s48, 0x2000
	s_add_u32 s48, s22, 0x40000
	v_lshl_add_u64 v[220:221], s[22:23], 0, v[130:131]
	s_addc_u32 s49, s23, 0
	s_add_i32 s50, s41, s28
	global_load_lds_dwordx4 v[220:221], off
	v_lshl_add_u64 v[224:225], s[24:25], 0, v[132:133]
	v_lshl_add_u64 v[222:223], s[24:25], 0, v[136:137]
	s_mov_b32 m0, s30
	s_nop 0
	global_load_lds_dwordx4 v[222:223], off
	s_mov_b32 m0, s31
	s_nop 0
	global_load_lds_dwordx4 v[224:225], off
	ds_read_b128 v[186:189], v153 offset:16384
	ds_read_b128 v[190:193], v153 offset:17408
	ds_read_b128 v[194:197], v153 offset:18432
	ds_read_b128 v[198:201], v153 offset:19456
	ds_read_b128 v[202:205], v153 offset:20480
	ds_read_b128 v[206:209], v153 offset:21504
	ds_read_b128 v[210:213], v153 offset:22528
	ds_read_b128 v[214:217], v153 offset:23552
	s_waitcnt vmcnt(6)
	s_waitcnt lgkmcnt(0)
	s_barrier
; #define GM_STAGE(bufoff, gbase, voff) do { _Pragma("unroll") for (int _i = 0; _i < 2; ++_i) \
;         __builtin_amdgcn_global_load_lds((const unsigned*)((const char*)(gbase) + (voff)[_i]), (LAS unsigned*)(lds + (bufoff) + ldsw + _i * 8192), 16, 0, 0); } while (0)
; #define GM_LDA(dst, b, h) do { _Pragma("unroll") for (int m = 0; m < 4; ++m) _Pragma("unroll") for (int k = 0; k < 2; ++k) dst[m][k] = *(const LAS s16x8*)(lds + GM_SA(b, h) + aoff + m * 2048 + k * 1024); } while (0)
; #define GM_LDB(dst, b, h) do { _Pragma("unroll") for (int n = 0; n < 2; ++n) _Pragma("unroll") for (int k = 0; k < 2; ++k) dst[n][k] = *(const LAS s16x8*)(lds + GM_SB(b, h) + boff + n * 2048 + k * 1024); } while (0)
; #define GM_MMA(ai, bj, At, Bt) do { __builtin_amdgcn_s_setprio(1); _Pragma("unroll") for (int m = 0; m < 4; ++m) _Pragma("unroll") for (int n = 0; n < 2; ++n) _Pragma("unroll") for (int k = 0; k < 2; ++k) \
;         acc[ai][bj][m][n] = mma16<BF>(Bt[n][k], At[m][k], acc[ai][bj][m][n]); __builtin_amdgcn_s_setprio(0); } while (0)
; #define GM_WAIT_V(n) asm volatile("s_waitcnt vmcnt(" #n ")" ::: "memory")
; #define GM_WAIT_L(n) asm volatile("s_waitcnt lgkmcnt(" #n ")" ::: "memory")
; #define GM_BAR __builtin_amdgcn_s_barrier()
; #define GM_SCHED __builtin_amdgcn_sched_barrier(0)
; #define GM_STA_H0(buf, p, o0) do { if constexpr (GATHER) GM_STAGE(buf, p, o0); else GM_STAGE(buf, p, voffA); } while (0)
; #define GM_STA_H1(buf, p, o1) do { if constexpr (GATHER) GM_STAGE(buf, p, o1); else GM_STAGE(buf, (p) + hstepB, voffA); } while (0)
; template <bool BF, bool GATHER = false, class Epi, class Hook>
; __device__ __forceinline__ void gemm_phase(LAS unsigned char* lds, const Gemm g, const Order& S, const Epi& E, Hook& HK) {
;     ...
;             GM_WAIT_V(8); GM_WAIT_L(0); GM_BAR; GM_MMA(1, 0, At, B0); GM_MMA(1, 1, At, B1); GM_BAR; GM_SCHED;
;             GM_LDB(B0, 1, 0); GM_LDB(B1, 1, 1); GM_SCHED; GM_LDA(At, 1, 0); GM_STA_H1(GM_SA(0, 1), a2, s1);
;             GM_WAIT_V(8); GM_WAIT_L(0); GM_BAR; GM_MMA(0, 0, At, B0); GM_MMA(0, 1, At, B1); GM_BAR; GM_SCHED;
;             GM_LDA(At, 1, 1); GM_STAGE(GM_SB(1, 0), b3, voffB); GM_STAGE(GM_SB(1, 1), b3 + hstepB, voffB); GM_STA_H0(GM_SA(1, 0), a3, s0);
	s_waitcnt lgkmcnt(0)
	v_mfma_f32_16x16x32_f16 v[62:65], v[154:157], v[186:189], v[62:65]
	v_mfma_f32_16x16x32_f16 v[54:57], v[162:165], v[186:189], v[54:57]
	v_mfma_f32_16x16x32_f16 v[46:49], v[154:157], v[194:197], v[46:49]
	v_mfma_f32_16x16x32_f16 v[38:41], v[162:165], v[194:197], v[38:41]
	v_mfma_f32_16x16x32_f16 v[30:33], v[154:157], v[202:205], v[30:33]
	v_mfma_f32_16x16x32_f16 v[22:25], v[162:165], v[202:205], v[22:25]
	v_mfma_f32_16x16x32_f16 v[14:17], v[154:157], v[210:213], v[14:17]
	v_mfma_f32_16x16x32_f16 v[6:9], v[162:165], v[210:213], v[6:9]
	v_mfma_f32_16x16x32_f16 v[62:65], v[158:161], v[190:193], v[62:65]
	v_mfma_f32_16x16x32_f16 v[54:57], v[166:169], v[190:193], v[54:57]
	v_mfma_f32_16x16x32_f16 v[46:49], v[158:161], v[198:201], v[46:49]
	v_mfma_f32_16x16x32_f16 v[38:41], v[166:169], v[198:201], v[38:41]
	v_mfma_f32_16x16x32_f16 v[30:33], v[158:161], v[206:209], v[30:33]
	v_mfma_f32_16x16x32_f16 v[22:25], v[166:169], v[206:209], v[22:25]
	v_mfma_f32_16x16x32_f16 v[14:17], v[158:161], v[214:217], v[14:17]
	v_mfma_f32_16x16x32_f16 v[6:9], v[166:169], v[214:217], v[6:9]
	v_mfma_f32_16x16x32_f16 v[58:61], v[170:173], v[186:189], v[58:61]
	v_mfma_f32_16x16x32_f16 v[50:53], v[178:181], v[186:189], v[50:53]
	v_mfma_f32_16x16x32_f16 v[42:45], v[170:173], v[194:197], v[42:45]
	v_mfma_f32_16x16x32_f16 v[34:37], v[178:181], v[194:197], v[34:37]
	v_mfma_f32_16x16x32_f16 v[26:29], v[170:173], v[202:205], v[26:29]
	v_mfma_f32_16x16x32_f16 v[18:21], v[178:181], v[202:205], v[18:21]
	v_mfma_f32_16x16x32_f16 v[10:13], v[170:173], v[210:213], v[10:13]
	v_mfma_f32_16x16x32_f16 v[2:5], v[178:181], v[210:213], v[2:5]
	v_mfma_f32_16x16x32_f16 v[58:61], v[174:177], v[190:193], v[58:61]
	v_mfma_f32_16x16x32_f16 v[50:53], v[182:185], v[190:193], v[50:53]
	v_mfma_f32_16x16x32_f16 v[42:45], v[174:177], v[198:201], v[42:45]
	v_mfma_f32_16x16x32_f16 v[34:37], v[182:185], v[198:201], v[34:37]
	v_mfma_f32_16x16x32_f16 v[26:29], v[174:177], v[206:209], v[26:29]
	v_mfma_f32_16x16x32_f16 v[18:21], v[182:185], v[206:209], v[18:21]
	v_mfma_f32_16x16x32_f16 v[10:13], v[174:177], v[214:217], v[10:13]
	v_mfma_f32_16x16x32_f16 v[2:5], v[182:185], v[214:217], v[2:5]
	s_barrier
	s_add_u32 s24, s24, 0x40000
	s_addc_u32 s25, s25, 0
	s_add_u32 s98, s22, 0x40000
	s_addc_u32 s99, s23, 0
	v_lshl_add_u64 v[252:253], s[98:99], 0, v[134:135]
	s_add_i32 m0, s28, 0x14000
	s_nop 0
	global_load_lds_dwordx4 v[252:253], off
	v_lshl_add_u64 v[252:253], s[98:99], 0, v[130:131]
	s_add_i32 m0, s28, 0x16000
	s_nop 0
	global_load_lds_dwordx4 v[252:253], off
	s_mov_b32 m0, s33
	v_lshl_add_u64 v[226:227], s[24:25], 0, v[136:137]
	global_load_lds_dwordx4 v[226:227], off
	v_lshl_add_u64 v[226:227], s[24:25], 0, v[132:133]
	s_mov_b32 m0, s34
	s_nop 0
	global_load_lds_dwordx4 v[226:227], off
	s_mov_b32 s49, 0x1c000
	s_mov_b32 s48, 0x18000
	v_add_u32_e32 v244, s48, v148
	ds_read_b128 v[154:157], v244
	ds_read_b128 v[158:161], v244 offset:1024
	ds_read_b128 v[162:165], v244 offset:2048
	ds_read_b128 v[166:169], v244 offset:3072
	v_add_u32_e32 v244, s49, v148
	ds_read_b128 v[170:173], v244
	ds_read_b128 v[174:177], v244 offset:1024
	ds_read_b128 v[178:181], v244 offset:2048
	ds_read_b128 v[182:185], v244 offset:3072
	ds_read_b128 v[186:189], v153 offset:32768
	ds_read_b128 v[190:193], v153 offset:33792
	ds_read_b128 v[194:197], v153 offset:34816
	ds_read_b128 v[198:201], v153 offset:35840
	ds_read_b128 v[202:205], v153 offset:36864
	ds_read_b128 v[206:209], v153 offset:37888
	ds_read_b128 v[210:213], v153 offset:38912
	ds_read_b128 v[214:217], v153 offset:39936
	s_waitcnt vmcnt(8)
	s_waitcnt lgkmcnt(0)
	s_barrier
; #define GM_STAGE(bufoff, gbase, voff) do { _Pragma("unroll") for (int _i = 0; _i < 2; ++_i) \
;         __builtin_amdgcn_global_load_lds((const unsigned*)((const char*)(gbase) + (voff)[_i]), (LAS unsigned*)(lds + (bufoff) + ldsw + _i * 8192), 16, 0, 0); } while (0)
; #define GM_LDA(dst, b, h) do { _Pragma("unroll") for (int m = 0; m < 4; ++m) _Pragma("unroll") for (int k = 0; k < 2; ++k) dst[m][k] = *(const LAS s16x8*)(lds + GM_SA(b, h) + aoff + m * 2048 + k * 1024); } while (0)
; #define GM_LDB(dst, b, h) do { _Pragma("unroll") for (int n = 0; n < 2; ++n) _Pragma("unroll") for (int k = 0; k < 2; ++k) dst[n][k] = *(const LAS s16x8*)(lds + GM_SB(b, h) + boff + n * 2048 + k * 1024); } while (0)
; #define GM_MMA(ai, bj, At, Bt) do { __builtin_amdgcn_s_setprio(1); _Pragma("unroll") for (int m = 0; m < 4; ++m) _Pragma("unroll") for (int n = 0; n < 2; ++n) _Pragma("unroll") for (int k = 0; k < 2; ++k) \
;         acc[ai][bj][m][n] = mma16<BF>(Bt[n][k], At[m][k], acc[ai][bj][m][n]); __builtin_amdgcn_s_setprio(0); } while (0)
; #define GM_WAIT_V(n) asm volatile("s_waitcnt vmcnt(" #n ")" ::: "memory")
; #define GM_WAIT_L(n) asm volatile("s_waitcnt lgkmcnt(" #n ")" ::: "memory")
; #define GM_BAR __builtin_amdgcn_s_barrier()
; #define GM_SCHED __builtin_amdgcn_sched_barrier(0)
; #define GM_STA_H0(buf, p, o0) do { if constexpr (GATHER) GM_STAGE(buf, p, o0); else GM_STAGE(buf, p, voffA); } while (0)
; #define GM_STA_H1(buf, p, o1) do { if constexpr (GATHER) GM_STAGE(buf, p, o1); else GM_STAGE(buf, (p) + hstepB, voffA); } while (0)
; template <bool BF, bool GATHER = false, class Epi, class Hook>
; __device__ __forceinline__ void gemm_phase(LAS unsigned char* lds, const Gemm g, const Order& S, const Epi& E, Hook& HK) {
;     ...
;             GM_LDB(B0, 1, 0); GM_LDB(B1, 1, 1); GM_SCHED; GM_LDA(At, 1, 0); GM_STA_H1(GM_SA(0, 1), a2, s1);
;             GM_WAIT_V(8); GM_WAIT_L(0); GM_BAR; GM_MMA(0, 0, At, B0); GM_MMA(0, 1, At, B1); GM_BAR; GM_SCHED;
;             GM_LDA(At, 1, 1); GM_STAGE(GM_SB(1, 0), b3, voffB); GM_STAGE(GM_SB(1, 1), b3 + hstepB, voffB); GM_STA_H0(GM_SA(1, 0), a3, s0);
;             GM_WAIT_V(8); GM_WAIT_L(0); GM_BAR; GM_MMA(1, 0, At, B0); GM_MMA(1, 1, At, B1); GM_BAR; GM_SCHED;
;         }
	s_waitcnt lgkmcnt(0)
	v_mfma_f32_16x16x32_f16 v[126:129], v[154:157], v[186:189], v[126:129]
	v_mfma_f32_16x16x32_f16 v[118:121], v[162:165], v[186:189], v[118:121]
	v_mfma_f32_16x16x32_f16 v[110:113], v[154:157], v[194:197], v[110:113]
	v_mfma_f32_16x16x32_f16 v[102:105], v[162:165], v[194:197], v[102:105]
	v_mfma_f32_16x16x32_f16 v[94:97], v[154:157], v[202:205], v[94:97]
	v_mfma_f32_16x16x32_f16 v[86:89], v[162:165], v[202:205], v[86:89]
	v_mfma_f32_16x16x32_f16 v[78:81], v[154:157], v[210:213], v[78:81]
	v_mfma_f32_16x16x32_f16 v[70:73], v[162:165], v[210:213], v[70:73]
	v_mfma_f32_16x16x32_f16 v[126:129], v[158:161], v[190:193], v[126:129]
	v_mfma_f32_16x16x32_f16 v[118:121], v[166:169], v[190:193], v[118:121]
	v_mfma_f32_16x16x32_f16 v[110:113], v[158:161], v[198:201], v[110:113]
	v_mfma_f32_16x16x32_f16 v[102:105], v[166:169], v[198:201], v[102:105]
	v_mfma_f32_16x16x32_f16 v[94:97], v[158:161], v[206:209], v[94:97]
	v_mfma_f32_16x16x32_f16 v[86:89], v[166:169], v[206:209], v[86:89]
	v_mfma_f32_16x16x32_f16 v[78:81], v[158:161], v[214:217], v[78:81]
	v_mfma_f32_16x16x32_f16 v[70:73], v[166:169], v[214:217], v[70:73]
	v_mfma_f32_16x16x32_f16 v[122:125], v[170:173], v[186:189], v[122:125]
	v_mfma_f32_16x16x32_f16 v[114:117], v[178:181], v[186:189], v[114:117]
	v_mfma_f32_16x16x32_f16 v[106:109], v[170:173], v[194:197], v[106:109]
	v_mfma_f32_16x16x32_f16 v[98:101], v[178:181], v[194:197], v[98:101]
	v_mfma_f32_16x16x32_f16 v[90:93], v[170:173], v[202:205], v[90:93]
	v_mfma_f32_16x16x32_f16 v[82:85], v[178:181], v[202:205], v[82:85]
	v_mfma_f32_16x16x32_f16 v[74:77], v[170:173], v[210:213], v[74:77]
	v_mfma_f32_16x16x32_f16 v[66:69], v[178:181], v[210:213], v[66:69]
	v_mfma_f32_16x16x32_f16 v[122:125], v[174:177], v[190:193], v[122:125]
	v_mfma_f32_16x16x32_f16 v[114:117], v[182:185], v[190:193], v[114:117]
	v_mfma_f32_16x16x32_f16 v[106:109], v[174:177], v[198:201], v[106:109]
	v_mfma_f32_16x16x32_f16 v[98:101], v[182:185], v[198:201], v[98:101]
	v_mfma_f32_16x16x32_f16 v[90:93], v[174:177], v[206:209], v[90:93]
	v_mfma_f32_16x16x32_f16 v[82:85], v[182:185], v[206:209], v[82:85]
	v_mfma_f32_16x16x32_f16 v[74:77], v[174:177], v[214:217], v[74:77]
	v_mfma_f32_16x16x32_f16 v[66:69], v[182:185], v[214:217], v[66:69]
	s_barrier
	s_add_i32 s24, s48, s28
	v_lshl_add_u64 v[218:219], v[218:219], 0, s[8:9]
	s_mov_b32 m0, s24
	global_load_lds_dwordx4 v[218:219], off
	s_add_i32 m0, s24, 0x2000
	s_add_u32 s22, s22, 0x40080
	v_lshl_add_u64 v[218:219], v[220:221], 0, s[8:9]
	s_addc_u32 s23, s23, 0
	s_add_i32 s24, s49, s28
	global_load_lds_dwordx4 v[218:219], off
	v_lshl_add_u64 v[218:219], v[222:223], 0, s[8:9]
	s_mov_b32 m0, s37
	s_nop 0
	global_load_lds_dwordx4 v[218:219], off
	v_lshl_add_u64 v[218:219], v[224:225], 0, s[8:9]
	s_mov_b32 m0, s38
	s_nop 0
	global_load_lds_dwordx4 v[218:219], off
	ds_read_b128 v[186:189], v153 offset:49152
	ds_read_b128 v[190:193], v153 offset:50176
	ds_read_b128 v[194:197], v153 offset:51200
	ds_read_b128 v[198:201], v153 offset:52224
	ds_read_b128 v[202:205], v153 offset:53248
	ds_read_b128 v[206:209], v153 offset:54272
	ds_read_b128 v[210:213], v153 offset:55296
	ds_read_b128 v[214:217], v153 offset:56320
	s_waitcnt vmcnt(6)
	s_waitcnt lgkmcnt(0)
	s_barrier
	s_waitcnt lgkmcnt(0)
	v_mfma_f32_16x16x32_f16 v[62:65], v[154:157], v[186:189], v[62:65]
	v_mfma_f32_16x16x32_f16 v[54:57], v[162:165], v[186:189], v[54:57]
	v_mfma_f32_16x16x32_f16 v[46:49], v[154:157], v[194:197], v[46:49]
	v_mfma_f32_16x16x32_f16 v[38:41], v[162:165], v[194:197], v[38:41]
	v_mfma_f32_16x16x32_f16 v[30:33], v[154:157], v[202:205], v[30:33]
	v_mfma_f32_16x16x32_f16 v[22:25], v[162:165], v[202:205], v[22:25]
	v_mfma_f32_16x16x32_f16 v[14:17], v[154:157], v[210:213], v[14:17]
	v_mfma_f32_16x16x32_f16 v[6:9], v[162:165], v[210:213], v[6:9]
	v_mfma_f32_16x16x32_f16 v[62:65], v[158:161], v[190:193], v[62:65]
	v_mfma_f32_16x16x32_f16 v[54:57], v[166:169], v[190:193], v[54:57]
	v_mfma_f32_16x16x32_f16 v[46:49], v[158:161], v[198:201], v[46:49]
	v_mfma_f32_16x16x32_f16 v[38:41], v[166:169], v[198:201], v[38:41]
	v_mfma_f32_16x16x32_f16 v[30:33], v[158:161], v[206:209], v[30:33]
	v_mfma_f32_16x16x32_f16 v[22:25], v[166:169], v[206:209], v[22:25]
	v_mfma_f32_16x16x32_f16 v[14:17], v[158:161], v[214:217], v[14:17]
	v_mfma_f32_16x16x32_f16 v[6:9], v[166:169], v[214:217], v[6:9]
	v_mfma_f32_16x16x32_f16 v[58:61], v[170:173], v[186:189], v[58:61]
	v_mfma_f32_16x16x32_f16 v[50:53], v[178:181], v[186:189], v[50:53]
	v_mfma_f32_16x16x32_f16 v[42:45], v[170:173], v[194:197], v[42:45]
	v_mfma_f32_16x16x32_f16 v[34:37], v[178:181], v[194:197], v[34:37]
	v_mfma_f32_16x16x32_f16 v[26:29], v[170:173], v[202:205], v[26:29]
	v_mfma_f32_16x16x32_f16 v[18:21], v[178:181], v[202:205], v[18:21]
	v_mfma_f32_16x16x32_f16 v[10:13], v[170:173], v[210:213], v[10:13]
	v_mfma_f32_16x16x32_f16 v[2:5], v[178:181], v[210:213], v[2:5]
	v_mfma_f32_16x16x32_f16 v[58:61], v[174:177], v[190:193], v[58:61]
	v_mfma_f32_16x16x32_f16 v[50:53], v[182:185], v[190:193], v[50:53]
	v_mfma_f32_16x16x32_f16 v[42:45], v[174:177], v[198:201], v[42:45]
	v_mfma_f32_16x16x32_f16 v[34:37], v[182:185], v[198:201], v[34:37]
	v_mfma_f32_16x16x32_f16 v[26:29], v[174:177], v[206:209], v[26:29]
	v_mfma_f32_16x16x32_f16 v[18:21], v[182:185], v[206:209], v[18:21]
	v_mfma_f32_16x16x32_f16 v[10:13], v[174:177], v[214:217], v[10:13]
	v_mfma_f32_16x16x32_f16 v[2:5], v[182:185], v[214:217], v[2:5]
	s_barrier
	s_add_i32 s47, s47, 2
	s_add_u32 s20, s20, 0x100
	s_addc_u32 s21, s21, 0
	s_add_u32 s45, s45, 0x100
	s_addc_u32 s46, s46, 0
	s_cmp_gt_u32 s47, 13
	s_cbranch_scc0 .LBB0_1281
	s_and_b64 vcc, exec, s[10:11]
	s_cbranch_vccnz .LBB0_1286
	v_lshl_add_u32 v154, s2, 8, v1
	s_cmp_gt_i32 s43, 7
	s_mov_b64 s[2:3], -1
	s_cbranch_scc1 .LBB0_1287

; #define GM_STAGE(bufoff, gbase, voff) do { _Pragma("unroll") for (int _i = 0; _i < 2; ++_i) \
;         __builtin_amdgcn_global_load_lds((const unsigned*)((const char*)(gbase) + (voff)[_i]), (LAS unsigned*)(lds + (bufoff) + ldsw + _i * 8192), 16, 0, 0); } while (0)
; #define GM_WAIT_V(n) asm volatile("s_waitcnt vmcnt(" #n ")" ::: "memory")
; #define GM_BAR __builtin_amdgcn_s_barrier()
; #define GM_STA_H0(buf, p, o0) do { if constexpr (GATHER) GM_STAGE(buf, p, o0); else GM_STAGE(buf, p, voffA); } while (0)
; template <bool BF, bool GATHER = false, class Epi, class Hook>
; __device__ __forceinline__ void gemm_phase(LAS unsigned char* lds, const Gemm g, const Order& S, const Epi& E, Hook& HK) {
;     ...
;     const unsigned ldsw = (unsigned)wid * 1024u;
;     const int aoff = lds_byte(wr * 64 + fr, fq * 8), boff = lds_byte(wc * 32 + fr, fq * 8);
;     ...
;     GM_WAIT_V(2); GM_BAR;
;     GM_STAGE(GM_SB(1, 0), cB + kstep, voffB); GM_STA_H0(GM_SA(1, 0), cA + kstep, gA0); GM_STAGE(GM_SB(1, 1), cB + hstepB + kstep, voffB);
;     GM_WAIT_V(6); GM_BAR;
.LBB0_1470:
	v_readlane_b32 s16, v250, 17
	v_readlane_b32 s18, v250, 19
	s_cmp_eq_u32 s18, 0
	s_cselect_b32 s9, s67, s77
	s_cselect_b32 s8, s66, s76
	s_add_u32 s38, s90, 0x168000
	s_addc_u32 s39, s91, 0
	s_lshl_b32 s3, s10, 5
	s_mov_b64 s[10:11], 0x80
	v_readlane_b32 s17, v250, 18
	s_and_b32 s16, s3, 0x60
	s_add_i32 m0, s33, 0x18000
	v_lshl_add_u64 v[8:9], v[8:9], 0, s[10:11]
	s_lshl_b32 s13, s12, 13
	s_lshl_b32 s17, s16, 7
	s_waitcnt vmcnt(2)
	s_barrier
	global_load_lds_dwordx4 v[8:9], off
	v_lshl_add_u64 v[6:7], v[6:7], 0, s[10:11]
	s_add_i32 m0, s33, 0x1a000
	s_add_i32 s40, s33, 0x8000
	s_add_i32 s41, s33, 0xa000
	global_load_lds_dwordx4 v[6:7], off
	v_lshl_add_u64 v[2:3], v[2:3], 0, s[10:11]
	s_mov_b32 m0, s40
	s_add_u32 s14, s24, 0x40080
	global_load_lds_dwordx4 v[2:3], off
	v_lshl_add_u64 v[2:3], v[4:5], 0, s[10:11]
	s_mov_b32 m0, s41
	s_addc_u32 s15, s25, 0
	global_load_lds_dwordx4 v[2:3], off
	s_cmpk_lt_u32 s5, 0x100
	v_lshrrev_b32_e32 v3, 1, v10
	v_and_b32_e32 v3, 24, v3
	v_and_b32_e32 v2, 15, v10
	v_lshlrev_b32_e32 v4, 1, v3
	v_lshl_or_b32 v1, s12, 6, v2
	v_lshl_or_b32 v2, v2, 6, v4
	v_lshlrev_b32_e32 v4, 2, v10
	v_and_b32_e32 v4, 32, v4
	v_bitop3_b32 v5, v2, s13, v4 bitop3:0xde
	v_bitop3_b32 v166, v2, s17, v4 bitop3:0xde
	v_lshlrev_b32_e32 v2, 14, v11
	v_and_b32_e32 v2, 0xffff8000, v2
	v_or_b32_e32 v167, s16, v3
	v_lshl_add_u32 v2, v12, 11, v2
	v_and_b32_e32 v3, 1, v11
	v_lshl_or_b32 v2, v3, 6, v2
	v_lshl_add_u32 v154, v13, 1, v2
	v_lshlrev_b32_e32 v2, 14, v14
	v_and_b32_e32 v2, 0xffff8000, v2
	s_waitcnt vmcnt(4)
	v_lshl_add_u32 v2, v15, 11, v2
	v_and_b32_e32 v3, 1, v14
	s_cselect_b64 s[12:13], -1, 0
	v_lshl_or_b32 v2, v3, 6, v2
	s_add_i32 s43, 0, 0x10000
	s_add_i32 s44, 0, 0x14000
	s_sext_i32_i8 s3, s4
	s_ashr_i32 s42, s96, 31
	v_mov_b32_e32 v155, v149
	v_lshl_add_u32 v156, v16, 1, v2
	v_mov_b32_e32 v157, v149
	v_mov_b64_e32 v[158:159], 0x200
	v_mov_b64_e32 v[160:161], 0x1ff
	v_add_u32_e32 v168, s43, v166
	v_add_u32_e32 v169, s44, v166
	v_add_u32_e32 v170, 0, v5
	v_readlane_b32 s19, v250, 20
	s_barrier
	s_branch .LBB0_1473

; #define GM_STAGE(bufoff, gbase, voff) do { _Pragma("unroll") for (int _i = 0; _i < 2; ++_i) \
;         __builtin_amdgcn_global_load_lds((const unsigned*)((const char*)(gbase) + (voff)[_i]), (LAS unsigned*)(lds + (bufoff) + ldsw + _i * 8192), 16, 0, 0); } while (0)
; #define GM_LDA(dst, b, h) do { _Pragma("unroll") for (int m = 0; m < 4; ++m) _Pragma("unroll") for (int k = 0; k < 2; ++k) dst[m][k] = *(const LAS s16x8*)(lds + GM_SA(b, h) + aoff + m * 2048 + k * 1024); } while (0)
; #define GM_LDB(dst, b, h) do { _Pragma("unroll") for (int n = 0; n < 2; ++n) _Pragma("unroll") for (int k = 0; k < 2; ++k) dst[n][k] = *(const LAS s16x8*)(lds + GM_SB(b, h) + boff + n * 2048 + k * 1024); } while (0)
; #define GM_MMA(ai, bj, At, Bt) do { __builtin_amdgcn_s_setprio(1); _Pragma("unroll") for (int m = 0; m < 4; ++m) _Pragma("unroll") for (int n = 0; n < 2; ++n) _Pragma("unroll") for (int k = 0; k < 2; ++k) \
;         acc[ai][bj][m][n] = mma16<BF>(Bt[n][k], At[m][k], acc[ai][bj][m][n]); __builtin_amdgcn_s_setprio(0); } while (0)
; #define GM_WAIT_V(n) asm volatile("s_waitcnt vmcnt(" #n ")" ::: "memory")
; #define GM_WAIT_L(n) asm volatile("s_waitcnt lgkmcnt(" #n ")" ::: "memory")
; #define GM_BAR __builtin_amdgcn_s_barrier()
; template <bool BF, bool GATHER = false, class Epi, class Hook>
; __device__ __forceinline__ void gemm_phase(LAS unsigned char* lds, const Gemm g, const Order& S, const Epi& E, Hook& HK) {
;     ...
;             const char* a1 = cA + (size_t)(t + 1) * kstep;
;             const char* a2 = last ? nA : cA + (size_t)(t + 2) * kstep; const char* b2 = last ? nB : cB + (size_t)(t + 2) * kstep;
;             const char* a3 = a2 + kstep; const char* b3 = b2 + kstep;
;             unsigned s0[2], s1[2];
;             if constexpr (GATHER) { s0[0] = last ? nA0[0] : gA0[0]; s0[1] = last ? nA0[1] : gA0[1]; s1[0] = last ? nA1[0] : gA1[0]; s1[1] = last ? nA1[1] : gA1[1]; }
;             GM_LDB(B0, 0, 0); GM_LDB(B1, 0, 1); GM_SCHED; GM_LDA(At, 0, 0); GM_STA_H1(GM_SA(1, 1), a1, gA1);
;             GM_WAIT_V(8); GM_WAIT_L(0); GM_BAR; GM_MMA(0, 0, At, B0); GM_MMA(0, 1, At, B1); GM_BAR; GM_SCHED;
;             GM_LDA(At, 0, 1); GM_STAGE(GM_SB(0, 0), b2, voffB); GM_STAGE(GM_SB(0, 1), b2 + hstepB, voffB); GM_STA_H0(GM_SA(0, 0), a2, s0);
;             GM_WAIT_V(8); GM_WAIT_L(0); GM_BAR; GM_MMA(1, 0, At, B0); GM_MMA(1, 1, At, B1); GM_BAR; GM_SCHED;
.LBB0_1480:
	s_add_u32 s24, s22, 0xfffc0080
	s_addc_u32 s25, s23, -1
	s_cmp_eq_u32 s49, 12
	s_cselect_b32 s27, s15, s25
	s_cselect_b32 s26, s45, s24
	s_cselect_b32 s25, s17, s48
	s_cselect_b32 s24, s46, s47
	s_add_u32 s98, s47, 0x3ff80
	s_addc_u32 s99, s48, 0
	v_lshl_add_u64 v[252:253], s[98:99], 0, v[148:149]
	s_add_i32 m0, s31, 0x1c000
	s_nop 0
	global_load_lds_dwordx4 v[252:253], off
	v_lshl_add_u64 v[252:253], s[98:99], 0, v[152:153]
	s_add_i32 m0, s31, 0x1e000
	s_nop 0
	global_load_lds_dwordx4 v[252:253], off
	v_lshl_add_u64 v[216:217], s[22:23], 0, v[154:155]
	s_add_i32 m0, s33, 0xc000
	global_load_lds_dwordx4 v[216:217], off
	v_lshl_add_u64 v[216:217], s[22:23], 0, v[156:157]
	s_add_i32 m0, s33, 0xe000
	s_nop 0
	global_load_lds_dwordx4 v[216:217], off
	ds_read_b128 v[122:125], v168
	ds_read_b128 v[126:129], v168 offset:1024
	ds_read_b128 v[130:133], v168 offset:2048
	ds_read_b128 v[134:137], v168 offset:3072
	ds_read_b128 v[162:165], v169
	ds_read_b128 v[172:175], v169 offset:1024
	ds_read_b128 v[176:179], v169 offset:2048
	ds_read_b128 v[180:183], v169 offset:3072
	ds_read_b128 v[184:187], v170
	ds_read_b128 v[188:191], v170 offset:1024
	ds_read_b128 v[192:195], v170 offset:2048
	ds_read_b128 v[196:199], v170 offset:3072
	ds_read_b128 v[200:203], v170 offset:4096
	ds_read_b128 v[204:207], v170 offset:5120
	ds_read_b128 v[208:211], v170 offset:6144
	ds_read_b128 v[212:215], v170 offset:7168
	s_waitcnt vmcnt(8)
	s_waitcnt lgkmcnt(0)
	s_barrier
	s_waitcnt lgkmcnt(0)
	v_mfma_f32_16x16x32_f16 v[142:145], v[122:125], v[184:187], v[142:145]
	v_mfma_f32_16x16x32_f16 v[138:141], v[130:133], v[184:187], v[138:141]
	v_mfma_f32_16x16x32_f16 v[110:113], v[122:125], v[192:195], v[110:113]
	v_mfma_f32_16x16x32_f16 v[106:109], v[130:133], v[192:195], v[106:109]
	v_mfma_f32_16x16x32_f16 v[94:97], v[122:125], v[200:203], v[94:97]
	v_mfma_f32_16x16x32_f16 v[90:93], v[130:133], v[200:203], v[90:93]
	v_mfma_f32_16x16x32_f16 v[78:81], v[122:125], v[208:211], v[78:81]
	v_mfma_f32_16x16x32_f16 v[74:77], v[130:133], v[208:211], v[74:77]
	v_mfma_f32_16x16x32_f16 v[142:145], v[126:129], v[188:191], v[142:145]
	v_mfma_f32_16x16x32_f16 v[138:141], v[134:137], v[188:191], v[138:141]
	v_mfma_f32_16x16x32_f16 v[110:113], v[126:129], v[196:199], v[110:113]
	v_mfma_f32_16x16x32_f16 v[106:109], v[134:137], v[196:199], v[106:109]
	v_mfma_f32_16x16x32_f16 v[94:97], v[126:129], v[204:207], v[94:97]
	v_mfma_f32_16x16x32_f16 v[90:93], v[134:137], v[204:207], v[90:93]
	v_mfma_f32_16x16x32_f16 v[78:81], v[126:129], v[212:215], v[78:81]
	v_mfma_f32_16x16x32_f16 v[74:77], v[134:137], v[212:215], v[74:77]
	v_mfma_f32_16x16x32_f16 v[118:121], v[162:165], v[184:187], v[118:121]
	v_mfma_f32_16x16x32_f16 v[114:117], v[176:179], v[184:187], v[114:117]
	v_mfma_f32_16x16x32_f16 v[102:105], v[162:165], v[192:195], v[102:105]
	v_mfma_f32_16x16x32_f16 v[98:101], v[176:179], v[192:195], v[98:101]
	v_mfma_f32_16x16x32_f16 v[86:89], v[162:165], v[200:203], v[86:89]
	v_mfma_f32_16x16x32_f16 v[82:85], v[176:179], v[200:203], v[82:85]
	v_mfma_f32_16x16x32_f16 v[70:73], v[162:165], v[208:211], v[70:73]
	v_mfma_f32_16x16x32_f16 v[66:69], v[176:179], v[208:211], v[66:69]
	v_mfma_f32_16x16x32_f16 v[118:121], v[172:175], v[188:191], v[118:121]
	v_mfma_f32_16x16x32_f16 v[114:117], v[180:183], v[188:191], v[114:117]
	v_mfma_f32_16x16x32_f16 v[102:105], v[172:175], v[196:199], v[102:105]
	v_mfma_f32_16x16x32_f16 v[98:101], v[180:183], v[196:199], v[98:101]
	v_mfma_f32_16x16x32_f16 v[86:89], v[172:175], v[204:207], v[86:89]
	v_mfma_f32_16x16x32_f16 v[82:85], v[180:183], v[204:207], v[82:85]
	v_mfma_f32_16x16x32_f16 v[70:73], v[172:175], v[212:215], v[70:73]
	v_mfma_f32_16x16x32_f16 v[66:69], v[180:183], v[212:215], v[66:69]
	s_barrier
	s_add_i32 s50, s43, s31
	v_lshl_add_u64 v[216:217], s[24:25], 0, v[148:149]
	s_mov_b32 m0, s50
	global_load_lds_dwordx4 v[216:217], off
	s_add_i32 m0, s50, 0x2000
	s_add_u32 s50, s24, 0x40000
	v_lshl_add_u64 v[218:219], s[24:25], 0, v[152:153]
	s_addc_u32 s51, s25, 0
	s_add_i32 s52, s44, s31
	global_load_lds_dwordx4 v[218:219], off
	v_lshl_add_u64 v[222:223], s[26:27], 0, v[150:151]
	v_lshl_add_u64 v[220:221], s[26:27], 0, v[146:147]
	s_mov_b32 m0, s33
	s_nop 0
	global_load_lds_dwordx4 v[220:221], off
	s_mov_b32 m0, s34
	s_nop 0
	global_load_lds_dwordx4 v[222:223], off
	ds_read_b128 v[184:187], v170 offset:16384
	ds_read_b128 v[188:191], v170 offset:17408
	ds_read_b128 v[192:195], v170 offset:18432
	ds_read_b128 v[196:199], v170 offset:19456
	ds_read_b128 v[200:203], v170 offset:20480
	ds_read_b128 v[204:207], v170 offset:21504
	ds_read_b128 v[208:211], v170 offset:22528
	ds_read_b128 v[212:215], v170 offset:23552
	s_waitcnt vmcnt(6)
	s_waitcnt lgkmcnt(0)
	s_barrier
; #define GM_LDA(dst, b, h) do { _Pragma("unroll") for (int m = 0; m < 4; ++m) _Pragma("unroll") for (int k = 0; k < 2; ++k) dst[m][k] = *(const LAS s16x8*)(lds + GM_SA(b, h) + aoff + m * 2048 + k * 1024); } while (0)
; #define GM_LDB(dst, b, h) do { _Pragma("unroll") for (int n = 0; n < 2; ++n) _Pragma("unroll") for (int k = 0; k < 2; ++k) dst[n][k] = *(const LAS s16x8*)(lds + GM_SB(b, h) + boff + n * 2048 + k * 1024); } while (0)
; #define GM_MMA(ai, bj, At, Bt) do { __builtin_amdgcn_s_setprio(1); _Pragma("unroll") for (int m = 0; m < 4; ++m) _Pragma("unroll") for (int n = 0; n < 2; ++n) _Pragma("unroll") for (int k = 0; k < 2; ++k) \
;         acc[ai][bj][m][n] = mma16<BF>(Bt[n][k], At[m][k], acc[ai][bj][m][n]); __builtin_amdgcn_s_setprio(0); } while (0)
; #define GM_WAIT_V(n) asm volatile("s_waitcnt vmcnt(" #n ")" ::: "memory")
; #define GM_WAIT_L(n) asm volatile("s_waitcnt lgkmcnt(" #n ")" ::: "memory")
; #define GM_BAR __builtin_amdgcn_s_barrier()
; #define GM_SCHED __builtin_amdgcn_sched_barrier(0)
; #define GM_STA_H1(buf, p, o1) do { if constexpr (GATHER) GM_STAGE(buf, p, o1); else GM_STAGE(buf, (p) + hstepB, voffA); } while (0)
; template <bool BF, bool GATHER = false, class Epi, class Hook>
; __device__ __forceinline__ void gemm_phase(LAS unsigned char* lds, const Gemm g, const Order& S, const Epi& E, Hook& HK) {
;     ...
;             GM_WAIT_V(8); GM_WAIT_L(0); GM_BAR; GM_MMA(1, 0, At, B0); GM_MMA(1, 1, At, B1); GM_BAR; GM_SCHED;
;             GM_LDB(B0, 1, 0); GM_LDB(B1, 1, 1); GM_SCHED; GM_LDA(At, 1, 0); GM_STA_H1(GM_SA(0, 1), a2, s1);
;             GM_WAIT_V(8); GM_WAIT_L(0); GM_BAR; GM_MMA(0, 0, At, B0); GM_MMA(0, 1, At, B1); GM_BAR; GM_SCHED;
	s_waitcnt lgkmcnt(0)
	v_mfma_f32_16x16x32_f16 v[62:65], v[122:125], v[184:187], v[62:65]
	v_mfma_f32_16x16x32_f16 v[58:61], v[130:133], v[184:187], v[58:61]
	v_mfma_f32_16x16x32_f16 v[46:49], v[122:125], v[192:195], v[46:49]
	v_mfma_f32_16x16x32_f16 v[42:45], v[130:133], v[192:195], v[42:45]
	v_mfma_f32_16x16x32_f16 v[30:33], v[122:125], v[200:203], v[30:33]
	v_mfma_f32_16x16x32_f16 v[26:29], v[130:133], v[200:203], v[26:29]
	v_mfma_f32_16x16x32_f16 v[14:17], v[122:125], v[208:211], v[14:17]
	v_mfma_f32_16x16x32_f16 v[10:13], v[130:133], v[208:211], v[10:13]
	v_mfma_f32_16x16x32_f16 v[62:65], v[126:129], v[188:191], v[62:65]
	v_mfma_f32_16x16x32_f16 v[58:61], v[134:137], v[188:191], v[58:61]
	v_mfma_f32_16x16x32_f16 v[46:49], v[126:129], v[196:199], v[46:49]
	v_mfma_f32_16x16x32_f16 v[42:45], v[134:137], v[196:199], v[42:45]
	v_mfma_f32_16x16x32_f16 v[30:33], v[126:129], v[204:207], v[30:33]
	v_mfma_f32_16x16x32_f16 v[26:29], v[134:137], v[204:207], v[26:29]
	v_mfma_f32_16x16x32_f16 v[14:17], v[126:129], v[212:215], v[14:17]
	v_mfma_f32_16x16x32_f16 v[10:13], v[134:137], v[212:215], v[10:13]
	v_mfma_f32_16x16x32_f16 v[54:57], v[162:165], v[184:187], v[54:57]
	v_mfma_f32_16x16x32_f16 v[50:53], v[176:179], v[184:187], v[50:53]
	v_mfma_f32_16x16x32_f16 v[38:41], v[162:165], v[192:195], v[38:41]
	v_mfma_f32_16x16x32_f16 v[34:37], v[176:179], v[192:195], v[34:37]
	v_mfma_f32_16x16x32_f16 v[22:25], v[162:165], v[200:203], v[22:25]
	v_mfma_f32_16x16x32_f16 v[18:21], v[176:179], v[200:203], v[18:21]
	v_mfma_f32_16x16x32_f16 v[6:9], v[162:165], v[208:211], v[6:9]
	v_mfma_f32_16x16x32_f16 v[2:5], v[176:179], v[208:211], v[2:5]
	v_mfma_f32_16x16x32_f16 v[54:57], v[172:175], v[188:191], v[54:57]
	v_mfma_f32_16x16x32_f16 v[50:53], v[180:183], v[188:191], v[50:53]
	v_mfma_f32_16x16x32_f16 v[38:41], v[172:175], v[196:199], v[38:41]
	v_mfma_f32_16x16x32_f16 v[34:37], v[180:183], v[196:199], v[34:37]
	v_mfma_f32_16x16x32_f16 v[22:25], v[172:175], v[204:207], v[22:25]
	v_mfma_f32_16x16x32_f16 v[18:21], v[180:183], v[204:207], v[18:21]
	v_mfma_f32_16x16x32_f16 v[6:9], v[172:175], v[212:215], v[6:9]
	v_mfma_f32_16x16x32_f16 v[2:5], v[180:183], v[212:215], v[2:5]
	s_barrier
	s_add_u32 s26, s26, 0x40000
	s_addc_u32 s27, s27, 0
	s_add_u32 s98, s24, 0x40000
	s_addc_u32 s99, s25, 0
	v_lshl_add_u64 v[252:253], s[98:99], 0, v[148:149]
	s_add_i32 m0, s31, 0x14000
	s_nop 0
	global_load_lds_dwordx4 v[252:253], off
	v_lshl_add_u64 v[252:253], s[98:99], 0, v[152:153]
	s_add_i32 m0, s31, 0x16000
	s_nop 0
	global_load_lds_dwordx4 v[252:253], off
	s_mov_b32 m0, s35
	v_lshl_add_u64 v[224:225], s[26:27], 0, v[146:147]
	global_load_lds_dwordx4 v[224:225], off
	v_lshl_add_u64 v[224:225], s[26:27], 0, v[150:151]
	s_mov_b32 m0, s36
	s_nop 0
	global_load_lds_dwordx4 v[224:225], off
	s_mov_b32 s51, 0x1c000
	s_mov_b32 s50, 0x18000
	v_add_u32_e32 v244, s50, v166
	v_add_u32_e32 v245, s51, v166
	ds_read_b128 v[122:125], v244
	ds_read_b128 v[126:129], v244 offset:1024
	ds_read_b128 v[130:133], v244 offset:2048
	ds_read_b128 v[134:137], v244 offset:3072
	ds_read_b128 v[162:165], v245
	ds_read_b128 v[172:175], v245 offset:1024
	ds_read_b128 v[176:179], v245 offset:2048
	ds_read_b128 v[180:183], v245 offset:3072
	ds_read_b128 v[184:187], v170 offset:32768
	ds_read_b128 v[188:191], v170 offset:33792
	ds_read_b128 v[192:195], v170 offset:34816
	ds_read_b128 v[196:199], v170 offset:35840
	ds_read_b128 v[200:203], v170 offset:36864
	ds_read_b128 v[204:207], v170 offset:37888
	ds_read_b128 v[208:211], v170 offset:38912
	ds_read_b128 v[212:215], v170 offset:39936
	s_waitcnt vmcnt(8)
	s_waitcnt lgkmcnt(0)
	s_barrier
; #define GM_STAGE(bufoff, gbase, voff) do { _Pragma("unroll") for (int _i = 0; _i < 2; ++_i) \
;         __builtin_amdgcn_global_load_lds((const unsigned*)((const char*)(gbase) + (voff)[_i]), (LAS unsigned*)(lds + (bufoff) + ldsw + _i * 8192), 16, 0, 0); } while (0)
; #define GM_LDA(dst, b, h) do { _Pragma("unroll") for (int m = 0; m < 4; ++m) _Pragma("unroll") for (int k = 0; k < 2; ++k) dst[m][k] = *(const LAS s16x8*)(lds + GM_SA(b, h) + aoff + m * 2048 + k * 1024); } while (0)
; #define GM_MMA(ai, bj, At, Bt) do { __builtin_amdgcn_s_setprio(1); _Pragma("unroll") for (int m = 0; m < 4; ++m) _Pragma("unroll") for (int n = 0; n < 2; ++n) _Pragma("unroll") for (int k = 0; k < 2; ++k) \
;         acc[ai][bj][m][n] = mma16<BF>(Bt[n][k], At[m][k], acc[ai][bj][m][n]); __builtin_amdgcn_s_setprio(0); } while (0)
; #define GM_WAIT_V(n) asm volatile("s_waitcnt vmcnt(" #n ")" ::: "memory")
; #define GM_WAIT_L(n) asm volatile("s_waitcnt lgkmcnt(" #n ")" ::: "memory")
; #define GM_BAR __builtin_amdgcn_s_barrier()
; #define GM_SCHED __builtin_amdgcn_sched_barrier(0)
; #define GM_STA_H0(buf, p, o0) do { if constexpr (GATHER) GM_STAGE(buf, p, o0); else GM_STAGE(buf, p, voffA); } while (0)
; template <bool BF, bool GATHER = false, class Epi, class Hook>
; __device__ __forceinline__ void gemm_phase(LAS unsigned char* lds, const Gemm g, const Order& S, const Epi& E, Hook& HK) {
;     ...
;             GM_WAIT_V(8); GM_WAIT_L(0); GM_BAR; GM_MMA(0, 0, At, B0); GM_MMA(0, 1, At, B1); GM_BAR; GM_SCHED;
;             GM_LDA(At, 1, 1); GM_STAGE(GM_SB(1, 0), b3, voffB); GM_STAGE(GM_SB(1, 1), b3 + hstepB, voffB); GM_STA_H0(GM_SA(1, 0), a3, s0);
;             GM_WAIT_V(8); GM_WAIT_L(0); GM_BAR; GM_MMA(1, 0, At, B0); GM_MMA(1, 1, At, B1); GM_BAR; GM_SCHED;
;         }
	s_waitcnt lgkmcnt(0)
	v_mfma_f32_16x16x32_f16 v[142:145], v[122:125], v[184:187], v[142:145]
	v_mfma_f32_16x16x32_f16 v[138:141], v[130:133], v[184:187], v[138:141]
	v_mfma_f32_16x16x32_f16 v[110:113], v[122:125], v[192:195], v[110:113]
	v_mfma_f32_16x16x32_f16 v[106:109], v[130:133], v[192:195], v[106:109]
	v_mfma_f32_16x16x32_f16 v[94:97], v[122:125], v[200:203], v[94:97]
	v_mfma_f32_16x16x32_f16 v[90:93], v[130:133], v[200:203], v[90:93]
	v_mfma_f32_16x16x32_f16 v[78:81], v[122:125], v[208:211], v[78:81]
	v_mfma_f32_16x16x32_f16 v[74:77], v[130:133], v[208:211], v[74:77]
	v_mfma_f32_16x16x32_f16 v[142:145], v[126:129], v[188:191], v[142:145]
	v_mfma_f32_16x16x32_f16 v[138:141], v[134:137], v[188:191], v[138:141]
	v_mfma_f32_16x16x32_f16 v[110:113], v[126:129], v[196:199], v[110:113]
	v_mfma_f32_16x16x32_f16 v[106:109], v[134:137], v[196:199], v[106:109]
	v_mfma_f32_16x16x32_f16 v[94:97], v[126:129], v[204:207], v[94:97]
	v_mfma_f32_16x16x32_f16 v[90:93], v[134:137], v[204:207], v[90:93]
	v_mfma_f32_16x16x32_f16 v[78:81], v[126:129], v[212:215], v[78:81]
	v_mfma_f32_16x16x32_f16 v[74:77], v[134:137], v[212:215], v[74:77]
	v_mfma_f32_16x16x32_f16 v[118:121], v[162:165], v[184:187], v[118:121]
	v_mfma_f32_16x16x32_f16 v[114:117], v[176:179], v[184:187], v[114:117]
	v_mfma_f32_16x16x32_f16 v[102:105], v[162:165], v[192:195], v[102:105]
	v_mfma_f32_16x16x32_f16 v[98:101], v[176:179], v[192:195], v[98:101]
	v_mfma_f32_16x16x32_f16 v[86:89], v[162:165], v[200:203], v[86:89]
	v_mfma_f32_16x16x32_f16 v[82:85], v[176:179], v[200:203], v[82:85]
	v_mfma_f32_16x16x32_f16 v[70:73], v[162:165], v[208:211], v[70:73]
	v_mfma_f32_16x16x32_f16 v[66:69], v[176:179], v[208:211], v[66:69]
	v_mfma_f32_16x16x32_f16 v[118:121], v[172:175], v[188:191], v[118:121]
	v_mfma_f32_16x16x32_f16 v[114:117], v[180:183], v[188:191], v[114:117]
	v_mfma_f32_16x16x32_f16 v[102:105], v[172:175], v[196:199], v[102:105]
	v_mfma_f32_16x16x32_f16 v[98:101], v[180:183], v[196:199], v[98:101]
	v_mfma_f32_16x16x32_f16 v[86:89], v[172:175], v[204:207], v[86:89]
	v_mfma_f32_16x16x32_f16 v[82:85], v[180:183], v[204:207], v[82:85]
	v_mfma_f32_16x16x32_f16 v[70:73], v[172:175], v[212:215], v[70:73]
	v_mfma_f32_16x16x32_f16 v[66:69], v[180:183], v[212:215], v[66:69]
	s_barrier
	s_add_i32 s26, s50, s31
	v_lshl_add_u64 v[216:217], v[216:217], 0, s[10:11]
	s_mov_b32 m0, s26
	global_load_lds_dwordx4 v[216:217], off
	s_add_i32 m0, s26, 0x2000
	s_add_u32 s24, s24, 0x40080
	v_lshl_add_u64 v[216:217], v[218:219], 0, s[10:11]
	s_addc_u32 s25, s25, 0
	s_add_i32 s26, s51, s31
	global_load_lds_dwordx4 v[216:217], off
	v_lshl_add_u64 v[216:217], v[220:221], 0, s[10:11]
	s_mov_b32 m0, s40
	s_nop 0
	global_load_lds_dwordx4 v[216:217], off
	v_lshl_add_u64 v[216:217], v[222:223], 0, s[10:11]
	s_mov_b32 m0, s41
	s_nop 0
	global_load_lds_dwordx4 v[216:217], off
	ds_read_b128 v[184:187], v170 offset:49152
	ds_read_b128 v[188:191], v170 offset:50176
	ds_read_b128 v[192:195], v170 offset:51200
	ds_read_b128 v[196:199], v170 offset:52224
	ds_read_b128 v[200:203], v170 offset:53248
	ds_read_b128 v[204:207], v170 offset:54272
	ds_read_b128 v[208:211], v170 offset:55296
	ds_read_b128 v[212:215], v170 offset:56320
	s_waitcnt vmcnt(6)
	s_waitcnt lgkmcnt(0)
	s_barrier
	s_waitcnt lgkmcnt(0)
	v_mfma_f32_16x16x32_f16 v[62:65], v[122:125], v[184:187], v[62:65]
	v_mfma_f32_16x16x32_f16 v[58:61], v[130:133], v[184:187], v[58:61]
	v_mfma_f32_16x16x32_f16 v[46:49], v[122:125], v[192:195], v[46:49]
	v_mfma_f32_16x16x32_f16 v[42:45], v[130:133], v[192:195], v[42:45]
	v_mfma_f32_16x16x32_f16 v[30:33], v[122:125], v[200:203], v[30:33]
	v_mfma_f32_16x16x32_f16 v[26:29], v[130:133], v[200:203], v[26:29]
	v_mfma_f32_16x16x32_f16 v[14:17], v[122:125], v[208:211], v[14:17]
	v_mfma_f32_16x16x32_f16 v[10:13], v[130:133], v[208:211], v[10:13]
	v_mfma_f32_16x16x32_f16 v[62:65], v[126:129], v[188:191], v[62:65]
	v_mfma_f32_16x16x32_f16 v[58:61], v[134:137], v[188:191], v[58:61]
	v_mfma_f32_16x16x32_f16 v[46:49], v[126:129], v[196:199], v[46:49]
	v_mfma_f32_16x16x32_f16 v[42:45], v[134:137], v[196:199], v[42:45]
	v_mfma_f32_16x16x32_f16 v[30:33], v[126:129], v[204:207], v[30:33]
	v_mfma_f32_16x16x32_f16 v[26:29], v[134:137], v[204:207], v[26:29]
	v_mfma_f32_16x16x32_f16 v[14:17], v[126:129], v[212:215], v[14:17]
	v_mfma_f32_16x16x32_f16 v[10:13], v[134:137], v[212:215], v[10:13]
	v_mfma_f32_16x16x32_f16 v[54:57], v[162:165], v[184:187], v[54:57]
	v_mfma_f32_16x16x32_f16 v[50:53], v[176:179], v[184:187], v[50:53]
	v_mfma_f32_16x16x32_f16 v[38:41], v[162:165], v[192:195], v[38:41]
	v_mfma_f32_16x16x32_f16 v[34:37], v[176:179], v[192:195], v[34:37]
	v_mfma_f32_16x16x32_f16 v[22:25], v[162:165], v[200:203], v[22:25]
	v_mfma_f32_16x16x32_f16 v[18:21], v[176:179], v[200:203], v[18:21]
	v_mfma_f32_16x16x32_f16 v[6:9], v[162:165], v[208:211], v[6:9]
	v_mfma_f32_16x16x32_f16 v[2:5], v[176:179], v[208:211], v[2:5]
	v_mfma_f32_16x16x32_f16 v[54:57], v[172:175], v[188:191], v[54:57]
	v_mfma_f32_16x16x32_f16 v[50:53], v[180:183], v[188:191], v[50:53]
	v_mfma_f32_16x16x32_f16 v[38:41], v[172:175], v[196:199], v[38:41]
	v_mfma_f32_16x16x32_f16 v[34:37], v[180:183], v[196:199], v[34:37]
	v_mfma_f32_16x16x32_f16 v[22:25], v[172:175], v[204:207], v[22:25]
	v_mfma_f32_16x16x32_f16 v[18:21], v[180:183], v[204:207], v[18:21]
	v_mfma_f32_16x16x32_f16 v[6:9], v[172:175], v[212:215], v[6:9]
	v_mfma_f32_16x16x32_f16 v[2:5], v[180:183], v[212:215], v[2:5]
	s_barrier
	s_add_i32 s49, s49, 2
	s_add_u32 s22, s22, 0x100
	s_addc_u32 s23, s23, 0
	s_add_u32 s47, s47, 0x100
	s_addc_u32 s48, s48, 0
	s_cmp_gt_u32 s49, 13
	s_cbranch_scc0 .LBB0_1480
	s_and_b64 vcc, exec, s[12:13]
	s_cbranch_vccz .LBB0_1483
	s_barrier

; #define GM_STAGE(bufoff, gbase, voff) do { _Pragma("unroll") for (int _i = 0; _i < 2; ++_i) \
;         __builtin_amdgcn_global_load_lds((const unsigned*)((const char*)(gbase) + (voff)[_i]), (LAS unsigned*)(lds + (bufoff) + ldsw + _i * 8192), 16, 0, 0); } while (0)
; #define GM_WAIT_V(n) asm volatile("s_waitcnt vmcnt(" #n ")" ::: "memory")
; #define GM_BAR __builtin_amdgcn_s_barrier()
; #define GM_STA_H0(buf, p, o0) do { if constexpr (GATHER) GM_STAGE(buf, p, o0); else GM_STAGE(buf, p, voffA); } while (0)
; template <bool BF, bool GATHER = false, class Epi, class Hook>
; __device__ __forceinline__ void gemm_phase(LAS unsigned char* lds, const Gemm g, const Order& S, const Epi& E, Hook& HK) {
;     ...
;     const unsigned ldsw = (unsigned)wid * 1024u;
;     const int aoff = lds_byte(wr * 64 + fr, fq * 8), boff = lds_byte(wc * 32 + fr, fq * 8);
;     ...
;     GM_WAIT_V(2); GM_BAR;
;     GM_STAGE(GM_SB(1, 0), cB + kstep, voffB); GM_STA_H0(GM_SA(1, 0), cA + kstep, gA0); GM_STAGE(GM_SB(1, 1), cB + hstepB + kstep, voffB);
;     GM_WAIT_V(6); GM_BAR;
.LBB0_1850:
	s_lshl_b32 s18, s6, 6
	s_lshl_b32 s14, s6, 13
	s_lshl_b32 s6, s7, 5
	s_mov_b64 s[12:13], 0x80
	s_and_b32 s19, s6, 0x60
	s_add_i32 m0, s29, 0x18000
	v_lshl_add_u64 v[8:9], v[8:9], 0, s[12:13]
	s_lshl_b32 s15, s19, 7
	s_ashr_i32 s35, s92, 31
	s_waitcnt vmcnt(2)
	s_barrier
	global_load_lds_dwordx4 v[8:9], off
	v_lshl_add_u64 v[6:7], v[6:7], 0, s[12:13]
	s_add_i32 m0, s29, 0x1a000
	s_add_i32 s36, s29, 0x8000
	s_add_i32 s37, s29, 0xa000
	global_load_lds_dwordx4 v[6:7], off
	v_lshl_add_u64 v[2:3], v[2:3], 0, s[12:13]
	s_mov_b32 m0, s36
	s_add_u32 s6, s22, 0xb0080
	global_load_lds_dwordx4 v[2:3], off
	v_lshl_add_u64 v[2:3], v[4:5], 0, s[12:13]
	s_mov_b32 m0, s37
	s_addc_u32 s7, s23, 0
	global_load_lds_dwordx4 v[2:3], off
	v_lshlrev_b32_e32 v5, 2, v10
	v_lshrrev_b32_e32 v3, 1, v10
	v_and_b32_e32 v3, 24, v3
	v_and_b32_e32 v2, 15, v10
	v_lshlrev_b32_e32 v4, 1, v3
	v_lshl_or_b32 v4, v2, 6, v4
	v_and_b32_e32 v5, 32, v5
	s_cmpk_lt_u32 s4, 0x100
	v_bitop3_b32 v6, v4, s14, v5 bitop3:0xde
	v_bitop3_b32 v150, v4, s15, v5 bitop3:0xde
	s_cselect_b64 s[14:15], -1, 0
	s_lshl_b32 s4, s92, 3
	v_mov_b32_e32 v4, 0xcf
	s_and_b32 s41, s4, 8
	s_ashr_i32 s4, s92, 5
	v_or_b32_e32 v1, s18, v2
	v_bitop3_b32 v151, s18, v4, v2 bitop3:0xc8
	s_add_i32 s41, s41, s4
	v_or_b32_e32 v152, s19, v3
	v_lshrrev_b32_e32 v3, 1, v11
	v_mul_lo_u32 v2, v13, s5
	s_mov_b32 s4, 0xb000
	v_mad_u64_u32 v[2:3], s[18:19], v3, s4, v[2:3]
	v_or_b32_e32 v2, v2, v12
	s_mov_b64 s[6:7], 0xb0080
	v_add_lshl_u32 v2, v2, v14, 1
	v_mov_b32_e32 v3, v133
	v_lshl_add_u64 v[138:139], v[2:3], 0, s[6:7]
	v_lshrrev_b32_e32 v3, 1, v15
	v_mul_lo_u32 v2, v16, s5
	v_mad_u64_u32 v[2:3], s[4:5], v3, s4, v[2:3]
	s_waitcnt vmcnt(4)
	v_or_b32_e32 v2, v2, v17
	v_add_lshl_u32 v2, v2, v18, 1
	v_mov_b32_e32 v3, v133
	s_add_i32 s43, 0, 0x10000
	s_add_i32 s44, 0, 0x14000
	s_movk_i32 s38, 0xcf
	s_ashr_i32 s39, s96, 31
	s_bfe_u32 s40, s92, 0x20001
	s_bfe_u32 s42, s92, 0x20003
	v_lshl_add_u64 v[140:141], v[2:3], 0, s[6:7]
	v_mov_b64_e32 v[142:143], 0x400
	v_mov_b64_e32 v[144:145], 0x3ff
	v_add_u32_e32 v153, s43, v150
	v_add_u32_e32 v154, s44, v150
	v_add_u32_e32 v155, 0, v6
	s_movk_i32 s45, 0xdf
	s_movk_i32 s46, 0xef
	s_movk_i32 s47, 0xff
	s_barrier
	s_branch .LBB0_1853

; #define GM_STAGE(bufoff, gbase, voff) do { _Pragma("unroll") for (int _i = 0; _i < 2; ++_i) \
;         __builtin_amdgcn_global_load_lds((const unsigned*)((const char*)(gbase) + (voff)[_i]), (LAS unsigned*)(lds + (bufoff) + ldsw + _i * 8192), 16, 0, 0); } while (0)
; #define GM_LDA(dst, b, h) do { _Pragma("unroll") for (int m = 0; m < 4; ++m) _Pragma("unroll") for (int k = 0; k < 2; ++k) dst[m][k] = *(const LAS s16x8*)(lds + GM_SA(b, h) + aoff + m * 2048 + k * 1024); } while (0)
; #define GM_LDB(dst, b, h) do { _Pragma("unroll") for (int n = 0; n < 2; ++n) _Pragma("unroll") for (int k = 0; k < 2; ++k) dst[n][k] = *(const LAS s16x8*)(lds + GM_SB(b, h) + boff + n * 2048 + k * 1024); } while (0)
; #define GM_MMA(ai, bj, At, Bt) do { __builtin_amdgcn_s_setprio(1); _Pragma("unroll") for (int m = 0; m < 4; ++m) _Pragma("unroll") for (int n = 0; n < 2; ++n) _Pragma("unroll") for (int k = 0; k < 2; ++k) \
;         acc[ai][bj][m][n] = mma16<BF>(Bt[n][k], At[m][k], acc[ai][bj][m][n]); __builtin_amdgcn_s_setprio(0); } while (0)
; #define GM_WAIT_V(n) asm volatile("s_waitcnt vmcnt(" #n ")" ::: "memory")
; #define GM_WAIT_L(n) asm volatile("s_waitcnt lgkmcnt(" #n ")" ::: "memory")
; #define GM_BAR __builtin_amdgcn_s_barrier()
; template <bool BF, bool GATHER = false, class Epi, class Hook>
; __device__ __forceinline__ void gemm_phase(LAS unsigned char* lds, const Gemm g, const Order& S, const Epi& E, Hook& HK) {
;     ...
;             const char* a1 = cA + (size_t)(t + 1) * kstep;
;             const char* a2 = last ? nA : cA + (size_t)(t + 2) * kstep; const char* b2 = last ? nB : cB + (size_t)(t + 2) * kstep;
;             const char* a3 = a2 + kstep; const char* b3 = b2 + kstep;
;             unsigned s0[2], s1[2];
;             if constexpr (GATHER) { s0[0] = last ? nA0[0] : gA0[0]; s0[1] = last ? nA0[1] : gA0[1]; s1[0] = last ? nA1[0] : gA1[0]; s1[1] = last ? nA1[1] : gA1[1]; }
;             GM_LDB(B0, 0, 0); GM_LDB(B1, 0, 1); GM_SCHED; GM_LDA(At, 0, 0); GM_STA_H1(GM_SA(1, 1), a1, gA1);
;             GM_WAIT_V(8); GM_WAIT_L(0); GM_BAR; GM_MMA(0, 0, At, B0); GM_MMA(0, 1, At, B1); GM_BAR; GM_SCHED;
;             GM_LDA(At, 0, 1); GM_STAGE(GM_SB(0, 0), b2, voffB); GM_STAGE(GM_SB(0, 1), b2 + hstepB, voffB); GM_STA_H0(GM_SA(0, 0), a2, s0);
;             GM_WAIT_V(8); GM_WAIT_L(0); GM_BAR; GM_MMA(1, 0, At, B0); GM_MMA(1, 1, At, B1); GM_BAR; GM_SCHED;
.LBB0_1867:
	s_add_u32 s22, s2, 0x100
	s_addc_u32 s23, s3, 0
	s_cmp_eq_u32 s52, 40
	s_cselect_b32 s27, s7, s23
	s_cselect_b32 s26, s6, s22
	s_cselect_b32 s25, s21, s51
	s_cselect_b32 s24, s20, s50
	s_add_u32 s98, s50, 0xaff80
	s_addc_u32 s99, s51, 0
	v_lshl_add_u64 v[252:253], s[98:99], 0, v[132:133]
	s_add_i32 m0, s28, 0x1c000
	s_nop 0
	global_load_lds_dwordx4 v[252:253], off
	v_lshl_add_u64 v[252:253], s[98:99], 0, v[136:137]
	s_add_i32 m0, s28, 0x1e000
	s_nop 0
	global_load_lds_dwordx4 v[252:253], off
	v_lshl_add_u64 v[216:217], s[2:3], 0, v[138:139]
	s_add_i32 m0, s29, 0xc000
	global_load_lds_dwordx4 v[216:217], off
	v_lshl_add_u64 v[216:217], s[2:3], 0, v[140:141]
	s_add_i32 m0, s29, 0xe000
	s_nop 0
	global_load_lds_dwordx4 v[216:217], off
	ds_read_b128 v[146:149], v153
	ds_read_b128 v[156:159], v153 offset:1024
	ds_read_b128 v[160:163], v153 offset:2048
	ds_read_b128 v[164:167], v153 offset:3072
	ds_read_b128 v[168:171], v154
	ds_read_b128 v[172:175], v154 offset:1024
	ds_read_b128 v[176:179], v154 offset:2048
	ds_read_b128 v[180:183], v154 offset:3072
	ds_read_b128 v[184:187], v155
	ds_read_b128 v[188:191], v155 offset:1024
	ds_read_b128 v[192:195], v155 offset:2048
	ds_read_b128 v[196:199], v155 offset:3072
	ds_read_b128 v[200:203], v155 offset:4096
	ds_read_b128 v[204:207], v155 offset:5120
	ds_read_b128 v[208:211], v155 offset:6144
	ds_read_b128 v[212:215], v155 offset:7168
	s_waitcnt vmcnt(8)
	s_waitcnt lgkmcnt(0)
	s_barrier
	s_waitcnt lgkmcnt(0)
	v_mfma_f32_16x16x32_bf16 v[126:129], v[146:149], v[184:187], v[126:129]
	v_mfma_f32_16x16x32_bf16 v[122:125], v[160:163], v[184:187], v[122:125]
	v_mfma_f32_16x16x32_bf16 v[110:113], v[146:149], v[192:195], v[110:113]
	v_mfma_f32_16x16x32_bf16 v[106:109], v[160:163], v[192:195], v[106:109]
	v_mfma_f32_16x16x32_bf16 v[94:97], v[146:149], v[200:203], v[94:97]
	v_mfma_f32_16x16x32_bf16 v[90:93], v[160:163], v[200:203], v[90:93]
	v_mfma_f32_16x16x32_bf16 v[78:81], v[146:149], v[208:211], v[78:81]
	v_mfma_f32_16x16x32_bf16 v[74:77], v[160:163], v[208:211], v[74:77]
	v_mfma_f32_16x16x32_bf16 v[126:129], v[156:159], v[188:191], v[126:129]
	v_mfma_f32_16x16x32_bf16 v[122:125], v[164:167], v[188:191], v[122:125]
	v_mfma_f32_16x16x32_bf16 v[110:113], v[156:159], v[196:199], v[110:113]
	v_mfma_f32_16x16x32_bf16 v[106:109], v[164:167], v[196:199], v[106:109]
	v_mfma_f32_16x16x32_bf16 v[94:97], v[156:159], v[204:207], v[94:97]
	v_mfma_f32_16x16x32_bf16 v[90:93], v[164:167], v[204:207], v[90:93]
	v_mfma_f32_16x16x32_bf16 v[78:81], v[156:159], v[212:215], v[78:81]
	v_mfma_f32_16x16x32_bf16 v[74:77], v[164:167], v[212:215], v[74:77]
	v_mfma_f32_16x16x32_bf16 v[118:121], v[168:171], v[184:187], v[118:121]
	v_mfma_f32_16x16x32_bf16 v[114:117], v[176:179], v[184:187], v[114:117]
	v_mfma_f32_16x16x32_bf16 v[102:105], v[168:171], v[192:195], v[102:105]
	v_mfma_f32_16x16x32_bf16 v[98:101], v[176:179], v[192:195], v[98:101]
	v_mfma_f32_16x16x32_bf16 v[86:89], v[168:171], v[200:203], v[86:89]
	v_mfma_f32_16x16x32_bf16 v[82:85], v[176:179], v[200:203], v[82:85]
	v_mfma_f32_16x16x32_bf16 v[70:73], v[168:171], v[208:211], v[70:73]
	v_mfma_f32_16x16x32_bf16 v[66:69], v[176:179], v[208:211], v[66:69]
	v_mfma_f32_16x16x32_bf16 v[118:121], v[172:175], v[188:191], v[118:121]
	v_mfma_f32_16x16x32_bf16 v[114:117], v[180:183], v[188:191], v[114:117]
	v_mfma_f32_16x16x32_bf16 v[102:105], v[172:175], v[196:199], v[102:105]
	v_mfma_f32_16x16x32_bf16 v[98:101], v[180:183], v[196:199], v[98:101]
	v_mfma_f32_16x16x32_bf16 v[86:89], v[172:175], v[204:207], v[86:89]
	v_mfma_f32_16x16x32_bf16 v[82:85], v[180:183], v[204:207], v[82:85]
	v_mfma_f32_16x16x32_bf16 v[70:73], v[172:175], v[212:215], v[70:73]
	v_mfma_f32_16x16x32_bf16 v[66:69], v[180:183], v[212:215], v[66:69]
	s_barrier
	s_add_i32 s2, s43, s28
	v_lshl_add_u64 v[216:217], s[24:25], 0, v[132:133]
	s_mov_b32 m0, s2
	global_load_lds_dwordx4 v[216:217], off
	s_add_i32 m0, s2, 0x2000
	s_add_u32 s2, s24, 0xb0000
	v_lshl_add_u64 v[218:219], s[24:25], 0, v[136:137]
	s_addc_u32 s3, s25, 0
	s_add_i32 s53, s44, s28
	global_load_lds_dwordx4 v[218:219], off
	v_lshl_add_u64 v[222:223], s[26:27], 0, v[134:135]
	v_lshl_add_u64 v[220:221], s[26:27], 0, v[130:131]
	s_mov_b32 m0, s29
	s_nop 0
	global_load_lds_dwordx4 v[220:221], off
	s_mov_b32 m0, s30
	s_nop 0
	global_load_lds_dwordx4 v[222:223], off
	ds_read_b128 v[184:187], v155 offset:16384
	ds_read_b128 v[188:191], v155 offset:17408
	ds_read_b128 v[192:195], v155 offset:18432
	ds_read_b128 v[196:199], v155 offset:19456
	ds_read_b128 v[200:203], v155 offset:20480
	ds_read_b128 v[204:207], v155 offset:21504
	ds_read_b128 v[208:211], v155 offset:22528
	ds_read_b128 v[212:215], v155 offset:23552
	s_waitcnt vmcnt(6)
	s_waitcnt lgkmcnt(0)
	s_barrier
; #define GM_LDA(dst, b, h) do { _Pragma("unroll") for (int m = 0; m < 4; ++m) _Pragma("unroll") for (int k = 0; k < 2; ++k) dst[m][k] = *(const LAS s16x8*)(lds + GM_SA(b, h) + aoff + m * 2048 + k * 1024); } while (0)
; #define GM_LDB(dst, b, h) do { _Pragma("unroll") for (int n = 0; n < 2; ++n) _Pragma("unroll") for (int k = 0; k < 2; ++k) dst[n][k] = *(const LAS s16x8*)(lds + GM_SB(b, h) + boff + n * 2048 + k * 1024); } while (0)
; #define GM_MMA(ai, bj, At, Bt) do { __builtin_amdgcn_s_setprio(1); _Pragma("unroll") for (int m = 0; m < 4; ++m) _Pragma("unroll") for (int n = 0; n < 2; ++n) _Pragma("unroll") for (int k = 0; k < 2; ++k) \
;         acc[ai][bj][m][n] = mma16<BF>(Bt[n][k], At[m][k], acc[ai][bj][m][n]); __builtin_amdgcn_s_setprio(0); } while (0)
; #define GM_WAIT_V(n) asm volatile("s_waitcnt vmcnt(" #n ")" ::: "memory")
; #define GM_WAIT_L(n) asm volatile("s_waitcnt lgkmcnt(" #n ")" ::: "memory")
; #define GM_BAR __builtin_amdgcn_s_barrier()
; #define GM_SCHED __builtin_amdgcn_sched_barrier(0)
; #define GM_STA_H1(buf, p, o1) do { if constexpr (GATHER) GM_STAGE(buf, p, o1); else GM_STAGE(buf, (p) + hstepB, voffA); } while (0)
; template <bool BF, bool GATHER = false, class Epi, class Hook>
; __device__ __forceinline__ void gemm_phase(LAS unsigned char* lds, const Gemm g, const Order& S, const Epi& E, Hook& HK) {
;     ...
;             GM_WAIT_V(8); GM_WAIT_L(0); GM_BAR; GM_MMA(1, 0, At, B0); GM_MMA(1, 1, At, B1); GM_BAR; GM_SCHED;
;             GM_LDB(B0, 1, 0); GM_LDB(B1, 1, 1); GM_SCHED; GM_LDA(At, 1, 0); GM_STA_H1(GM_SA(0, 1), a2, s1);
;             GM_WAIT_V(8); GM_WAIT_L(0); GM_BAR; GM_MMA(0, 0, At, B0); GM_MMA(0, 1, At, B1); GM_BAR; GM_SCHED;
	s_waitcnt lgkmcnt(0)
	v_mfma_f32_16x16x32_bf16 v[62:65], v[146:149], v[184:187], v[62:65]
	v_mfma_f32_16x16x32_bf16 v[58:61], v[160:163], v[184:187], v[58:61]
	v_mfma_f32_16x16x32_bf16 v[46:49], v[146:149], v[192:195], v[46:49]
	v_mfma_f32_16x16x32_bf16 v[42:45], v[160:163], v[192:195], v[42:45]
	v_mfma_f32_16x16x32_bf16 v[30:33], v[146:149], v[200:203], v[30:33]
	v_mfma_f32_16x16x32_bf16 v[26:29], v[160:163], v[200:203], v[26:29]
	v_mfma_f32_16x16x32_bf16 v[14:17], v[146:149], v[208:211], v[14:17]
	v_mfma_f32_16x16x32_bf16 v[10:13], v[160:163], v[208:211], v[10:13]
	v_mfma_f32_16x16x32_bf16 v[62:65], v[156:159], v[188:191], v[62:65]
	v_mfma_f32_16x16x32_bf16 v[58:61], v[164:167], v[188:191], v[58:61]
	v_mfma_f32_16x16x32_bf16 v[46:49], v[156:159], v[196:199], v[46:49]
	v_mfma_f32_16x16x32_bf16 v[42:45], v[164:167], v[196:199], v[42:45]
	v_mfma_f32_16x16x32_bf16 v[30:33], v[156:159], v[204:207], v[30:33]
	v_mfma_f32_16x16x32_bf16 v[26:29], v[164:167], v[204:207], v[26:29]
	v_mfma_f32_16x16x32_bf16 v[14:17], v[156:159], v[212:215], v[14:17]
	v_mfma_f32_16x16x32_bf16 v[10:13], v[164:167], v[212:215], v[10:13]
	v_mfma_f32_16x16x32_bf16 v[54:57], v[168:171], v[184:187], v[54:57]
	v_mfma_f32_16x16x32_bf16 v[50:53], v[176:179], v[184:187], v[50:53]
	v_mfma_f32_16x16x32_bf16 v[38:41], v[168:171], v[192:195], v[38:41]
	v_mfma_f32_16x16x32_bf16 v[34:37], v[176:179], v[192:195], v[34:37]
	v_mfma_f32_16x16x32_bf16 v[22:25], v[168:171], v[200:203], v[22:25]
	v_mfma_f32_16x16x32_bf16 v[18:21], v[176:179], v[200:203], v[18:21]
	v_mfma_f32_16x16x32_bf16 v[6:9], v[168:171], v[208:211], v[6:9]
	v_mfma_f32_16x16x32_bf16 v[2:5], v[176:179], v[208:211], v[2:5]
	v_mfma_f32_16x16x32_bf16 v[54:57], v[172:175], v[188:191], v[54:57]
	v_mfma_f32_16x16x32_bf16 v[50:53], v[180:183], v[188:191], v[50:53]
	v_mfma_f32_16x16x32_bf16 v[38:41], v[172:175], v[196:199], v[38:41]
	v_mfma_f32_16x16x32_bf16 v[34:37], v[180:183], v[196:199], v[34:37]
	v_mfma_f32_16x16x32_bf16 v[22:25], v[172:175], v[204:207], v[22:25]
	v_mfma_f32_16x16x32_bf16 v[18:21], v[180:183], v[204:207], v[18:21]
	v_mfma_f32_16x16x32_bf16 v[6:9], v[172:175], v[212:215], v[6:9]
	v_mfma_f32_16x16x32_bf16 v[2:5], v[180:183], v[212:215], v[2:5]
	s_barrier
	s_add_u32 s2, s26, 0xb0000
	s_addc_u32 s3, s27, 0
	s_add_u32 s98, s24, 0xb0000
	s_addc_u32 s99, s25, 0
	v_lshl_add_u64 v[252:253], s[98:99], 0, v[132:133]
	s_add_i32 m0, s28, 0x14000
	s_nop 0
	global_load_lds_dwordx4 v[252:253], off
	v_lshl_add_u64 v[252:253], s[98:99], 0, v[136:137]
	s_add_i32 m0, s28, 0x16000
	s_nop 0
	global_load_lds_dwordx4 v[252:253], off
	s_mov_b32 m0, s31
	v_lshl_add_u64 v[224:225], s[2:3], 0, v[130:131]
	global_load_lds_dwordx4 v[224:225], off
	v_lshl_add_u64 v[224:225], s[2:3], 0, v[134:135]
	s_mov_b32 m0, s33
	s_nop 0
	global_load_lds_dwordx4 v[224:225], off
	s_mov_b32 s54, 0x1c000
	s_mov_b32 s53, 0x18000
	v_add_u32_e32 v244, s53, v150
	v_add_u32_e32 v245, s54, v150
	ds_read_b128 v[146:149], v244
	ds_read_b128 v[156:159], v244 offset:1024
	ds_read_b128 v[160:163], v244 offset:2048
	ds_read_b128 v[164:167], v244 offset:3072
	ds_read_b128 v[168:171], v245
	ds_read_b128 v[172:175], v245 offset:1024
	ds_read_b128 v[176:179], v245 offset:2048
	ds_read_b128 v[180:183], v245 offset:3072
	ds_read_b128 v[184:187], v155 offset:32768
	ds_read_b128 v[188:191], v155 offset:33792
	ds_read_b128 v[192:195], v155 offset:34816
	ds_read_b128 v[196:199], v155 offset:35840
	ds_read_b128 v[200:203], v155 offset:36864
	ds_read_b128 v[204:207], v155 offset:37888
	ds_read_b128 v[208:211], v155 offset:38912
	ds_read_b128 v[212:215], v155 offset:39936
	s_waitcnt vmcnt(8)
	s_waitcnt lgkmcnt(0)
	s_barrier
; #define GM_STAGE(bufoff, gbase, voff) do { _Pragma("unroll") for (int _i = 0; _i < 2; ++_i) \
;         __builtin_amdgcn_global_load_lds((const unsigned*)((const char*)(gbase) + (voff)[_i]), (LAS unsigned*)(lds + (bufoff) + ldsw + _i * 8192), 16, 0, 0); } while (0)
; #define GM_LDA(dst, b, h) do { _Pragma("unroll") for (int m = 0; m < 4; ++m) _Pragma("unroll") for (int k = 0; k < 2; ++k) dst[m][k] = *(const LAS s16x8*)(lds + GM_SA(b, h) + aoff + m * 2048 + k * 1024); } while (0)
; #define GM_MMA(ai, bj, At, Bt) do { __builtin_amdgcn_s_setprio(1); _Pragma("unroll") for (int m = 0; m < 4; ++m) _Pragma("unroll") for (int n = 0; n < 2; ++n) _Pragma("unroll") for (int k = 0; k < 2; ++k) \
;         acc[ai][bj][m][n] = mma16<BF>(Bt[n][k], At[m][k], acc[ai][bj][m][n]); __builtin_amdgcn_s_setprio(0); } while (0)
; #define GM_WAIT_V(n) asm volatile("s_waitcnt vmcnt(" #n ")" ::: "memory")
; #define GM_WAIT_L(n) asm volatile("s_waitcnt lgkmcnt(" #n ")" ::: "memory")
; #define GM_BAR __builtin_amdgcn_s_barrier()
; #define GM_SCHED __builtin_amdgcn_sched_barrier(0)
; #define GM_STA_H0(buf, p, o0) do { if constexpr (GATHER) GM_STAGE(buf, p, o0); else GM_STAGE(buf, p, voffA); } while (0)
; template <bool BF, bool GATHER = false, class Epi, class Hook>
; __device__ __forceinline__ void gemm_phase(LAS unsigned char* lds, const Gemm g, const Order& S, const Epi& E, Hook& HK) {
;     ...
;             GM_WAIT_V(8); GM_WAIT_L(0); GM_BAR; GM_MMA(0, 0, At, B0); GM_MMA(0, 1, At, B1); GM_BAR; GM_SCHED;
;             GM_LDA(At, 1, 1); GM_STAGE(GM_SB(1, 0), b3, voffB); GM_STAGE(GM_SB(1, 1), b3 + hstepB, voffB); GM_STA_H0(GM_SA(1, 0), a3, s0);
;             GM_WAIT_V(8); GM_WAIT_L(0); GM_BAR; GM_MMA(1, 0, At, B0); GM_MMA(1, 1, At, B1); GM_BAR; GM_SCHED;
;         }
	s_waitcnt lgkmcnt(0)
	v_mfma_f32_16x16x32_bf16 v[126:129], v[146:149], v[184:187], v[126:129]
	v_mfma_f32_16x16x32_bf16 v[122:125], v[160:163], v[184:187], v[122:125]
	v_mfma_f32_16x16x32_bf16 v[110:113], v[146:149], v[192:195], v[110:113]
	v_mfma_f32_16x16x32_bf16 v[106:109], v[160:163], v[192:195], v[106:109]
	v_mfma_f32_16x16x32_bf16 v[94:97], v[146:149], v[200:203], v[94:97]
	v_mfma_f32_16x16x32_bf16 v[90:93], v[160:163], v[200:203], v[90:93]
	v_mfma_f32_16x16x32_bf16 v[78:81], v[146:149], v[208:211], v[78:81]
	v_mfma_f32_16x16x32_bf16 v[74:77], v[160:163], v[208:211], v[74:77]
	v_mfma_f32_16x16x32_bf16 v[126:129], v[156:159], v[188:191], v[126:129]
	v_mfma_f32_16x16x32_bf16 v[122:125], v[164:167], v[188:191], v[122:125]
	v_mfma_f32_16x16x32_bf16 v[110:113], v[156:159], v[196:199], v[110:113]
	v_mfma_f32_16x16x32_bf16 v[106:109], v[164:167], v[196:199], v[106:109]
	v_mfma_f32_16x16x32_bf16 v[94:97], v[156:159], v[204:207], v[94:97]
	v_mfma_f32_16x16x32_bf16 v[90:93], v[164:167], v[204:207], v[90:93]
	v_mfma_f32_16x16x32_bf16 v[78:81], v[156:159], v[212:215], v[78:81]
	v_mfma_f32_16x16x32_bf16 v[74:77], v[164:167], v[212:215], v[74:77]
	v_mfma_f32_16x16x32_bf16 v[118:121], v[168:171], v[184:187], v[118:121]
	v_mfma_f32_16x16x32_bf16 v[114:117], v[176:179], v[184:187], v[114:117]
	v_mfma_f32_16x16x32_bf16 v[102:105], v[168:171], v[192:195], v[102:105]
	v_mfma_f32_16x16x32_bf16 v[98:101], v[176:179], v[192:195], v[98:101]
	v_mfma_f32_16x16x32_bf16 v[86:89], v[168:171], v[200:203], v[86:89]
	v_mfma_f32_16x16x32_bf16 v[82:85], v[176:179], v[200:203], v[82:85]
	v_mfma_f32_16x16x32_bf16 v[70:73], v[168:171], v[208:211], v[70:73]
	v_mfma_f32_16x16x32_bf16 v[66:69], v[176:179], v[208:211], v[66:69]
	v_mfma_f32_16x16x32_bf16 v[118:121], v[172:175], v[188:191], v[118:121]
	v_mfma_f32_16x16x32_bf16 v[114:117], v[180:183], v[188:191], v[114:117]
	v_mfma_f32_16x16x32_bf16 v[102:105], v[172:175], v[196:199], v[102:105]
	v_mfma_f32_16x16x32_bf16 v[98:101], v[180:183], v[196:199], v[98:101]
	v_mfma_f32_16x16x32_bf16 v[86:89], v[172:175], v[204:207], v[86:89]
	v_mfma_f32_16x16x32_bf16 v[82:85], v[180:183], v[204:207], v[82:85]
	v_mfma_f32_16x16x32_bf16 v[70:73], v[172:175], v[212:215], v[70:73]
	v_mfma_f32_16x16x32_bf16 v[66:69], v[180:183], v[212:215], v[66:69]
	s_barrier
	s_add_i32 s2, s53, s28
	v_lshl_add_u64 v[216:217], v[216:217], 0, s[12:13]
	s_mov_b32 m0, s2
	global_load_lds_dwordx4 v[216:217], off
	s_add_i32 m0, s2, 0x2000
	s_add_u32 s2, s24, 0xb0080
	v_lshl_add_u64 v[216:217], v[218:219], 0, s[12:13]
	s_addc_u32 s3, s25, 0
	s_add_i32 s24, s54, s28
	global_load_lds_dwordx4 v[216:217], off
	v_lshl_add_u64 v[216:217], v[220:221], 0, s[12:13]
	s_mov_b32 m0, s36
	s_nop 0
	global_load_lds_dwordx4 v[216:217], off
	v_lshl_add_u64 v[216:217], v[222:223], 0, s[12:13]
	s_mov_b32 m0, s37
	s_nop 0
	global_load_lds_dwordx4 v[216:217], off
	ds_read_b128 v[184:187], v155 offset:49152
	ds_read_b128 v[188:191], v155 offset:50176
	ds_read_b128 v[192:195], v155 offset:51200
	ds_read_b128 v[196:199], v155 offset:52224
	ds_read_b128 v[200:203], v155 offset:53248
	ds_read_b128 v[204:207], v155 offset:54272
	ds_read_b128 v[208:211], v155 offset:55296
	ds_read_b128 v[212:215], v155 offset:56320
	s_waitcnt vmcnt(6)
	s_waitcnt lgkmcnt(0)
	s_barrier
	s_waitcnt lgkmcnt(0)
	v_mfma_f32_16x16x32_bf16 v[62:65], v[146:149], v[184:187], v[62:65]
	v_mfma_f32_16x16x32_bf16 v[58:61], v[160:163], v[184:187], v[58:61]
	v_mfma_f32_16x16x32_bf16 v[46:49], v[146:149], v[192:195], v[46:49]
	v_mfma_f32_16x16x32_bf16 v[42:45], v[160:163], v[192:195], v[42:45]
	v_mfma_f32_16x16x32_bf16 v[30:33], v[146:149], v[200:203], v[30:33]
	v_mfma_f32_16x16x32_bf16 v[26:29], v[160:163], v[200:203], v[26:29]
	v_mfma_f32_16x16x32_bf16 v[14:17], v[146:149], v[208:211], v[14:17]
	v_mfma_f32_16x16x32_bf16 v[10:13], v[160:163], v[208:211], v[10:13]
	v_mfma_f32_16x16x32_bf16 v[62:65], v[156:159], v[188:191], v[62:65]
	v_mfma_f32_16x16x32_bf16 v[58:61], v[164:167], v[188:191], v[58:61]
	v_mfma_f32_16x16x32_bf16 v[46:49], v[156:159], v[196:199], v[46:49]
	v_mfma_f32_16x16x32_bf16 v[42:45], v[164:167], v[196:199], v[42:45]
	v_mfma_f32_16x16x32_bf16 v[30:33], v[156:159], v[204:207], v[30:33]
	v_mfma_f32_16x16x32_bf16 v[26:29], v[164:167], v[204:207], v[26:29]
	v_mfma_f32_16x16x32_bf16 v[14:17], v[156:159], v[212:215], v[14:17]
	v_mfma_f32_16x16x32_bf16 v[10:13], v[164:167], v[212:215], v[10:13]
	v_mfma_f32_16x16x32_bf16 v[54:57], v[168:171], v[184:187], v[54:57]
	v_mfma_f32_16x16x32_bf16 v[50:53], v[176:179], v[184:187], v[50:53]
	v_mfma_f32_16x16x32_bf16 v[38:41], v[168:171], v[192:195], v[38:41]
	v_mfma_f32_16x16x32_bf16 v[34:37], v[176:179], v[192:195], v[34:37]
	v_mfma_f32_16x16x32_bf16 v[22:25], v[168:171], v[200:203], v[22:25]
	v_mfma_f32_16x16x32_bf16 v[18:21], v[176:179], v[200:203], v[18:21]
	v_mfma_f32_16x16x32_bf16 v[6:9], v[168:171], v[208:211], v[6:9]
	v_mfma_f32_16x16x32_bf16 v[2:5], v[176:179], v[208:211], v[2:5]
	v_mfma_f32_16x16x32_bf16 v[54:57], v[172:175], v[188:191], v[54:57]
	v_mfma_f32_16x16x32_bf16 v[50:53], v[180:183], v[188:191], v[50:53]
	v_mfma_f32_16x16x32_bf16 v[38:41], v[172:175], v[196:199], v[38:41]
	v_mfma_f32_16x16x32_bf16 v[34:37], v[180:183], v[196:199], v[34:37]
	v_mfma_f32_16x16x32_bf16 v[22:25], v[172:175], v[204:207], v[22:25]
	v_mfma_f32_16x16x32_bf16 v[18:21], v[180:183], v[204:207], v[18:21]
	v_mfma_f32_16x16x32_bf16 v[6:9], v[172:175], v[212:215], v[6:9]
	v_mfma_f32_16x16x32_bf16 v[2:5], v[180:183], v[212:215], v[2:5]
	s_barrier
	s_add_i32 s52, s52, 2
	s_add_u32 s50, s50, 0x100
	s_addc_u32 s51, s51, 0
	s_cmp_gt_u32 s52, 41
	s_mov_b64 s[2:3], s[22:23]
	s_cbranch_scc0 .LBB0_1867
	s_and_b64 vcc, exec, s[14:15]
	s_cbranch_vccz .LBB0_1870
	s_barrier

; __global__ void __launch_bounds__(512, 2) fwd(Params p) {
;     extern __shared__ __attribute__((aligned(16))) unsigned char lds_raw[];
	.amdhsa_kernel _Z3fwd6Params
		.amdhsa_group_segment_fixed_size 0
		.amdhsa_private_segment_fixed_size 0
		.amdhsa_kernarg_size 576
		.amdhsa_user_sgpr_count 2
		.amdhsa_user_sgpr_dispatch_ptr 0
		.amdhsa_user_sgpr_queue_ptr 0
		.amdhsa_user_sgpr_kernarg_segment_ptr 1
		.amdhsa_user_sgpr_dispatch_id 0
		.amdhsa_user_sgpr_kernarg_preload_length 0
		.amdhsa_user_sgpr_kernarg_preload_offset 0
		.amdhsa_user_sgpr_private_segment_size 0
		.amdhsa_uses_dynamic_stack 0
		.amdhsa_enable_private_segment 0
		.amdhsa_system_sgpr_workgroup_id_x 1
		.amdhsa_system_sgpr_workgroup_id_y 0
		.amdhsa_system_sgpr_workgroup_id_z 0
		.amdhsa_system_sgpr_workgroup_info 0
		.amdhsa_system_vgpr_workitem_id 0
		.amdhsa_next_free_vgpr 256
		.amdhsa_next_free_sgpr 100
		.amdhsa_accum_offset 256
		.amdhsa_reserve_vcc 1
		.amdhsa_float_round_mode_32 0
		.amdhsa_float_round_mode_16_64 0
		.amdhsa_float_denorm_mode_32 3
		.amdhsa_float_denorm_mode_16_64 3
		.amdhsa_dx10_clamp 1
		.amdhsa_ieee_mode 1
		.amdhsa_fp16_overflow 0
		.amdhsa_tg_split 0
		.amdhsa_exception_fp_ieee_invalid_op 0
		.amdhsa_exception_fp_denorm_src 0
		.amdhsa_exception_fp_ieee_div_zero 0
		.amdhsa_exception_fp_ieee_overflow 0
		.amdhsa_exception_fp_ieee_underflow 0
		.amdhsa_exception_fp_ieee_inexact 0
		.amdhsa_exception_int_div_zero 0
	.end_amdhsa_kernel

; __global__ void __launch_bounds__(512, 2) fwd(Params p) {
;     extern __shared__ __attribute__((aligned(16))) unsigned char lds_raw[];
amdhsa.kernels:
  - .agpr_count:     0
    .args:
      - .offset:         0
        .size:           320
        .value_kind:     by_value
      - .offset:         320
        .size:           4
        .value_kind:     hidden_block_count_x
      - .offset:         324
        .size:           4
        .value_kind:     hidden_block_count_y
      - .offset:         328
        .size:           4
        .value_kind:     hidden_block_count_z
      - .offset:         332
        .size:           2
        .value_kind:     hidden_group_size_x
      - .offset:         334
        .size:           2
        .value_kind:     hidden_group_size_y
      - .offset:         336
        .size:           2
        .value_kind:     hidden_group_size_z
      - .offset:         338
        .size:           2
        .value_kind:     hidden_remainder_x
      - .offset:         340
        .size:           2
        .value_kind:     hidden_remainder_y
      - .offset:         342
        .size:           2
        .value_kind:     hidden_remainder_z
      - .offset:         360
        .size:           8
        .value_kind:     hidden_global_offset_x
      - .offset:         368
        .size:           8
        .value_kind:     hidden_global_offset_y
      - .offset:         376
        .size:           8
        .value_kind:     hidden_global_offset_z
      - .offset:         384
        .size:           2
        .value_kind:     hidden_grid_dims
      - .offset:         440
        .size:           4
        .value_kind:     hidden_dynamic_lds_size
    .group_segment_fixed_size: 0
    .kernarg_segment_align: 8
    .kernarg_segment_size: 576
    .language:       OpenCL C
    .language_version:
      - 2
      - 0
    .max_flat_workgroup_size: 512
    .name:           _Z3fwd6Params
    .private_segment_fixed_size: 0
    .sgpr_count:     106
    .sgpr_spill_count: 133
    .symbol:         _Z3fwd6Params.kd
    .uniform_work_group_size: 1
    .uses_dynamic_stack: false
    .vgpr_count:     256
    .vgpr_spill_count: 0
    .wavefront_size: 64
